# combination: DPP/permlane wave sums in LayerNorms, scalar address math for C2 LDS-DMA, pipelined glu staging loads in E2 (on top of the previous version)
# speedup vs baseline: 1.0166x; 1.0047x over previous
; #define LAS __attribute__((address_space(3)))
; __device__ __forceinline__ unsigned pk2(float lo, float hi) { unsigned r; asm("v_cvt_pk_bf16_f32 %0, %1, %2" : "=v"(r) : "v"(lo), "v"(hi)); return r; }
; __device__ __forceinline__ float sigmoidf_(float x) { return __builtin_amdgcn_rcpf(1.0f + __builtin_amdgcn_exp2f(x * -1.44269504089f)); }
; __device__ __forceinline__ void phase_even_mix(CArgs a, LAS unsigned char* lds, int i2, int wv, int xw  ) {
;     ...
;         for (int it = 0; it < 6; ++it) { const int item = it * NTHR + tid, tt = item >> 6, cg = item & 63, p = t0 - 16 + tt;
;             u32x4 o = (u32x4){0u, 0u, 0u, 0u};
;             if (p >= 0) o = *(const u32x4*)(HB + ((size_t)b * SEQ + p) * EVEN_IN + cg * 8);
;             *(LAS u32x4*)(glu + tt * 512 + cg * 8) = o; }
;         {
;             const float* lg = a->in[I_CLNG] + i2 * 512 + lane * 8; const float* lb = a->in[I_CLNB] + i2 * 512 + lane * 8;
;             const f32x4 g0 = *(const f32x4*)lg, g1 = *(const f32x4*)(lg + 4), b0 = *(const f32x4*)lb, b1 = *(const f32x4*)(lb + 4);
; #pragma unroll
;             for (int tt = 0; tt < 4; ++tt) { const int t = wave * 4 + tt;
;                 f32x4 v0 = *(const LAS f32x4*)(ybuf + t * 512 + lane * 8), v1 = *(const LAS f32x4*)(ybuf + t * 512 + lane * 8 + 4);
;                 const float mean = wave_sum((v0.x + v0.y) + (v0.z + v0.w) + (v1.x + v1.y) + (v1.z + v1.w), lane) * (1.f / 512.f);
;                 v0 = v0 - mean; v1 = v1 - mean;
;                 const float var = wave_sum((v0.x * v0.x + v0.y * v0.y) + (v0.z * v0.z + v0.w * v0.w) + (v1.x * v1.x + v1.y * v1.y) + (v1.z * v1.z + v1.w * v1.w), lane) * (1.f / 512.f);
;                 const float rstd = 1.0f / sqrtf(var + LN_EPS);
;                 float o[8];
; #pragma unroll
;                 for (int j = 0; j < 4; ++j) { const float x0 = v0[j] * rstd * g0[j] + b0[j], x1 = v1[j] * rstd * g1[j] + b1[j]; o[j] = x0 * sigmoidf_(x0); o[4 + j] = x1 * sigmoidf_(x1); }
;                 u32x4 wv4; wv4.x = pk2(o[0], o[1]); wv4.y = pk2(o[2], o[3]); wv4.z = pk2(o[4], o[5]); wv4.w = pk2(o[6], o[7]);
;                 *(u32x4*)(YB + (tokbase + t) * DM + 512 + lane * 8) = wv4; }
.LBB0_460:
	s_or_b64 exec, exec, s[16:17]
	s_xor_b64 s[68:69], s[12:13], -1
	v_readlane_b32 s12, v254, 29
	s_waitcnt vmcnt(0)
	ds_write_b128 v151, v[0:3]
	s_or_b32 s12, s18, s12
	s_load_dwordx4 s[16:19], s[88:89], 0x20
	s_load_dwordx4 s[64:67], s[88:89], 0x40
	s_ashr_i32 s13, s12, 31
	s_lshl_b64 s[22:23], s[12:13], 5
	s_waitcnt lgkmcnt(0)
	s_add_u32 s12, s64, s86
	s_addc_u32 s13, s65, s87
	s_add_u32 s64, s66, s86
	s_addc_u32 s65, s67, s87
	global_load_dwordx4 v[8:11], v143, s[12:13] offset:16
	global_load_dwordx4 v[12:15], v143, s[12:13]
	global_load_dwordx4 v[0:3], v143, s[64:65] offset:16
	global_load_dwordx4 v[4:7], v143, s[64:65]
	v_readlane_b32 s12, v255, 3
	s_mov_b32 s64, 32
	s_nop 0
	v_add_u32_e32 v20, s12, v62
	ds_read_b128 v[16:19], v20
	ds_read_b128 v[20:23], v20 offset:16
	s_waitcnt lgkmcnt(1)
	v_mov_b32_e32 v154, v17
	v_mov_b32_e32 v155, v18
	v_mov_b32_e32 v156, v16
	v_mov_b32_e32 v157, v19
	v_pk_add_f32 v[154:155], v[154:155], v[156:157]
	s_waitcnt lgkmcnt(0)
	v_mov_b32_e32 v156, v22
	v_mov_b32_e32 v157, v20
	v_mov_b32_e32 v158, v23
	v_mov_b32_e32 v159, v21
	v_pk_add_f32 v[156:157], v[156:157], v[158:159]
	v_add_f32_e32 v152, v154, v155
	v_add_f32_e32 v152, v152, v157
	v_add_f32_e32 v152, v156, v152
	s_waitcnt lgkmcnt(0)
	s_nop 1
	v_add_f32_dpp v152, v152, v152 quad_perm:[1,0,3,2] row_mask:0xf bank_mask:0xf
	s_nop 1
	v_add_f32_dpp v152, v152, v152 quad_perm:[2,3,0,1] row_mask:0xf bank_mask:0xf
	s_nop 1
	v_add_f32_dpp v152, v152, v152 row_half_mirror row_mask:0xf bank_mask:0xf
	s_nop 1
	v_add_f32_dpp v152, v152, v152 row_mirror row_mask:0xf bank_mask:0xf
	v_mov_b32_e32 v154, v152
	s_nop 1
	v_permlane16_swap_b32_e32 v154, v152
	v_add_f32_e32 v152, v152, v154
	v_mov_b32_e32 v154, v152
	s_nop 1
	v_permlane32_swap_b32_e32 v154, v152
	v_add_f32_e32 v152, v152, v154
	v_fmamk_f32 v19, v152, 0xbb000000, v19
	v_fmac_f32_e32 v17, 0xbb000000, v152
	v_fmamk_f32 v18, v152, 0xbb000000, v18
	v_fmamk_f32 v16, v152, 0xbb000000, v16
	v_fmamk_f32 v22, v152, 0xbb000000, v22
	v_fmamk_f32 v23, v152, 0xbb000000, v23
	v_fmamk_f32 v20, v152, 0xbb000000, v20
	v_fmac_f32_e32 v21, 0xbb000000, v152
	v_mul_f32_e32 v152, v17, v17
	v_mul_f32_e32 v154, v19, v19
	v_fmac_f32_e32 v152, v16, v16
	v_fmac_f32_e32 v154, v18, v18
	v_add_f32_e32 v152, v152, v154
	v_mul_f32_e32 v154, v21, v21
	v_fmac_f32_e32 v154, v20, v20
	v_add_f32_e32 v152, v154, v152
	v_mul_f32_e32 v154, v23, v23
	v_fmac_f32_e32 v154, v22, v22
	v_add_f32_e32 v152, v154, v152
	s_waitcnt lgkmcnt(0)
	s_nop 1
	v_add_f32_dpp v152, v152, v152 quad_perm:[1,0,3,2] row_mask:0xf bank_mask:0xf
	s_nop 1
	v_add_f32_dpp v152, v152, v152 quad_perm:[2,3,0,1] row_mask:0xf bank_mask:0xf
	s_nop 1
	v_add_f32_dpp v152, v152, v152 row_half_mirror row_mask:0xf bank_mask:0xf
	s_nop 1
	v_add_f32_dpp v152, v152, v152 row_mirror row_mask:0xf bank_mask:0xf
	v_mov_b32_e32 v154, v152
	s_nop 1
	v_permlane16_swap_b32_e32 v154, v152
	v_add_f32_e32 v152, v152, v154
	v_mov_b32_e32 v154, v152
	s_nop 1
	v_permlane32_swap_b32_e32 v154, v152
	v_add_f32_e32 v152, v152, v154
	v_fmamk_f32 v152, v152, 0x3b000000, v185
	v_cmp_gt_f32_e32 vcc, s55, v152
	v_mul_f32_e32 v154, 0x4f800000, v152
	s_nop 0
	v_cndmask_b32_e32 v152, v152, v154, vcc
	v_sqrt_f32_e32 v154, v152
	s_nop 0
	v_add_u32_e32 v155, -1, v154
	v_fma_f32 v156, -v155, v154, v152
	v_cmp_ge_f32_e64 s[12:13], 0, v156
	v_add_u32_e32 v156, 1, v154
	s_nop 0
	v_cndmask_b32_e64 v155, v154, v155, s[12:13]
	v_fma_f32 v154, -v156, v154, v152
	v_cmp_lt_f32_e64 s[12:13], 0, v154
	s_nop 1
	v_cndmask_b32_e64 v154, v155, v156, s[12:13]
	v_mul_f32_e32 v155, 0x37800000, v154
	v_cndmask_b32_e32 v154, v154, v155, vcc
	v_cmp_class_f32_e32 vcc, v152, v183
	s_nop 1
	v_cndmask_b32_e32 v152, v154, v152, vcc
	v_div_scale_f32 v154, s[12:13], v152, v152, 1.0
	v_rcp_f32_e32 v155, v154
	s_add_u32 s12, s22, s79
	v_readlane_b32 s13, v255, 4
	s_addc_u32 s13, s23, s13
	v_fma_f32 v156, -v154, v155, 1.0
	v_fmac_f32_e32 v155, v156, v155
	v_div_scale_f32 v156, vcc, 1.0, v152, 1.0
	v_mul_f32_e32 v157, v156, v155
	v_fma_f32 v158, -v154, v157, v156
	v_fmac_f32_e32 v157, v158, v155
	v_fma_f32 v154, -v154, v157, v156
	v_div_fmas_f32 v154, v154, v155, v157
	v_div_fixup_f32 v152, v154, v152, 1.0
	v_mul_f32_e32 v16, v16, v152
	s_waitcnt vmcnt(0)
	v_fma_f32 v16, v12, v16, v4
	v_mul_f32_e32 v154, 0xbfb8aa3b, v16
	v_exp_f32_e32 v154, v154
	v_mul_f32_e32 v20, v20, v152
	v_fma_f32 v20, v8, v20, v0
	v_mul_f32_e32 v17, v17, v152
	v_add_f32_e32 v154, 1.0, v154
	v_rcp_f32_e32 v154, v154
	v_fma_f32 v17, v13, v17, v5
	v_mul_f32_e32 v21, v21, v152
	v_fma_f32 v21, v9, v21, v1
	v_mul_f32_e32 v16, v16, v154
	v_mul_f32_e32 v154, 0xbfb8aa3b, v20
	v_exp_f32_e32 v154, v154
	v_mul_f32_e32 v18, v18, v152
	v_mul_f32_e32 v19, v19, v152
	v_fma_f32 v18, v14, v18, v6
	v_add_f32_e32 v154, 1.0, v154
	v_rcp_f32_e32 v154, v154
	v_fma_f32 v19, v15, v19, v7
	v_mul_f32_e32 v22, v22, v152
	v_mul_f32_e32 v23, v23, v152
	v_mul_f32_e32 v20, v20, v154
	v_mul_f32_e32 v154, 0xbfb8aa3b, v17
	v_exp_f32_e32 v154, v154
	v_mul_f32_e32 v152, 0xbfb8aa3b, v19
	v_exp_f32_e32 v152, v152
	v_fma_f32 v22, v10, v22, v2
	v_add_f32_e32 v154, 1.0, v154
	v_rcp_f32_e32 v154, v154
	v_add_f32_e32 v152, 1.0, v152
	v_rcp_f32_e32 v152, v152
	v_fma_f32 v23, v11, v23, v3
	v_mul_f32_e32 v17, v17, v154
	v_mul_f32_e32 v154, 0xbfb8aa3b, v21
	v_exp_f32_e32 v154, v154
	v_mul_f32_e32 v19, v19, v152
	v_mul_f32_e32 v152, 0xbfb8aa3b, v23
	v_exp_f32_e32 v152, v152
	v_add_f32_e32 v154, 1.0, v154
	v_rcp_f32_e32 v154, v154
	s_lshl_b64 s[12:13], s[12:13], 11
	v_add_f32_e32 v152, 1.0, v152
	v_rcp_f32_e32 v152, v152
	v_mul_f32_e32 v21, v21, v154
	v_mul_f32_e32 v154, 0xbfb8aa3b, v18
	v_exp_f32_e32 v154, v154
	v_cvt_pk_bf16_f32 v16, v16, v17
	v_mul_f32_e32 v23, v23, v152
	v_add_f32_e32 v154, 1.0, v154
	v_rcp_f32_e32 v154, v154
	s_nop 0
	v_mul_f32_e32 v18, v18, v154
	v_mul_f32_e32 v154, 0xbfb8aa3b, v22
	v_exp_f32_e32 v154, v154
	v_cvt_pk_bf16_f32 v17, v18, v19
	v_cvt_pk_bf16_f32 v18, v20, v21
	v_lshl_add_u64 v[20:21], v[32:33], 0, s[12:13]
	v_add_f32_e32 v154, 1.0, v154
	v_rcp_f32_e32 v154, v154
	v_readlane_b32 s12, v255, 5
	v_mul_f32_e32 v22, v22, v154
	v_cvt_pk_bf16_f32 v19, v22, v23
	global_store_dwordx4 v[20:21], v[16:19], off offset:1024
	v_add_u32_e32 v20, s12, v62
	ds_read_b128 v[16:19], v20
	ds_read_b128 v[20:23], v20 offset:16
	s_waitcnt lgkmcnt(1)
; #define LAS __attribute__((address_space(3)))
; __device__ __forceinline__ unsigned pk2(float lo, float hi) { unsigned r; asm("v_cvt_pk_bf16_f32 %0, %1, %2" : "=v"(r) : "v"(lo), "v"(hi)); return r; }
; __device__ __forceinline__ float sigmoidf_(float x) { return __builtin_amdgcn_rcpf(1.0f + __builtin_amdgcn_exp2f(x * -1.44269504089f)); }
; __device__ __forceinline__ void phase_even_mix(CArgs a, LAS unsigned char* lds, int i2, int wv, int xw  ) {
;     ...
;             for (int tt = 0; tt < 4; ++tt) { const int t = wave * 4 + tt;
;                 f32x4 v0 = *(const LAS f32x4*)(ybuf + t * 512 + lane * 8), v1 = *(const LAS f32x4*)(ybuf + t * 512 + lane * 8 + 4);
;                 const float mean = wave_sum((v0.x + v0.y) + (v0.z + v0.w) + (v1.x + v1.y) + (v1.z + v1.w), lane) * (1.f / 512.f);
;                 v0 = v0 - mean; v1 = v1 - mean;
;                 const float var = wave_sum((v0.x * v0.x + v0.y * v0.y) + (v0.z * v0.z + v0.w * v0.w) + (v1.x * v1.x + v1.y * v1.y) + (v1.z * v1.z + v1.w * v1.w), lane) * (1.f / 512.f);
;                 const float rstd = 1.0f / sqrtf(var + LN_EPS);
;                 float o[8];
; #pragma unroll
;                 for (int j = 0; j < 4; ++j) { const float x0 = v0[j] * rstd * g0[j] + b0[j], x1 = v1[j] * rstd * g1[j] + b1[j]; o[j] = x0 * sigmoidf_(x0); o[4 + j] = x1 * sigmoidf_(x1); }
;                 u32x4 wv4; wv4.x = pk2(o[0], o[1]); wv4.y = pk2(o[2], o[3]); wv4.z = pk2(o[4], o[5]); wv4.w = pk2(o[6], o[7]);
;                 *(u32x4*)(YB + (tokbase + t) * DM + 512 + lane * 8) = wv4; }
	v_mov_b32_e32 v154, v17
	v_mov_b32_e32 v155, v18
	v_mov_b32_e32 v156, v16
	v_mov_b32_e32 v157, v19
	v_pk_add_f32 v[154:155], v[154:155], v[156:157]
	s_waitcnt lgkmcnt(0)
	v_mov_b32_e32 v156, v22
	v_mov_b32_e32 v157, v20
	v_mov_b32_e32 v158, v23
	v_mov_b32_e32 v159, v21
	v_pk_add_f32 v[156:157], v[156:157], v[158:159]
	v_add_f32_e32 v152, v154, v155
	v_add_f32_e32 v152, v152, v157
	v_add_f32_e32 v152, v156, v152
	s_waitcnt lgkmcnt(0)
	s_nop 1
	v_add_f32_dpp v152, v152, v152 quad_perm:[1,0,3,2] row_mask:0xf bank_mask:0xf
	s_nop 1
	v_add_f32_dpp v152, v152, v152 quad_perm:[2,3,0,1] row_mask:0xf bank_mask:0xf
	s_nop 1
	v_add_f32_dpp v152, v152, v152 row_half_mirror row_mask:0xf bank_mask:0xf
	s_nop 1
	v_add_f32_dpp v152, v152, v152 row_mirror row_mask:0xf bank_mask:0xf
	v_mov_b32_e32 v154, v152
	s_nop 1
	v_permlane16_swap_b32_e32 v154, v152
	v_add_f32_e32 v152, v152, v154
	v_mov_b32_e32 v154, v152
	s_nop 1
	v_permlane32_swap_b32_e32 v154, v152
	v_add_f32_e32 v152, v152, v154
	v_fmamk_f32 v19, v152, 0xbb000000, v19
	v_fmac_f32_e32 v17, 0xbb000000, v152
	v_fmamk_f32 v18, v152, 0xbb000000, v18
	v_fmamk_f32 v16, v152, 0xbb000000, v16
	v_fmamk_f32 v22, v152, 0xbb000000, v22
	v_fmamk_f32 v23, v152, 0xbb000000, v23
	v_fmamk_f32 v20, v152, 0xbb000000, v20
	v_fmac_f32_e32 v21, 0xbb000000, v152
	v_mul_f32_e32 v152, v17, v17
	v_mul_f32_e32 v154, v19, v19
	v_fmac_f32_e32 v152, v16, v16
	v_fmac_f32_e32 v154, v18, v18
	v_add_f32_e32 v152, v152, v154
	v_mul_f32_e32 v154, v21, v21
	v_fmac_f32_e32 v154, v20, v20
	v_add_f32_e32 v152, v154, v152
	v_mul_f32_e32 v154, v23, v23
	v_fmac_f32_e32 v154, v22, v22
	v_add_f32_e32 v152, v154, v152
	s_waitcnt lgkmcnt(0)
	s_nop 1
	v_add_f32_dpp v152, v152, v152 quad_perm:[1,0,3,2] row_mask:0xf bank_mask:0xf
	s_nop 1
	v_add_f32_dpp v152, v152, v152 quad_perm:[2,3,0,1] row_mask:0xf bank_mask:0xf
	s_nop 1
	v_add_f32_dpp v152, v152, v152 row_half_mirror row_mask:0xf bank_mask:0xf
	s_nop 1
	v_add_f32_dpp v152, v152, v152 row_mirror row_mask:0xf bank_mask:0xf
	v_mov_b32_e32 v154, v152
	s_nop 1
	v_permlane16_swap_b32_e32 v154, v152
	v_add_f32_e32 v152, v152, v154
	v_mov_b32_e32 v154, v152
	s_nop 1
	v_permlane32_swap_b32_e32 v154, v152
	v_add_f32_e32 v152, v152, v154
	v_fmamk_f32 v152, v152, 0x3b000000, v185
	v_cmp_gt_f32_e32 vcc, s55, v152
	v_mul_f32_e32 v154, 0x4f800000, v152
	s_nop 0
	v_cndmask_b32_e32 v152, v152, v154, vcc
	v_sqrt_f32_e32 v154, v152
	s_nop 0
	v_add_u32_e32 v155, -1, v154
	v_fma_f32 v156, -v155, v154, v152
	v_cmp_ge_f32_e64 s[12:13], 0, v156
	v_add_u32_e32 v156, 1, v154
	s_nop 0
	v_cndmask_b32_e64 v155, v154, v155, s[12:13]
	v_fma_f32 v154, -v156, v154, v152
	v_cmp_lt_f32_e64 s[12:13], 0, v154
	s_nop 1
	v_cndmask_b32_e64 v154, v155, v156, s[12:13]
	v_mul_f32_e32 v155, 0x37800000, v154
	v_cndmask_b32_e32 v154, v154, v155, vcc
	v_cmp_class_f32_e32 vcc, v152, v183
	s_nop 1
	v_cndmask_b32_e32 v152, v154, v152, vcc
	v_div_scale_f32 v154, s[12:13], v152, v152, 1.0
	v_rcp_f32_e32 v155, v154
	s_add_u32 s12, s22, s33
	v_readlane_b32 s13, v255, 6
	s_addc_u32 s13, s23, s13
	v_fma_f32 v156, -v154, v155, 1.0
	v_fmac_f32_e32 v155, v156, v155
	v_div_scale_f32 v156, vcc, 1.0, v152, 1.0
	v_mul_f32_e32 v157, v156, v155
	v_fma_f32 v158, -v154, v157, v156
	v_fmac_f32_e32 v157, v158, v155
	v_fma_f32 v154, -v154, v157, v156
	v_div_fmas_f32 v154, v154, v155, v157
	v_div_fixup_f32 v152, v154, v152, 1.0
	v_mul_f32_e32 v16, v16, v152
	v_fma_f32 v16, v12, v16, v4
	v_mul_f32_e32 v154, 0xbfb8aa3b, v16
	v_exp_f32_e32 v154, v154
	v_mul_f32_e32 v20, v20, v152
	v_fma_f32 v20, v8, v20, v0
	v_mul_f32_e32 v17, v17, v152
	v_add_f32_e32 v154, 1.0, v154
	v_rcp_f32_e32 v154, v154
	v_fma_f32 v17, v13, v17, v5
	v_mul_f32_e32 v21, v21, v152
	v_fma_f32 v21, v9, v21, v1
	v_mul_f32_e32 v16, v16, v154
	v_mul_f32_e32 v154, 0xbfb8aa3b, v20
	v_exp_f32_e32 v154, v154
	v_mul_f32_e32 v18, v18, v152
	v_mul_f32_e32 v19, v19, v152
	v_fma_f32 v18, v14, v18, v6
	v_add_f32_e32 v154, 1.0, v154
	v_rcp_f32_e32 v154, v154
	v_fma_f32 v19, v15, v19, v7
	v_mul_f32_e32 v22, v22, v152
	v_mul_f32_e32 v23, v23, v152
	v_mul_f32_e32 v20, v20, v154
	v_mul_f32_e32 v154, 0xbfb8aa3b, v17
	v_exp_f32_e32 v154, v154
	v_mul_f32_e32 v152, 0xbfb8aa3b, v19
	v_exp_f32_e32 v152, v152
	v_fma_f32 v22, v10, v22, v2
	v_add_f32_e32 v154, 1.0, v154
	v_rcp_f32_e32 v154, v154
	v_add_f32_e32 v152, 1.0, v152
	v_rcp_f32_e32 v152, v152
	v_fma_f32 v23, v11, v23, v3
	v_mul_f32_e32 v17, v17, v154
	v_mul_f32_e32 v154, 0xbfb8aa3b, v21
	v_exp_f32_e32 v154, v154
	v_mul_f32_e32 v19, v19, v152
	v_mul_f32_e32 v152, 0xbfb8aa3b, v23
	v_exp_f32_e32 v152, v152
	v_add_f32_e32 v154, 1.0, v154
	v_rcp_f32_e32 v154, v154
	s_lshl_b64 s[12:13], s[12:13], 11
	v_add_f32_e32 v152, 1.0, v152
	v_rcp_f32_e32 v152, v152
	v_mul_f32_e32 v21, v21, v154
	v_mul_f32_e32 v154, 0xbfb8aa3b, v18
	v_exp_f32_e32 v154, v154
	v_cvt_pk_bf16_f32 v16, v16, v17
	v_mul_f32_e32 v23, v23, v152
	v_add_f32_e32 v154, 1.0, v154
	v_rcp_f32_e32 v154, v154
	s_nop 0
	v_mul_f32_e32 v18, v18, v154
	v_mul_f32_e32 v154, 0xbfb8aa3b, v22
	v_exp_f32_e32 v154, v154
	v_cvt_pk_bf16_f32 v17, v18, v19
	v_cvt_pk_bf16_f32 v18, v20, v21
	v_lshl_add_u64 v[20:21], v[32:33], 0, s[12:13]
	v_add_f32_e32 v154, 1.0, v154
	v_rcp_f32_e32 v154, v154
	v_readlane_b32 s12, v255, 7
	v_mul_f32_e32 v22, v22, v154
	v_cvt_pk_bf16_f32 v19, v22, v23
	global_store_dwordx4 v[20:21], v[16:19], off offset:1024
	v_add_u32_e32 v20, s12, v62
	ds_read_b128 v[16:19], v20
	ds_read_b128 v[20:23], v20 offset:16
	s_waitcnt lgkmcnt(1)
	v_mov_b32_e32 v154, v17
	v_mov_b32_e32 v155, v18
	v_mov_b32_e32 v156, v16
	v_mov_b32_e32 v157, v19
	v_pk_add_f32 v[154:155], v[154:155], v[156:157]
	s_waitcnt lgkmcnt(0)
; #define LAS __attribute__((address_space(3)))
; __device__ __forceinline__ unsigned pk2(float lo, float hi) { unsigned r; asm("v_cvt_pk_bf16_f32 %0, %1, %2" : "=v"(r) : "v"(lo), "v"(hi)); return r; }
; __device__ __forceinline__ float sigmoidf_(float x) { return __builtin_amdgcn_rcpf(1.0f + __builtin_amdgcn_exp2f(x * -1.44269504089f)); }
; __device__ __forceinline__ void phase_even_mix(CArgs a, LAS unsigned char* lds, int i2, int wv, int xw  ) {
;     ...
;             for (int tt = 0; tt < 4; ++tt) { const int t = wave * 4 + tt;
;                 f32x4 v0 = *(const LAS f32x4*)(ybuf + t * 512 + lane * 8), v1 = *(const LAS f32x4*)(ybuf + t * 512 + lane * 8 + 4);
;                 const float mean = wave_sum((v0.x + v0.y) + (v0.z + v0.w) + (v1.x + v1.y) + (v1.z + v1.w), lane) * (1.f / 512.f);
;                 v0 = v0 - mean; v1 = v1 - mean;
;                 const float var = wave_sum((v0.x * v0.x + v0.y * v0.y) + (v0.z * v0.z + v0.w * v0.w) + (v1.x * v1.x + v1.y * v1.y) + (v1.z * v1.z + v1.w * v1.w), lane) * (1.f / 512.f);
;                 const float rstd = 1.0f / sqrtf(var + LN_EPS);
;                 float o[8];
; #pragma unroll
;                 for (int j = 0; j < 4; ++j) { const float x0 = v0[j] * rstd * g0[j] + b0[j], x1 = v1[j] * rstd * g1[j] + b1[j]; o[j] = x0 * sigmoidf_(x0); o[4 + j] = x1 * sigmoidf_(x1); }
;                 u32x4 wv4; wv4.x = pk2(o[0], o[1]); wv4.y = pk2(o[2], o[3]); wv4.z = pk2(o[4], o[5]); wv4.w = pk2(o[6], o[7]);
;                 *(u32x4*)(YB + (tokbase + t) * DM + 512 + lane * 8) = wv4; }
	v_mov_b32_e32 v156, v22
	v_mov_b32_e32 v157, v20
	v_mov_b32_e32 v158, v23
	v_mov_b32_e32 v159, v21
	v_pk_add_f32 v[156:157], v[156:157], v[158:159]
	v_add_f32_e32 v152, v154, v155
	v_add_f32_e32 v152, v152, v157
	v_add_f32_e32 v152, v156, v152
	s_waitcnt lgkmcnt(0)
	s_nop 1
	v_add_f32_dpp v152, v152, v152 quad_perm:[1,0,3,2] row_mask:0xf bank_mask:0xf
	s_nop 1
	v_add_f32_dpp v152, v152, v152 quad_perm:[2,3,0,1] row_mask:0xf bank_mask:0xf
	s_nop 1
	v_add_f32_dpp v152, v152, v152 row_half_mirror row_mask:0xf bank_mask:0xf
	s_nop 1
	v_add_f32_dpp v152, v152, v152 row_mirror row_mask:0xf bank_mask:0xf
	v_mov_b32_e32 v154, v152
	s_nop 1
	v_permlane16_swap_b32_e32 v154, v152
	v_add_f32_e32 v152, v152, v154
	v_mov_b32_e32 v154, v152
	s_nop 1
	v_permlane32_swap_b32_e32 v154, v152
	v_add_f32_e32 v152, v152, v154
	v_fmamk_f32 v19, v152, 0xbb000000, v19
	v_fmac_f32_e32 v17, 0xbb000000, v152
	v_fmamk_f32 v18, v152, 0xbb000000, v18
	v_fmamk_f32 v16, v152, 0xbb000000, v16
	v_fmamk_f32 v22, v152, 0xbb000000, v22
	v_fmamk_f32 v23, v152, 0xbb000000, v23
	v_fmamk_f32 v20, v152, 0xbb000000, v20
	v_fmac_f32_e32 v21, 0xbb000000, v152
	v_mul_f32_e32 v152, v17, v17
	v_mul_f32_e32 v154, v19, v19
	v_fmac_f32_e32 v152, v16, v16
	v_fmac_f32_e32 v154, v18, v18
	v_add_f32_e32 v152, v152, v154
	v_mul_f32_e32 v154, v21, v21
	v_fmac_f32_e32 v154, v20, v20
	v_add_f32_e32 v152, v154, v152
	v_mul_f32_e32 v154, v23, v23
	v_fmac_f32_e32 v154, v22, v22
	v_add_f32_e32 v152, v154, v152
	s_waitcnt lgkmcnt(0)
	s_nop 1
	v_add_f32_dpp v152, v152, v152 quad_perm:[1,0,3,2] row_mask:0xf bank_mask:0xf
	s_nop 1
	v_add_f32_dpp v152, v152, v152 quad_perm:[2,3,0,1] row_mask:0xf bank_mask:0xf
	s_nop 1
	v_add_f32_dpp v152, v152, v152 row_half_mirror row_mask:0xf bank_mask:0xf
	s_nop 1
	v_add_f32_dpp v152, v152, v152 row_mirror row_mask:0xf bank_mask:0xf
	v_mov_b32_e32 v154, v152
	s_nop 1
	v_permlane16_swap_b32_e32 v154, v152
	v_add_f32_e32 v152, v152, v154
	v_mov_b32_e32 v154, v152
	s_nop 1
	v_permlane32_swap_b32_e32 v154, v152
	v_add_f32_e32 v152, v152, v154
	v_fmamk_f32 v152, v152, 0x3b000000, v185
	v_cmp_gt_f32_e32 vcc, s55, v152
	v_mul_f32_e32 v154, 0x4f800000, v152
	s_nop 0
	v_cndmask_b32_e32 v152, v152, v154, vcc
	v_sqrt_f32_e32 v154, v152
	s_nop 0
	v_add_u32_e32 v155, -1, v154
	v_fma_f32 v156, -v155, v154, v152
	v_cmp_ge_f32_e64 s[12:13], 0, v156
	v_add_u32_e32 v156, 1, v154
	s_nop 0
	v_cndmask_b32_e64 v155, v154, v155, s[12:13]
	v_fma_f32 v154, -v156, v154, v152
	v_cmp_lt_f32_e64 s[12:13], 0, v154
	s_nop 1
	v_cndmask_b32_e64 v154, v155, v156, s[12:13]
	v_mul_f32_e32 v155, 0x37800000, v154
	v_cndmask_b32_e32 v154, v154, v155, vcc
	v_cmp_class_f32_e32 vcc, v152, v183
	s_nop 1
	v_cndmask_b32_e32 v152, v154, v152, vcc
	v_div_scale_f32 v154, s[12:13], v152, v152, 1.0
	v_rcp_f32_e32 v155, v154
	s_add_u32 s12, s22, s57
	v_readlane_b32 s13, v255, 8
	s_addc_u32 s13, s23, s13
	v_fma_f32 v156, -v154, v155, 1.0
	v_fmac_f32_e32 v155, v156, v155
	v_div_scale_f32 v156, vcc, 1.0, v152, 1.0
	v_mul_f32_e32 v157, v156, v155
	v_fma_f32 v158, -v154, v157, v156
	v_fmac_f32_e32 v157, v158, v155
	v_fma_f32 v154, -v154, v157, v156
	v_div_fmas_f32 v154, v154, v155, v157
	v_div_fixup_f32 v152, v154, v152, 1.0
	v_mul_f32_e32 v16, v16, v152
	v_fma_f32 v16, v12, v16, v4
	v_mul_f32_e32 v154, 0xbfb8aa3b, v16
	v_exp_f32_e32 v154, v154
	v_mul_f32_e32 v20, v20, v152
	v_fma_f32 v20, v8, v20, v0
	v_mul_f32_e32 v17, v17, v152
	v_add_f32_e32 v154, 1.0, v154
	v_rcp_f32_e32 v154, v154
	v_fma_f32 v17, v13, v17, v5
	v_mul_f32_e32 v21, v21, v152
	v_fma_f32 v21, v9, v21, v1
	v_mul_f32_e32 v16, v16, v154
	v_mul_f32_e32 v154, 0xbfb8aa3b, v20
	v_exp_f32_e32 v154, v154
	v_mul_f32_e32 v18, v18, v152
	v_mul_f32_e32 v19, v19, v152
	v_fma_f32 v18, v14, v18, v6
	v_add_f32_e32 v154, 1.0, v154
	v_rcp_f32_e32 v154, v154
	v_fma_f32 v19, v15, v19, v7
	v_mul_f32_e32 v22, v22, v152
	v_mul_f32_e32 v23, v23, v152
	v_mul_f32_e32 v20, v20, v154
	v_mul_f32_e32 v154, 0xbfb8aa3b, v17
	v_exp_f32_e32 v154, v154
	v_mul_f32_e32 v152, 0xbfb8aa3b, v19
	v_exp_f32_e32 v152, v152
	v_fma_f32 v22, v10, v22, v2
	v_add_f32_e32 v154, 1.0, v154
	v_rcp_f32_e32 v154, v154
	v_add_f32_e32 v152, 1.0, v152
	v_rcp_f32_e32 v152, v152
	v_fma_f32 v23, v11, v23, v3
	v_mul_f32_e32 v17, v17, v154
	v_mul_f32_e32 v154, 0xbfb8aa3b, v21
	v_exp_f32_e32 v154, v154
	v_mul_f32_e32 v19, v19, v152
	v_mul_f32_e32 v152, 0xbfb8aa3b, v23
	v_exp_f32_e32 v152, v152
	v_add_f32_e32 v154, 1.0, v154
	v_rcp_f32_e32 v154, v154
	s_lshl_b64 s[12:13], s[12:13], 11
	v_add_f32_e32 v152, 1.0, v152
	v_rcp_f32_e32 v152, v152
	v_mul_f32_e32 v21, v21, v154
	v_mul_f32_e32 v154, 0xbfb8aa3b, v18
	v_exp_f32_e32 v154, v154
	v_cvt_pk_bf16_f32 v16, v16, v17
	v_mul_f32_e32 v23, v23, v152
	v_add_f32_e32 v154, 1.0, v154
	v_rcp_f32_e32 v154, v154
	s_nop 0
	v_mul_f32_e32 v18, v18, v154
	v_mul_f32_e32 v154, 0xbfb8aa3b, v22
	v_exp_f32_e32 v154, v154
	v_cvt_pk_bf16_f32 v17, v18, v19
	v_cvt_pk_bf16_f32 v18, v20, v21
	v_lshl_add_u64 v[20:21], v[32:33], 0, s[12:13]
	v_add_f32_e32 v154, 1.0, v154
	v_rcp_f32_e32 v154, v154
	v_readlane_b32 s12, v255, 9
	v_mul_f32_e32 v22, v22, v154
	v_cvt_pk_bf16_f32 v19, v22, v23
	global_store_dwordx4 v[20:21], v[16:19], off offset:1024
	v_add_u32_e32 v20, s12, v62
	ds_read_b128 v[16:19], v20
	ds_read_b128 v[20:23], v20 offset:16
	s_waitcnt lgkmcnt(1)
	v_mov_b32_e32 v154, v17
	v_mov_b32_e32 v155, v18
	v_mov_b32_e32 v156, v16
	v_mov_b32_e32 v157, v19
	v_pk_add_f32 v[154:155], v[154:155], v[156:157]
	s_waitcnt lgkmcnt(0)
	v_mov_b32_e32 v156, v22
	v_mov_b32_e32 v157, v20
	v_mov_b32_e32 v158, v23
	v_mov_b32_e32 v159, v21
	v_pk_add_f32 v[156:157], v[156:157], v[158:159]
	v_add_f32_e32 v152, v154, v155
	v_add_f32_e32 v152, v152, v157
	v_add_f32_e32 v152, v156, v152
	s_waitcnt lgkmcnt(0)
; #define LAS __attribute__((address_space(3)))
; __device__ __forceinline__ unsigned pk2(float lo, float hi) { unsigned r; asm("v_cvt_pk_bf16_f32 %0, %1, %2" : "=v"(r) : "v"(lo), "v"(hi)); return r; }
; __device__ __forceinline__ float sigmoidf_(float x) { return __builtin_amdgcn_rcpf(1.0f + __builtin_amdgcn_exp2f(x * -1.44269504089f)); }
; __device__ __forceinline__ void phase_even_mix(CArgs a, LAS unsigned char* lds, int i2, int wv, int xw  ) {
;     ...
;             for (int tt = 0; tt < 4; ++tt) { const int t = wave * 4 + tt;
;                 f32x4 v0 = *(const LAS f32x4*)(ybuf + t * 512 + lane * 8), v1 = *(const LAS f32x4*)(ybuf + t * 512 + lane * 8 + 4);
;                 const float mean = wave_sum((v0.x + v0.y) + (v0.z + v0.w) + (v1.x + v1.y) + (v1.z + v1.w), lane) * (1.f / 512.f);
;                 v0 = v0 - mean; v1 = v1 - mean;
;                 const float var = wave_sum((v0.x * v0.x + v0.y * v0.y) + (v0.z * v0.z + v0.w * v0.w) + (v1.x * v1.x + v1.y * v1.y) + (v1.z * v1.z + v1.w * v1.w), lane) * (1.f / 512.f);
;                 const float rstd = 1.0f / sqrtf(var + LN_EPS);
;                 float o[8];
; #pragma unroll
;                 for (int j = 0; j < 4; ++j) { const float x0 = v0[j] * rstd * g0[j] + b0[j], x1 = v1[j] * rstd * g1[j] + b1[j]; o[j] = x0 * sigmoidf_(x0); o[4 + j] = x1 * sigmoidf_(x1); }
;                 u32x4 wv4; wv4.x = pk2(o[0], o[1]); wv4.y = pk2(o[2], o[3]); wv4.z = pk2(o[4], o[5]); wv4.w = pk2(o[6], o[7]);
;                 *(u32x4*)(YB + (tokbase + t) * DM + 512 + lane * 8) = wv4; }
;         }
;         __syncthreads();
	s_nop 1
	v_add_f32_dpp v152, v152, v152 quad_perm:[1,0,3,2] row_mask:0xf bank_mask:0xf
	s_nop 1
	v_add_f32_dpp v152, v152, v152 quad_perm:[2,3,0,1] row_mask:0xf bank_mask:0xf
	s_nop 1
	v_add_f32_dpp v152, v152, v152 row_half_mirror row_mask:0xf bank_mask:0xf
	s_nop 1
	v_add_f32_dpp v152, v152, v152 row_mirror row_mask:0xf bank_mask:0xf
	v_mov_b32_e32 v154, v152
	s_nop 1
	v_permlane16_swap_b32_e32 v154, v152
	v_add_f32_e32 v152, v152, v154
	v_mov_b32_e32 v154, v152
	s_nop 1
	v_permlane32_swap_b32_e32 v154, v152
	v_add_f32_e32 v152, v152, v154
	v_fmamk_f32 v19, v152, 0xbb000000, v19
	v_fmac_f32_e32 v17, 0xbb000000, v152
	v_fmamk_f32 v18, v152, 0xbb000000, v18
	v_fmamk_f32 v16, v152, 0xbb000000, v16
	v_fmamk_f32 v22, v152, 0xbb000000, v22
	v_fmamk_f32 v23, v152, 0xbb000000, v23
	v_fmamk_f32 v20, v152, 0xbb000000, v20
	v_fmac_f32_e32 v21, 0xbb000000, v152
	v_mul_f32_e32 v152, v17, v17
	v_mul_f32_e32 v154, v19, v19
	v_fmac_f32_e32 v152, v16, v16
	v_fmac_f32_e32 v154, v18, v18
	v_add_f32_e32 v152, v152, v154
	v_mul_f32_e32 v154, v21, v21
	v_fmac_f32_e32 v154, v20, v20
	v_add_f32_e32 v152, v154, v152
	v_mul_f32_e32 v154, v23, v23
	v_fmac_f32_e32 v154, v22, v22
	v_add_f32_e32 v152, v154, v152
	s_waitcnt lgkmcnt(0)
	s_nop 1
	v_add_f32_dpp v152, v152, v152 quad_perm:[1,0,3,2] row_mask:0xf bank_mask:0xf
	s_nop 1
	v_add_f32_dpp v152, v152, v152 quad_perm:[2,3,0,1] row_mask:0xf bank_mask:0xf
	s_nop 1
	v_add_f32_dpp v152, v152, v152 row_half_mirror row_mask:0xf bank_mask:0xf
	s_nop 1
	v_add_f32_dpp v152, v152, v152 row_mirror row_mask:0xf bank_mask:0xf
	v_mov_b32_e32 v154, v152
	s_nop 1
	v_permlane16_swap_b32_e32 v154, v152
	v_add_f32_e32 v152, v152, v154
	v_mov_b32_e32 v154, v152
	s_nop 1
	v_permlane32_swap_b32_e32 v154, v152
	v_add_f32_e32 v152, v152, v154
	v_fmamk_f32 v152, v152, 0x3b000000, v185
	v_cmp_gt_f32_e32 vcc, s55, v152
	v_mul_f32_e32 v154, 0x4f800000, v152
	s_nop 0
	v_cndmask_b32_e32 v152, v152, v154, vcc
	v_sqrt_f32_e32 v154, v152
	s_nop 0
	v_add_u32_e32 v155, -1, v154
	v_fma_f32 v156, -v155, v154, v152
	v_cmp_ge_f32_e64 s[12:13], 0, v156
	v_add_u32_e32 v156, 1, v154
	s_nop 0
	v_cndmask_b32_e64 v155, v154, v155, s[12:13]
	v_fma_f32 v154, -v156, v154, v152
	v_cmp_lt_f32_e64 s[12:13], 0, v154
	s_nop 1
	v_cndmask_b32_e64 v154, v155, v156, s[12:13]
	v_mul_f32_e32 v155, 0x37800000, v154
	v_cndmask_b32_e32 v154, v154, v155, vcc
	v_cmp_class_f32_e32 vcc, v152, v183
	s_nop 1
	v_cndmask_b32_e32 v152, v154, v152, vcc
	v_div_scale_f32 v154, s[12:13], v152, v152, 1.0
	v_rcp_f32_e32 v155, v154
	s_add_u32 s12, s22, s14
	v_readlane_b32 s13, v255, 10
	s_addc_u32 s13, s23, s13
	v_fma_f32 v156, -v154, v155, 1.0
	v_fmac_f32_e32 v155, v156, v155
	v_div_scale_f32 v156, vcc, 1.0, v152, 1.0
	v_mul_f32_e32 v157, v156, v155
	v_fma_f32 v158, -v154, v157, v156
	v_fmac_f32_e32 v157, v158, v155
	v_fma_f32 v154, -v154, v157, v156
	v_div_fmas_f32 v154, v154, v155, v157
	v_div_fixup_f32 v152, v154, v152, 1.0
	v_mul_f32_e32 v16, v16, v152
	v_fma_f32 v4, v12, v16, v4
	v_mul_f32_e32 v12, v20, v152
	v_fma_f32 v0, v8, v12, v0
	v_mul_f32_e32 v8, 0xbfb8aa3b, v4
	v_exp_f32_e32 v8, v8
	s_lshl_b64 s[12:13], s[12:13], 11
	v_add_f32_e32 v8, 1.0, v8
	v_rcp_f32_e32 v8, v8
	s_nop 0
	v_mul_f32_e32 v4, v4, v8
	v_mul_f32_e32 v8, 0xbfb8aa3b, v0
	v_exp_f32_e32 v8, v8
	s_nop 0
	v_add_f32_e32 v8, 1.0, v8
	v_rcp_f32_e32 v8, v8
	s_nop 0
	v_mul_f32_e32 v8, v0, v8
	v_mul_f32_e32 v0, v17, v152
	v_fma_f32 v0, v13, v0, v5
	v_mul_f32_e32 v5, v21, v152
	v_fma_f32 v1, v9, v5, v1
	v_mul_f32_e32 v5, 0xbfb8aa3b, v0
	v_exp_f32_e32 v5, v5
	s_nop 0
	v_add_f32_e32 v5, 1.0, v5
	v_rcp_f32_e32 v5, v5
	s_nop 0
	v_mul_f32_e32 v0, v0, v5
	v_mul_f32_e32 v5, 0xbfb8aa3b, v1
	v_exp_f32_e32 v5, v5
	v_cvt_pk_bf16_f32 v0, v4, v0
	s_nop 0
	v_add_f32_e32 v5, 1.0, v5
	v_rcp_f32_e32 v5, v5
	s_nop 0
	v_mul_f32_e32 v5, v1, v5
	v_mul_f32_e32 v1, v18, v152
	v_fma_f32 v1, v14, v1, v6
	v_mul_f32_e32 v6, v22, v152
	v_fma_f32 v2, v10, v6, v2
	v_mul_f32_e32 v6, 0xbfb8aa3b, v1
	v_exp_f32_e32 v6, v6
	s_nop 0
	v_add_f32_e32 v6, 1.0, v6
	v_rcp_f32_e32 v6, v6
	s_nop 0
	v_mul_f32_e32 v1, v1, v6
	v_mul_f32_e32 v6, 0xbfb8aa3b, v2
	v_exp_f32_e32 v6, v6
	s_nop 0
	v_add_f32_e32 v6, 1.0, v6
	v_rcp_f32_e32 v6, v6
	s_nop 0
	v_mul_f32_e32 v6, v2, v6
	v_mul_f32_e32 v2, v19, v152
	v_fmac_f32_e32 v7, v15, v2
	v_mul_f32_e32 v2, v23, v152
	v_fmac_f32_e32 v3, v11, v2
	v_mul_f32_e32 v2, 0xbfb8aa3b, v7
	v_exp_f32_e32 v2, v2
	s_nop 0
	v_add_f32_e32 v2, 1.0, v2
	v_rcp_f32_e32 v2, v2
	s_nop 0
	v_mul_f32_e32 v2, v7, v2
	v_mul_f32_e32 v7, 0xbfb8aa3b, v3
	v_exp_f32_e32 v7, v7
	v_cvt_pk_bf16_f32 v1, v1, v2
	v_cvt_pk_bf16_f32 v2, v8, v5
	v_lshl_add_u64 v[4:5], v[32:33], 0, s[12:13]
	v_add_f32_e32 v7, 1.0, v7
	v_rcp_f32_e32 v7, v7
	s_or_b32 s12, s15, 1
	s_min_i32 s12, s12, s28
	v_mul_f32_e32 v3, v3, v7
	v_cvt_pk_bf16_f32 v3, v6, v3
	global_store_dwordx4 v[4:5], v[0:3], off offset:1024
	s_barrier
; __device__ __forceinline__ unsigned f2bf(float f) { unsigned u = __builtin_bit_cast(unsigned, f); return (u + 0x7fffu + ((u >> 16) & 1u)) >> 16; }
; __device__ __forceinline__ void phase_even_mix(CArgs a, LAS unsigned char* lds, int i2, int wv, int xw  ) {
;     ...
;             const int g = wave >> 1, winw = 2 << g;
;             float pprev = 0.f, a2r[3] = {0.f, 0.f, 0.f}, a4r[5] = {0.f, 0.f, 0.f, 0.f, 0.f}, a8r[9] = {0.f, 0.f, 0.f, 0.f, 0.f, 0.f, 0.f, 0.f, 0.f};
; #pragma clang loop unroll(full)
;             for (int r = 0; r < 48; ++r) {
;                 const float p = bf2f(glu[r * 512 + c]);
;                 const float a2 = p + pprev, a4 = a2 + a2r[(r + 1) % 3], a8 = a4 + a4r[(r + 1) % 5], a16 = a8 + a8r[(r + 1) % 9];
;                 a2r[r % 3] = a2; a4r[r % 5] = a4; a8r[r % 9] = a8; pprev = p;
;                 if (r >= 16) { const float s = g == 0 ? a2 : (g == 1 ? a4 : (g == 2 ? a8 : a16));
;                     const int pos = t0 + r - 16; const float cnt = (float)((pos + 1) < winw ? (pos + 1) : winw);
;                     pl[(r - 16) * PLS + c] = (bf16)f2bf(s / cnt - p); }
;             }
;         }
	ds_read_u16 v0, v35 offset:1024
	ds_read_u16 v1, v35 offset:2048
	ds_read_u16 v2, v35 offset:3072
	ds_read_u16 v3, v35 offset:4096
	ds_read_u16 v4, v35 offset:5120
	ds_read_u16 v5, v35 offset:6144
	ds_read_u16 v6, v35 offset:7168
	ds_read_u16 v7, v35 offset:8192
	s_waitcnt lgkmcnt(7)
	v_lshlrev_b32_e32 v0, 16, v0
	s_waitcnt lgkmcnt(6)
	v_lshlrev_b32_e32 v1, 16, v1
	s_waitcnt lgkmcnt(5)
	v_lshlrev_b32_e32 v2, 16, v2
	s_waitcnt lgkmcnt(4)
	v_lshlrev_b32_e32 v3, 16, v3
	s_waitcnt lgkmcnt(3)
	v_lshlrev_b32_e32 v4, 16, v4
	s_waitcnt lgkmcnt(2)
	v_lshlrev_b32_e32 v5, 16, v5
	s_waitcnt lgkmcnt(1)
	v_lshlrev_b32_e32 v6, 16, v6
	s_waitcnt lgkmcnt(0)
	v_lshlrev_b32_e32 v7, 16, v7
	v_add_f32_e32 v0, v0, v1
	v_add_f32_e32 v1, v1, v2
	v_add_f32_e32 v2, v2, v3
	v_add_f32_e32 v3, v3, v4
	v_add_f32_e32 v4, v4, v5
	v_add_f32_e32 v5, v5, v6
	v_add_f32_e32 v6, v6, v7
	v_add_f32_e32 v0, v0, v2
	v_add_f32_e32 v2, v2, v4
	v_add_f32_e32 v4, v4, v6
	v_add_f32_e32 v8, v0, v4
	ds_read_u16 v0, v35 offset:9216
	v_add_f32_e32 v1, v1, v3
	v_add_f32_e32 v3, v3, v5
	s_waitcnt lgkmcnt(0)
	v_lshlrev_b32_e32 v0, 16, v0
	v_add_f32_e32 v7, v7, v0
	v_add_f32_e32 v9, v5, v7
	v_add_f32_e32 v11, v1, v9
	ds_read_u16 v1, v35 offset:10240
	s_waitcnt lgkmcnt(0)
	v_lshlrev_b32_e32 v1, 16, v1
	v_add_f32_e32 v0, v0, v1
	v_add_f32_e32 v10, v6, v0
	v_add_f32_e32 v13, v2, v10
	ds_read_u16 v2, v35 offset:11264
	s_waitcnt lgkmcnt(0)
	v_lshlrev_b32_e32 v2, 16, v2
	v_add_f32_e32 v1, v1, v2
	v_add_f32_e32 v12, v7, v1
	v_add_f32_e32 v5, v3, v12
	ds_read_u16 v3, v35 offset:12288
	s_waitcnt lgkmcnt(0)
	v_lshlrev_b32_e32 v3, 16, v3
	v_add_f32_e32 v2, v2, v3
	v_add_f32_e32 v14, v0, v2
	ds_read_u16 v0, v35 offset:13312
	v_add_f32_e32 v6, v4, v14
	s_waitcnt lgkmcnt(0)
	v_lshlrev_b32_e32 v0, 16, v0
	v_add_f32_e32 v3, v3, v0
	v_add_f32_e32 v4, v1, v3
	ds_read_u16 v1, v35 offset:14336
	v_add_f32_e32 v7, v9, v4
	s_waitcnt lgkmcnt(0)
	v_lshlrev_b32_e32 v1, 16, v1
	v_add_f32_e32 v9, v0, v1
	v_add_f32_e32 v15, v2, v9
	ds_read_u16 v2, v35 offset:15360
	v_add_f32_e32 v0, v10, v15
	s_waitcnt lgkmcnt(0)
	v_lshlrev_b32_e32 v2, 16, v2
	v_add_f32_e32 v10, v1, v2
	ds_read_u16 v1, v35 offset:16384
	v_add_f32_e32 v17, v3, v10
	v_add_f32_e32 v12, v12, v17
	s_waitcnt lgkmcnt(0)
	v_lshlrev_b32_e32 v3, 16, v1
	v_add_f32_e32 v16, v2, v3
	v_add_f32_e32 v9, v9, v16
	v_add_f32_e32 v1, v14, v9
	v_add_f32_e32 v2, v8, v1
	v_cvt_f32_i32_e32 v8, s12
	v_cndmask_b32_e64 v2, v2, v1, s[10:11]
	v_cndmask_b32_e64 v2, v2, v9, s[8:9]
	v_cndmask_b32_e64 v2, v2, v16, s[6:7]
	v_div_scale_f32 v14, s[12:13], v8, v8, v2
	v_rcp_f32_e32 v18, v14
	s_or_b32 s12, s15, 2
	s_min_i32 s12, s12, s28
	v_fma_f32 v19, -v14, v18, 1.0
	v_fmac_f32_e32 v18, v19, v18
	v_div_scale_f32 v19, vcc, v2, v8, v2
	v_mul_f32_e32 v20, v19, v18
	v_fma_f32 v21, -v14, v20, v19
	v_fmac_f32_e32 v20, v21, v18
	v_fma_f32 v14, -v14, v20, v19
	v_div_fmas_f32 v14, v14, v18, v20
	v_div_fixup_f32 v2, v14, v8, v2
	v_sub_f32_e32 v2, v2, v3
	v_bfe_u32 v8, v2, 16, 1
	v_add3_u32 v2, v2, v8, s49
	ds_write_b16_d16_hi v77, v2
	ds_read_u16 v2, v35 offset:17408
	s_waitcnt lgkmcnt(0)
	v_lshlrev_b32_e32 v8, 16, v2
	v_add_f32_e32 v14, v3, v8
	v_add_f32_e32 v10, v10, v14
	v_add_f32_e32 v2, v4, v10
	v_add_f32_e32 v3, v11, v2
	v_cvt_f32_i32_e32 v4, s12
	v_cndmask_b32_e64 v3, v3, v2, s[10:11]
	v_cndmask_b32_e64 v3, v3, v10, s[8:9]
	v_cndmask_b32_e64 v3, v3, v14, s[6:7]
	v_div_scale_f32 v11, s[12:13], v4, v4, v3
	v_rcp_f32_e32 v18, v11
	s_or_b32 s12, s15, 3
	s_min_i32 s12, s12, s28
	v_fma_f32 v19, -v11, v18, 1.0
	v_fmac_f32_e32 v18, v19, v18
	v_div_scale_f32 v19, vcc, v3, v4, v3
	v_mul_f32_e32 v20, v19, v18
	v_fma_f32 v21, -v11, v20, v19
	v_fmac_f32_e32 v20, v21, v18
	v_fma_f32 v11, -v11, v20, v19
	v_div_fmas_f32 v11, v11, v18, v20
	v_div_fixup_f32 v3, v11, v4, v3
	v_sub_f32_e32 v3, v3, v8
	v_bfe_u32 v4, v3, 16, 1
	v_add3_u32 v3, v3, v4, s49
	ds_write_b16_d16_hi v110, v3
	ds_read_u16 v3, v35 offset:18432
	s_waitcnt lgkmcnt(0)
	v_lshlrev_b32_e32 v4, 16, v3
	v_add_f32_e32 v8, v8, v4
	v_add_f32_e32 v11, v16, v8
	v_add_f32_e32 v3, v15, v11
	v_add_f32_e32 v13, v13, v3
	v_cvt_f32_i32_e32 v15, s12
	v_cndmask_b32_e64 v13, v13, v3, s[10:11]
	v_cndmask_b32_e64 v13, v13, v11, s[8:9]
	v_cndmask_b32_e64 v13, v13, v8, s[6:7]
	v_div_scale_f32 v16, s[12:13], v15, v15, v13
	v_rcp_f32_e32 v18, v16
	s_or_b32 s12, s15, 4
	s_min_i32 s12, s12, s28
	v_fma_f32 v19, -v16, v18, 1.0
	v_fmac_f32_e32 v18, v19, v18
	v_div_scale_f32 v19, vcc, v13, v15, v13
	v_mul_f32_e32 v20, v19, v18
	v_fma_f32 v21, -v16, v20, v19
	v_fmac_f32_e32 v20, v21, v18
	v_fma_f32 v16, -v16, v20, v19
	v_div_fmas_f32 v16, v16, v18, v20
	v_div_fixup_f32 v13, v16, v15, v13
	v_sub_f32_e32 v13, v13, v4
	v_bfe_u32 v15, v13, 16, 1
	v_add3_u32 v13, v13, v15, s49
	ds_write_b16_d16_hi v111, v13
	ds_read_u16 v13, v35 offset:19456
	s_waitcnt lgkmcnt(0)
	v_lshlrev_b32_e32 v13, 16, v13
	v_add_f32_e32 v15, v4, v13
	v_add_f32_e32 v16, v14, v15
	v_add_f32_e32 v4, v17, v16
	v_add_f32_e32 v5, v5, v4
	v_cvt_f32_i32_e32 v14, s12
	v_cndmask_b32_e64 v5, v5, v4, s[10:11]
	v_cndmask_b32_e64 v5, v5, v16, s[8:9]
	v_cndmask_b32_e64 v5, v5, v15, s[6:7]
	v_div_scale_f32 v17, s[12:13], v14, v14, v5
	v_rcp_f32_e32 v18, v17
	s_or_b32 s12, s15, 5
	s_min_i32 s12, s12, s28
	v_fma_f32 v19, -v17, v18, 1.0
	v_fmac_f32_e32 v18, v19, v18
	v_div_scale_f32 v19, vcc, v5, v14, v5
	v_mul_f32_e32 v20, v19, v18
	v_fma_f32 v21, -v17, v20, v19
	v_fmac_f32_e32 v20, v21, v18
	v_fma_f32 v17, -v17, v20, v19
	v_div_fmas_f32 v17, v17, v18, v20
	v_div_fixup_f32 v5, v17, v14, v5
	v_sub_f32_e32 v5, v5, v13
	v_bfe_u32 v14, v5, 16, 1
	v_add3_u32 v5, v5, v14, s49
	ds_write_b16_d16_hi v112, v5
	ds_read_u16 v5, v35 offset:20480
	s_waitcnt lgkmcnt(0)
; __device__ __forceinline__ unsigned f2bf(float f) { unsigned u = __builtin_bit_cast(unsigned, f); return (u + 0x7fffu + ((u >> 16) & 1u)) >> 16; }
; __device__ __forceinline__ void phase_even_mix(CArgs a, LAS unsigned char* lds, int i2, int wv, int xw  ) {
;     ...
;             const int g = wave >> 1, winw = 2 << g;
;             float pprev = 0.f, a2r[3] = {0.f, 0.f, 0.f}, a4r[5] = {0.f, 0.f, 0.f, 0.f, 0.f}, a8r[9] = {0.f, 0.f, 0.f, 0.f, 0.f, 0.f, 0.f, 0.f, 0.f};
; #pragma clang loop unroll(full)
;             for (int r = 0; r < 48; ++r) {
;                 const float p = bf2f(glu[r * 512 + c]);
;                 const float a2 = p + pprev, a4 = a2 + a2r[(r + 1) % 3], a8 = a4 + a4r[(r + 1) % 5], a16 = a8 + a8r[(r + 1) % 9];
;                 a2r[r % 3] = a2; a4r[r % 5] = a4; a8r[r % 9] = a8; pprev = p;
;                 if (r >= 16) { const float s = g == 0 ? a2 : (g == 1 ? a4 : (g == 2 ? a8 : a16));
;                     const int pos = t0 + r - 16; const float cnt = (float)((pos + 1) < winw ? (pos + 1) : winw);
;                     pl[(r - 16) * PLS + c] = (bf16)f2bf(s / cnt - p); }
;             }
;         }
	v_lshlrev_b32_e32 v14, 16, v5
	v_add_f32_e32 v17, v13, v14
	v_add_f32_e32 v8, v8, v17
	v_add_f32_e32 v5, v9, v8
	v_add_f32_e32 v6, v6, v5
	v_cvt_f32_i32_e32 v9, s12
	v_cndmask_b32_e64 v6, v6, v5, s[10:11]
	v_cndmask_b32_e64 v6, v6, v8, s[8:9]
	v_cndmask_b32_e64 v6, v6, v17, s[6:7]
	v_div_scale_f32 v13, s[12:13], v9, v9, v6
	v_rcp_f32_e32 v18, v13
	s_or_b32 s12, s15, 6
	s_min_i32 s12, s12, s28
	v_fma_f32 v19, -v13, v18, 1.0
	v_fmac_f32_e32 v18, v19, v18
	v_div_scale_f32 v19, vcc, v6, v9, v6
	v_mul_f32_e32 v20, v19, v18
	v_fma_f32 v21, -v13, v20, v19
	v_fmac_f32_e32 v20, v21, v18
	v_fma_f32 v13, -v13, v20, v19
	v_div_fmas_f32 v13, v13, v18, v20
	v_div_fixup_f32 v6, v13, v9, v6
	v_sub_f32_e32 v6, v6, v14
	v_bfe_u32 v9, v6, 16, 1
	v_add3_u32 v6, v6, v9, s49
	ds_write_b16_d16_hi v113, v6
	ds_read_u16 v6, v35 offset:21504
	s_waitcnt lgkmcnt(0)
	v_lshlrev_b32_e32 v13, 16, v6
	v_add_f32_e32 v18, v14, v13
	v_add_f32_e32 v9, v15, v18
	v_add_f32_e32 v6, v10, v9
	v_add_f32_e32 v7, v7, v6
	v_cvt_f32_i32_e32 v10, s12
	v_cndmask_b32_e64 v7, v7, v6, s[10:11]
	v_cndmask_b32_e64 v7, v7, v9, s[8:9]
	v_cndmask_b32_e64 v7, v7, v18, s[6:7]
	v_div_scale_f32 v14, s[12:13], v10, v10, v7
	v_rcp_f32_e32 v15, v14
	s_or_b32 s12, s15, 7
	s_min_i32 s12, s12, s28
	v_fma_f32 v19, -v14, v15, 1.0
	v_fmac_f32_e32 v15, v19, v15
	v_div_scale_f32 v19, vcc, v7, v10, v7
	v_mul_f32_e32 v20, v19, v15
	v_fma_f32 v21, -v14, v20, v19
	v_fmac_f32_e32 v20, v21, v15
	v_fma_f32 v14, -v14, v20, v19
	v_div_fmas_f32 v14, v14, v15, v20
	v_div_fixup_f32 v7, v14, v10, v7
	v_sub_f32_e32 v7, v7, v13
	v_bfe_u32 v10, v7, 16, 1
	v_add3_u32 v7, v7, v10, s49
	ds_write_b16_d16_hi v114, v7
	ds_read_u16 v7, v35 offset:22528
	s_waitcnt lgkmcnt(0)
	v_lshlrev_b32_e32 v15, 16, v7
	v_add_f32_e32 v13, v13, v15
	v_add_f32_e32 v10, v17, v13
	v_add_f32_e32 v7, v11, v10
	v_add_f32_e32 v0, v0, v7
	v_cvt_f32_i32_e32 v11, s12
	v_cndmask_b32_e64 v0, v0, v7, s[10:11]
	v_cndmask_b32_e64 v0, v0, v10, s[8:9]
	v_cndmask_b32_e64 v0, v0, v13, s[6:7]
	v_div_scale_f32 v14, s[12:13], v11, v11, v0
	v_rcp_f32_e32 v17, v14
	s_or_b32 s12, s15, 8
	s_min_i32 s12, s12, s28
	v_fma_f32 v19, -v14, v17, 1.0
	v_fmac_f32_e32 v17, v19, v17
	v_div_scale_f32 v19, vcc, v0, v11, v0
	v_mul_f32_e32 v20, v19, v17
	v_fma_f32 v21, -v14, v20, v19
	v_fmac_f32_e32 v20, v21, v17
	v_fma_f32 v14, -v14, v20, v19
	v_div_fmas_f32 v14, v14, v17, v20
	v_div_fixup_f32 v0, v14, v11, v0
	v_sub_f32_e32 v0, v0, v15
	v_bfe_u32 v11, v0, 16, 1
	v_add3_u32 v0, v0, v11, s49
	ds_write_b16_d16_hi v115, v0
	ds_read_u16 v0, v35 offset:23552
	s_waitcnt lgkmcnt(0)
	v_lshlrev_b32_e32 v14, 16, v0
	v_add_f32_e32 v15, v15, v14
	v_add_f32_e32 v11, v18, v15
	v_add_f32_e32 v0, v16, v11
	v_add_f32_e32 v12, v12, v0
	v_cvt_f32_i32_e32 v16, s12
	v_cndmask_b32_e64 v12, v12, v0, s[10:11]
	v_cndmask_b32_e64 v12, v12, v11, s[8:9]
	v_cndmask_b32_e64 v12, v12, v15, s[6:7]
	v_div_scale_f32 v17, s[12:13], v16, v16, v12
	v_rcp_f32_e32 v18, v17
	s_or_b32 s12, s15, 9
	s_min_i32 s12, s12, s28
	v_fma_f32 v19, -v17, v18, 1.0
	v_fmac_f32_e32 v18, v19, v18
	v_div_scale_f32 v19, vcc, v12, v16, v12
	v_mul_f32_e32 v20, v19, v18
	v_fma_f32 v21, -v17, v20, v19
	v_fmac_f32_e32 v20, v21, v18
	v_fma_f32 v17, -v17, v20, v19
	v_div_fmas_f32 v17, v17, v18, v20
	v_div_fixup_f32 v12, v17, v16, v12
	v_sub_f32_e32 v12, v12, v14
	v_bfe_u32 v16, v12, 16, 1
	v_add3_u32 v12, v12, v16, s49
	ds_write_b16_d16_hi v116, v12
	ds_read_u16 v12, v35 offset:24576
	s_waitcnt lgkmcnt(0)
	v_lshlrev_b32_e32 v12, 16, v12
	v_add_f32_e32 v16, v14, v12
	v_add_f32_e32 v17, v13, v16
	v_add_f32_e32 v14, v8, v17
	v_add_f32_e32 v1, v1, v14
	v_cvt_f32_i32_e32 v8, s12
	v_cndmask_b32_e64 v1, v1, v14, s[10:11]
	v_cndmask_b32_e64 v1, v1, v17, s[8:9]
	v_cndmask_b32_e64 v1, v1, v16, s[6:7]
	v_div_scale_f32 v13, s[12:13], v8, v8, v1
	v_rcp_f32_e32 v18, v13
	s_or_b32 s12, s15, 10
	s_min_i32 s12, s12, s28
	v_fma_f32 v19, -v13, v18, 1.0
	v_fmac_f32_e32 v18, v19, v18
	v_div_scale_f32 v19, vcc, v1, v8, v1
	v_mul_f32_e32 v20, v19, v18
	v_fma_f32 v21, -v13, v20, v19
	v_fmac_f32_e32 v20, v21, v18
	v_fma_f32 v13, -v13, v20, v19
	v_div_fmas_f32 v13, v13, v18, v20
	v_div_fixup_f32 v1, v13, v8, v1
	v_sub_f32_e32 v1, v1, v12
	v_bfe_u32 v8, v1, 16, 1
	v_add3_u32 v1, v1, v8, s49
	ds_write_b16_d16_hi v117, v1
	ds_read_u16 v1, v35 offset:25600
	s_waitcnt lgkmcnt(0)
	v_lshlrev_b32_e32 v1, 16, v1
	v_add_f32_e32 v18, v12, v1
	v_add_f32_e32 v12, v15, v18
	v_add_f32_e32 v8, v9, v12
	v_add_f32_e32 v2, v2, v8
	v_cvt_f32_i32_e32 v9, s12
	v_cndmask_b32_e64 v2, v2, v8, s[10:11]
	v_cndmask_b32_e64 v2, v2, v12, s[8:9]
	v_cndmask_b32_e64 v2, v2, v18, s[6:7]
	v_div_scale_f32 v13, s[12:13], v9, v9, v2
	v_rcp_f32_e32 v15, v13
	s_or_b32 s12, s15, 11
	s_min_i32 s12, s12, s28
	v_fma_f32 v19, -v13, v15, 1.0
	v_fmac_f32_e32 v15, v19, v15
	v_div_scale_f32 v19, vcc, v2, v9, v2
	v_mul_f32_e32 v20, v19, v15
	v_fma_f32 v21, -v13, v20, v19
	v_fmac_f32_e32 v20, v21, v15
	v_fma_f32 v13, -v13, v20, v19
	v_div_fmas_f32 v13, v13, v15, v20
	v_div_fixup_f32 v2, v13, v9, v2
	v_sub_f32_e32 v2, v2, v1
	v_bfe_u32 v9, v2, 16, 1
	v_add3_u32 v2, v2, v9, s49
	ds_write_b16_d16_hi v118, v2
	ds_read_u16 v2, v35 offset:26624
	s_waitcnt lgkmcnt(0)
	v_lshlrev_b32_e32 v2, 16, v2
	v_add_f32_e32 v15, v1, v2
	v_add_f32_e32 v13, v16, v15
	v_add_f32_e32 v9, v10, v13
	v_add_f32_e32 v1, v3, v9
	v_cvt_f32_i32_e32 v3, s12
	v_cndmask_b32_e64 v1, v1, v9, s[10:11]
	v_cndmask_b32_e64 v1, v1, v13, s[8:9]
	v_cndmask_b32_e64 v1, v1, v15, s[6:7]
	v_div_scale_f32 v10, s[12:13], v3, v3, v1
	v_rcp_f32_e32 v16, v10
	s_or_b32 s12, s15, 12
	s_min_i32 s12, s12, s28
	v_fma_f32 v19, -v10, v16, 1.0
	v_fmac_f32_e32 v16, v19, v16
	v_div_scale_f32 v19, vcc, v1, v3, v1
	v_mul_f32_e32 v20, v19, v16
	v_fma_f32 v21, -v10, v20, v19
	v_fmac_f32_e32 v20, v21, v16
	v_fma_f32 v10, -v10, v20, v19
	v_div_fmas_f32 v10, v10, v16, v20
	v_div_fixup_f32 v1, v10, v3, v1
	v_sub_f32_e32 v1, v1, v2
	v_bfe_u32 v3, v1, 16, 1
	v_add3_u32 v1, v1, v3, s49
	ds_write_b16_d16_hi v119, v1
	ds_read_u16 v1, v35 offset:27648
	s_waitcnt lgkmcnt(0)
; __device__ __forceinline__ unsigned f2bf(float f) { unsigned u = __builtin_bit_cast(unsigned, f); return (u + 0x7fffu + ((u >> 16) & 1u)) >> 16; }
; __device__ __forceinline__ void phase_even_mix(CArgs a, LAS unsigned char* lds, int i2, int wv, int xw  ) {
;     ...
;             const int g = wave >> 1, winw = 2 << g;
;             float pprev = 0.f, a2r[3] = {0.f, 0.f, 0.f}, a4r[5] = {0.f, 0.f, 0.f, 0.f, 0.f}, a8r[9] = {0.f, 0.f, 0.f, 0.f, 0.f, 0.f, 0.f, 0.f, 0.f};
; #pragma clang loop unroll(full)
;             for (int r = 0; r < 48; ++r) {
;                 const float p = bf2f(glu[r * 512 + c]);
;                 const float a2 = p + pprev, a4 = a2 + a2r[(r + 1) % 3], a8 = a4 + a4r[(r + 1) % 5], a16 = a8 + a8r[(r + 1) % 9];
;                 a2r[r % 3] = a2; a4r[r % 5] = a4; a8r[r % 9] = a8; pprev = p;
;                 if (r >= 16) { const float s = g == 0 ? a2 : (g == 1 ? a4 : (g == 2 ? a8 : a16));
;                     const int pos = t0 + r - 16; const float cnt = (float)((pos + 1) < winw ? (pos + 1) : winw);
;                     pl[(r - 16) * PLS + c] = (bf16)f2bf(s / cnt - p); }
;             }
;         }
	v_lshlrev_b32_e32 v3, 16, v1
	v_add_f32_e32 v16, v2, v3
	v_add_f32_e32 v1, v18, v16
	v_add_f32_e32 v10, v11, v1
	v_add_f32_e32 v2, v4, v10
	v_cvt_f32_i32_e32 v4, s12
	v_cndmask_b32_e64 v2, v2, v10, s[10:11]
	v_cndmask_b32_e64 v2, v2, v1, s[8:9]
	v_cndmask_b32_e64 v2, v2, v16, s[6:7]
	v_div_scale_f32 v11, s[12:13], v4, v4, v2
	v_rcp_f32_e32 v18, v11
	s_or_b32 s12, s15, 13
	s_min_i32 s12, s12, s28
	v_fma_f32 v19, -v11, v18, 1.0
	v_fmac_f32_e32 v18, v19, v18
	v_div_scale_f32 v19, vcc, v2, v4, v2
	v_mul_f32_e32 v20, v19, v18
	v_fma_f32 v21, -v11, v20, v19
	v_fmac_f32_e32 v20, v21, v18
	v_fma_f32 v11, -v11, v20, v19
	v_div_fmas_f32 v11, v11, v18, v20
	v_div_fixup_f32 v2, v11, v4, v2
	v_sub_f32_e32 v2, v2, v3
	v_bfe_u32 v4, v2, 16, 1
	v_add3_u32 v2, v2, v4, s49
	ds_write_b16_d16_hi v120, v2
	ds_read_u16 v2, v35 offset:28672
	s_waitcnt lgkmcnt(0)
	v_lshlrev_b32_e32 v4, 16, v2
	v_add_f32_e32 v18, v3, v4
	v_add_f32_e32 v2, v15, v18
	v_add_f32_e32 v11, v17, v2
	v_add_f32_e32 v3, v5, v11
	v_cvt_f32_i32_e32 v5, s12
	v_cndmask_b32_e64 v3, v3, v11, s[10:11]
	v_cndmask_b32_e64 v3, v3, v2, s[8:9]
	v_cndmask_b32_e64 v3, v3, v18, s[6:7]
	v_div_scale_f32 v15, s[12:13], v5, v5, v3
	v_rcp_f32_e32 v17, v15
	s_or_b32 s12, s15, 14
	s_min_i32 s12, s12, s28
	v_fma_f32 v19, -v15, v17, 1.0
	v_fmac_f32_e32 v17, v19, v17
	v_div_scale_f32 v19, vcc, v3, v5, v3
	v_mul_f32_e32 v20, v19, v17
	v_fma_f32 v21, -v15, v20, v19
	v_fmac_f32_e32 v20, v21, v17
	v_fma_f32 v15, -v15, v20, v19
	v_div_fmas_f32 v15, v15, v17, v20
	v_div_fixup_f32 v3, v15, v5, v3
	v_sub_f32_e32 v3, v3, v4
	v_bfe_u32 v5, v3, 16, 1
	v_add3_u32 v3, v3, v5, s49
	ds_write_b16_d16_hi v121, v3
	ds_read_u16 v3, v35 offset:29696
	s_waitcnt lgkmcnt(0)
	v_lshlrev_b32_e32 v17, 16, v3
	v_add_f32_e32 v5, v4, v17
	v_add_f32_e32 v3, v16, v5
	v_add_f32_e32 v12, v12, v3
	v_add_f32_e32 v4, v6, v12
	v_cvt_f32_i32_e32 v6, s12
	v_cndmask_b32_e64 v4, v4, v12, s[10:11]
	v_cndmask_b32_e64 v4, v4, v3, s[8:9]
	v_cndmask_b32_e64 v4, v4, v5, s[6:7]
	v_div_scale_f32 v15, s[12:13], v6, v6, v4
	v_rcp_f32_e32 v16, v15
	s_or_b32 s12, s15, 15
	s_min_i32 s12, s12, s28
	v_fma_f32 v19, -v15, v16, 1.0
	v_fmac_f32_e32 v16, v19, v16
	v_div_scale_f32 v19, vcc, v4, v6, v4
	v_mul_f32_e32 v20, v19, v16
	v_fma_f32 v21, -v15, v20, v19
	v_fmac_f32_e32 v20, v21, v16
	v_fma_f32 v15, -v15, v20, v19
	v_div_fmas_f32 v15, v15, v16, v20
	v_div_fixup_f32 v4, v15, v6, v4
	v_sub_f32_e32 v4, v4, v17
	v_bfe_u32 v6, v4, 16, 1
	v_add3_u32 v4, v4, v6, s49
	ds_write_b16_d16_hi v122, v4
	ds_read_u16 v4, v35 offset:30720
	v_cvt_f32_i32_e32 v16, s12
	s_waitcnt lgkmcnt(0)
	v_lshlrev_b32_e32 v15, 16, v4
	v_add_f32_e32 v6, v17, v15
	v_add_f32_e32 v4, v18, v6
	v_add_f32_e32 v13, v13, v4
	v_add_f32_e32 v7, v7, v13
	v_cndmask_b32_e64 v7, v7, v13, s[10:11]
	v_cndmask_b32_e64 v7, v7, v4, s[8:9]
	v_cndmask_b32_e64 v7, v7, v6, s[6:7]
	v_div_scale_f32 v17, s[12:13], v16, v16, v7
	v_rcp_f32_e32 v18, v17
	s_or_b32 s12, s15, 16
	s_min_i32 s12, s12, s28
	v_fma_f32 v19, -v17, v18, 1.0
	v_fmac_f32_e32 v18, v19, v18
	v_div_scale_f32 v19, vcc, v7, v16, v7
	v_mul_f32_e32 v20, v19, v18
	v_fma_f32 v21, -v17, v20, v19
	v_fmac_f32_e32 v20, v21, v18
	v_fma_f32 v17, -v17, v20, v19
	v_div_fmas_f32 v17, v17, v18, v20
	v_div_fixup_f32 v7, v17, v16, v7
	v_sub_f32_e32 v7, v7, v15
	v_bfe_u32 v16, v7, 16, 1
	v_add3_u32 v7, v7, v16, s49
	ds_write_b16_d16_hi v123, v7
	ds_read_u16 v7, v35 offset:31744
	s_waitcnt lgkmcnt(0)
	v_lshlrev_b32_e32 v7, 16, v7
	v_add_f32_e32 v15, v15, v7
	v_add_f32_e32 v16, v5, v15
	v_add_f32_e32 v1, v1, v16
	v_add_f32_e32 v0, v0, v1
	v_cvt_f32_i32_e32 v5, s12
	v_cndmask_b32_e64 v0, v0, v1, s[10:11]
	v_cndmask_b32_e64 v0, v0, v16, s[8:9]
	v_cndmask_b32_e64 v0, v0, v15, s[6:7]
	v_div_scale_f32 v17, s[12:13], v5, v5, v0
	v_rcp_f32_e32 v18, v17
	s_or_b32 s12, s15, 17
	s_min_i32 s12, s12, s28
	v_fma_f32 v19, -v17, v18, 1.0
	v_fmac_f32_e32 v18, v19, v18
	v_div_scale_f32 v19, vcc, v0, v5, v0
	v_mul_f32_e32 v20, v19, v18
	v_fma_f32 v21, -v17, v20, v19
	v_fmac_f32_e32 v20, v21, v18
	v_fma_f32 v17, -v17, v20, v19
	v_div_fmas_f32 v17, v17, v18, v20
	v_div_fixup_f32 v0, v17, v5, v0
	v_sub_f32_e32 v0, v0, v7
	v_bfe_u32 v5, v0, 16, 1
	v_add3_u32 v0, v0, v5, s49
	ds_write_b16_d16_hi v124, v0
	ds_read_u16 v0, v35 offset:32768
	s_waitcnt lgkmcnt(0)
	v_lshlrev_b32_e32 v17, 16, v0
	v_add_f32_e32 v7, v7, v17
	v_add_f32_e32 v5, v6, v7
	v_add_f32_e32 v0, v2, v5
	v_add_f32_e32 v2, v14, v0
	v_cvt_f32_i32_e32 v6, s12
	v_cndmask_b32_e64 v2, v2, v0, s[10:11]
	v_cndmask_b32_e64 v2, v2, v5, s[8:9]
	v_cndmask_b32_e64 v2, v2, v7, s[6:7]
	v_div_scale_f32 v14, s[12:13], v6, v6, v2
	v_rcp_f32_e32 v18, v14
	s_or_b32 s12, s15, 18
	s_min_i32 s12, s12, s28
	v_fma_f32 v19, -v14, v18, 1.0
	v_fmac_f32_e32 v18, v19, v18
	v_div_scale_f32 v19, vcc, v2, v6, v2
	v_mul_f32_e32 v20, v19, v18
	v_fma_f32 v21, -v14, v20, v19
	v_fmac_f32_e32 v20, v21, v18
	v_fma_f32 v14, -v14, v20, v19
	v_div_fmas_f32 v14, v14, v18, v20
	v_div_fixup_f32 v2, v14, v6, v2
	v_sub_f32_e32 v2, v2, v17
	v_bfe_u32 v6, v2, 16, 1
	v_add3_u32 v2, v2, v6, s49
	ds_write_b16_d16_hi v125, v2
	ds_read_u16 v2, v35 offset:33792
	s_waitcnt lgkmcnt(0)
	v_lshlrev_b32_e32 v14, 16, v2
	v_add_f32_e32 v17, v17, v14
	v_add_f32_e32 v6, v15, v17
	v_add_f32_e32 v2, v3, v6
	v_add_f32_e32 v3, v8, v2
	v_cvt_f32_i32_e32 v8, s12
	v_cndmask_b32_e64 v3, v3, v2, s[10:11]
	v_cndmask_b32_e64 v3, v3, v6, s[8:9]
	v_cndmask_b32_e64 v3, v3, v17, s[6:7]
	v_div_scale_f32 v15, s[12:13], v8, v8, v3
	v_rcp_f32_e32 v18, v15
	s_or_b32 s12, s15, 19
	s_min_i32 s12, s12, s28
	v_fma_f32 v19, -v15, v18, 1.0
	v_fmac_f32_e32 v18, v19, v18
	v_div_scale_f32 v19, vcc, v3, v8, v3
	v_mul_f32_e32 v20, v19, v18
	v_fma_f32 v21, -v15, v20, v19
	v_fmac_f32_e32 v20, v21, v18
	v_fma_f32 v15, -v15, v20, v19
	v_div_fmas_f32 v15, v15, v18, v20
	v_div_fixup_f32 v3, v15, v8, v3
	v_sub_f32_e32 v3, v3, v14
	v_bfe_u32 v8, v3, 16, 1
	v_add3_u32 v3, v3, v8, s49
	ds_write_b16_d16_hi v126, v3
	ds_read_u16 v3, v35 offset:34816
	s_waitcnt lgkmcnt(0)
; __device__ __forceinline__ unsigned f2bf(float f) { unsigned u = __builtin_bit_cast(unsigned, f); return (u + 0x7fffu + ((u >> 16) & 1u)) >> 16; }
; __device__ __forceinline__ void phase_even_mix(CArgs a, LAS unsigned char* lds, int i2, int wv, int xw  ) {
;     ...
;             const int g = wave >> 1, winw = 2 << g;
;             float pprev = 0.f, a2r[3] = {0.f, 0.f, 0.f}, a4r[5] = {0.f, 0.f, 0.f, 0.f, 0.f}, a8r[9] = {0.f, 0.f, 0.f, 0.f, 0.f, 0.f, 0.f, 0.f, 0.f};
; #pragma clang loop unroll(full)
;             for (int r = 0; r < 48; ++r) {
;                 const float p = bf2f(glu[r * 512 + c]);
;                 const float a2 = p + pprev, a4 = a2 + a2r[(r + 1) % 3], a8 = a4 + a4r[(r + 1) % 5], a16 = a8 + a8r[(r + 1) % 9];
;                 a2r[r % 3] = a2; a4r[r % 5] = a4; a8r[r % 9] = a8; pprev = p;
;                 if (r >= 16) { const float s = g == 0 ? a2 : (g == 1 ? a4 : (g == 2 ? a8 : a16));
;                     const int pos = t0 + r - 16; const float cnt = (float)((pos + 1) < winw ? (pos + 1) : winw);
;                     pl[(r - 16) * PLS + c] = (bf16)f2bf(s / cnt - p); }
;             }
;         }
	v_lshlrev_b32_e32 v8, 16, v3
	v_add_f32_e32 v14, v14, v8
	v_add_f32_e32 v7, v7, v14
	v_add_f32_e32 v3, v4, v7
	v_add_f32_e32 v4, v9, v3
	v_cvt_f32_i32_e32 v9, s12
	v_cndmask_b32_e64 v4, v4, v3, s[10:11]
	v_cndmask_b32_e64 v4, v4, v7, s[8:9]
	v_cndmask_b32_e64 v4, v4, v14, s[6:7]
	v_div_scale_f32 v15, s[12:13], v9, v9, v4
	v_rcp_f32_e32 v18, v15
	s_or_b32 s12, s15, 20
	s_min_i32 s12, s12, s28
	v_fma_f32 v19, -v15, v18, 1.0
	v_fmac_f32_e32 v18, v19, v18
	v_div_scale_f32 v19, vcc, v4, v9, v4
	v_mul_f32_e32 v20, v19, v18
	v_fma_f32 v21, -v15, v20, v19
	v_fmac_f32_e32 v20, v21, v18
	v_fma_f32 v15, -v15, v20, v19
	v_div_fmas_f32 v15, v15, v18, v20
	v_div_fixup_f32 v4, v15, v9, v4
	v_sub_f32_e32 v4, v4, v8
	v_bfe_u32 v9, v4, 16, 1
	v_add3_u32 v4, v4, v9, s49
	ds_write_b16_d16_hi v127, v4
	ds_read_u16 v4, v35 offset:35840
	s_waitcnt lgkmcnt(0)
	v_lshlrev_b32_e32 v9, 16, v4
	v_add_f32_e32 v15, v8, v9
	v_add_f32_e32 v8, v17, v15
	v_add_f32_e32 v4, v16, v8
	v_add_f32_e32 v10, v10, v4
	v_cvt_f32_i32_e32 v16, s12
	v_cndmask_b32_e64 v10, v10, v4, s[10:11]
	v_cndmask_b32_e64 v10, v10, v8, s[8:9]
	v_cndmask_b32_e64 v10, v10, v15, s[6:7]
	v_div_scale_f32 v17, s[12:13], v16, v16, v10
	v_rcp_f32_e32 v18, v17
	s_or_b32 s12, s15, 21
	s_min_i32 s12, s12, s28
	v_fma_f32 v19, -v17, v18, 1.0
	v_fmac_f32_e32 v18, v19, v18
	v_div_scale_f32 v19, vcc, v10, v16, v10
	v_mul_f32_e32 v20, v19, v18
	v_fma_f32 v21, -v17, v20, v19
	v_fmac_f32_e32 v20, v21, v18
	v_fma_f32 v17, -v17, v20, v19
	v_div_fmas_f32 v17, v17, v18, v20
	v_div_fixup_f32 v10, v17, v16, v10
	v_sub_f32_e32 v10, v10, v9
	v_bfe_u32 v16, v10, 16, 1
	v_add3_u32 v10, v10, v16, s49
	ds_write_b16_d16_hi v128, v10
	ds_read_u16 v10, v35 offset:36864
	s_waitcnt lgkmcnt(0)
	v_lshlrev_b32_e32 v10, 16, v10
	v_add_f32_e32 v16, v9, v10
	v_add_f32_e32 v9, v14, v16
	v_add_f32_e32 v5, v5, v9
	v_add_f32_e32 v11, v11, v5
	v_cvt_f32_i32_e32 v14, s12
	v_cndmask_b32_e64 v11, v11, v5, s[10:11]
	v_cndmask_b32_e64 v11, v11, v9, s[8:9]
	v_cndmask_b32_e64 v11, v11, v16, s[6:7]
	v_div_scale_f32 v17, s[12:13], v14, v14, v11
	v_rcp_f32_e32 v18, v17
	s_or_b32 s12, s15, 22
	s_min_i32 s12, s12, s28
	v_fma_f32 v19, -v17, v18, 1.0
	v_fmac_f32_e32 v18, v19, v18
	v_div_scale_f32 v19, vcc, v11, v14, v11
	v_mul_f32_e32 v20, v19, v18
	v_fma_f32 v21, -v17, v20, v19
	v_fmac_f32_e32 v20, v21, v18
	v_fma_f32 v17, -v17, v20, v19
	v_div_fmas_f32 v17, v17, v18, v20
	v_div_fixup_f32 v11, v17, v14, v11
	v_sub_f32_e32 v11, v11, v10
	v_bfe_u32 v14, v11, 16, 1
	v_add3_u32 v11, v11, v14, s49
	ds_write_b16_d16_hi v129, v11
	ds_read_u16 v11, v35 offset:37888
	s_waitcnt lgkmcnt(0)
	v_lshlrev_b32_e32 v11, 16, v11
	v_add_f32_e32 v14, v10, v11
	v_add_f32_e32 v10, v15, v14
	v_add_f32_e32 v6, v6, v10
	v_add_f32_e32 v12, v12, v6
	v_cvt_f32_i32_e32 v15, s12
	v_cndmask_b32_e64 v12, v12, v6, s[10:11]
	v_cndmask_b32_e64 v12, v12, v10, s[8:9]
	v_cndmask_b32_e64 v12, v12, v14, s[6:7]
	v_div_scale_f32 v17, s[12:13], v15, v15, v12
	v_rcp_f32_e32 v18, v17
	s_or_b32 s12, s15, 23
	s_min_i32 s12, s12, s28
	v_fma_f32 v19, -v17, v18, 1.0
	v_fmac_f32_e32 v18, v19, v18
	v_div_scale_f32 v19, vcc, v12, v15, v12
	v_mul_f32_e32 v20, v19, v18
	v_fma_f32 v21, -v17, v20, v19
	v_fmac_f32_e32 v20, v21, v18
	v_fma_f32 v17, -v17, v20, v19
	v_div_fmas_f32 v17, v17, v18, v20
	v_div_fixup_f32 v12, v17, v15, v12
	v_sub_f32_e32 v12, v12, v11
	v_bfe_u32 v15, v12, 16, 1
	v_add3_u32 v12, v12, v15, s49
	ds_write_b16_d16_hi v130, v12
	ds_read_u16 v12, v35 offset:38912
	s_waitcnt lgkmcnt(0)
	v_lshlrev_b32_e32 v15, 16, v12
	v_add_f32_e32 v12, v11, v15
	v_add_f32_e32 v11, v16, v12
	v_add_f32_e32 v7, v7, v11
	v_add_f32_e32 v13, v13, v7
	v_cvt_f32_i32_e32 v16, s12
	v_cndmask_b32_e64 v13, v13, v7, s[10:11]
	v_cndmask_b32_e64 v13, v13, v11, s[8:9]
	v_cndmask_b32_e64 v13, v13, v12, s[6:7]
	v_div_scale_f32 v17, s[12:13], v16, v16, v13
	v_rcp_f32_e32 v18, v17
	s_or_b32 s12, s15, 24
	s_min_i32 s12, s12, s28
	v_fma_f32 v19, -v17, v18, 1.0
	v_fmac_f32_e32 v18, v19, v18
	v_div_scale_f32 v19, vcc, v13, v16, v13
	v_mul_f32_e32 v20, v19, v18
	v_fma_f32 v21, -v17, v20, v19
	v_fmac_f32_e32 v20, v21, v18
	v_fma_f32 v17, -v17, v20, v19
	v_div_fmas_f32 v17, v17, v18, v20
	v_div_fixup_f32 v13, v17, v16, v13
	v_sub_f32_e32 v13, v13, v15
	v_bfe_u32 v16, v13, 16, 1
	v_add3_u32 v13, v13, v16, s49
	ds_write_b16_d16_hi v131, v13
	ds_read_u16 v13, v35 offset:39936
	v_cvt_f32_i32_e32 v16, s12
	s_waitcnt lgkmcnt(0)
	v_lshlrev_b32_e32 v13, 16, v13
	v_add_f32_e32 v15, v15, v13
	v_add_f32_e32 v14, v14, v15
	v_add_f32_e32 v8, v8, v14
	v_add_f32_e32 v1, v1, v8
	v_cndmask_b32_e64 v1, v1, v8, s[10:11]
	v_cndmask_b32_e64 v1, v1, v14, s[8:9]
	v_cndmask_b32_e64 v1, v1, v15, s[6:7]
	v_div_scale_f32 v17, s[12:13], v16, v16, v1
	v_rcp_f32_e32 v18, v17
	s_or_b32 s12, s15, 25
	s_min_i32 s12, s12, s28
	v_fma_f32 v19, -v17, v18, 1.0
	v_fmac_f32_e32 v18, v19, v18
	v_div_scale_f32 v19, vcc, v1, v16, v1
	v_mul_f32_e32 v20, v19, v18
	v_fma_f32 v21, -v17, v20, v19
	v_fmac_f32_e32 v20, v21, v18
	v_fma_f32 v17, -v17, v20, v19
	v_div_fmas_f32 v17, v17, v18, v20
	v_div_fixup_f32 v1, v17, v16, v1
	v_sub_f32_e32 v1, v1, v13
	v_bfe_u32 v16, v1, 16, 1
	v_add3_u32 v1, v1, v16, s49
	ds_write_b16_d16_hi v132, v1
	ds_read_u16 v1, v35 offset:40960
	s_waitcnt lgkmcnt(0)
; __device__ __forceinline__ unsigned f2bf(float f) { unsigned u = __builtin_bit_cast(unsigned, f); return (u + 0x7fffu + ((u >> 16) & 1u)) >> 16; }
; __device__ __forceinline__ void phase_even_mix(CArgs a, LAS unsigned char* lds, int i2, int wv, int xw  ) {
;     ...
;             const int g = wave >> 1, winw = 2 << g;
;             float pprev = 0.f, a2r[3] = {0.f, 0.f, 0.f}, a4r[5] = {0.f, 0.f, 0.f, 0.f, 0.f}, a8r[9] = {0.f, 0.f, 0.f, 0.f, 0.f, 0.f, 0.f, 0.f, 0.f};
; #pragma clang loop unroll(full)
;             for (int r = 0; r < 48; ++r) {
;                 const float p = bf2f(glu[r * 512 + c]);
;                 const float a2 = p + pprev, a4 = a2 + a2r[(r + 1) % 3], a8 = a4 + a4r[(r + 1) % 5], a16 = a8 + a8r[(r + 1) % 9];
;                 a2r[r % 3] = a2; a4r[r % 5] = a4; a8r[r % 9] = a8; pprev = p;
;                 if (r >= 16) { const float s = g == 0 ? a2 : (g == 1 ? a4 : (g == 2 ? a8 : a16));
;                     const int pos = t0 + r - 16; const float cnt = (float)((pos + 1) < winw ? (pos + 1) : winw);
;                     pl[(r - 16) * PLS + c] = (bf16)f2bf(s / cnt - p); }
;             }
;         }
;         __syncthreads();
	v_lshlrev_b32_e32 v16, 16, v1
	v_add_f32_e32 v13, v13, v16
	v_add_f32_e32 v1, v12, v13
	v_add_f32_e32 v9, v9, v1
	v_add_f32_e32 v0, v0, v9
	v_cndmask_b32_e64 v0, v0, v9, s[10:11]
	v_cvt_f32_i32_e32 v9, s12
	v_cndmask_b32_e64 v0, v0, v1, s[8:9]
	v_cndmask_b32_e64 v0, v0, v13, s[6:7]
	v_div_scale_f32 v12, s[12:13], v9, v9, v0
	v_rcp_f32_e32 v17, v12
	s_or_b32 s12, s15, 26
	s_min_i32 s12, s12, s28
	v_fma_f32 v18, -v12, v17, 1.0
	v_fmac_f32_e32 v17, v18, v17
	v_div_scale_f32 v18, vcc, v0, v9, v0
	v_mul_f32_e32 v19, v18, v17
	v_fma_f32 v20, -v12, v19, v18
	v_fmac_f32_e32 v19, v20, v17
	v_fma_f32 v12, -v12, v19, v18
	v_div_fmas_f32 v12, v12, v17, v19
	v_div_fixup_f32 v0, v12, v9, v0
	v_sub_f32_e32 v0, v0, v16
	v_bfe_u32 v9, v0, 16, 1
	v_add3_u32 v0, v0, v9, s49
	ds_write_b16_d16_hi v133, v0
	ds_read_u16 v0, v35 offset:41984
	s_waitcnt lgkmcnt(0)
	v_lshlrev_b32_e32 v0, 16, v0
	v_add_f32_e32 v12, v16, v0
	v_add_f32_e32 v9, v15, v12
	v_add_f32_e32 v10, v10, v9
	v_add_f32_e32 v2, v2, v10
	v_cndmask_b32_e64 v2, v2, v10, s[10:11]
	v_cvt_f32_i32_e32 v10, s12
	v_cndmask_b32_e64 v2, v2, v9, s[8:9]
	v_cndmask_b32_e64 v2, v2, v12, s[6:7]
	v_div_scale_f32 v15, s[12:13], v10, v10, v2
	v_rcp_f32_e32 v16, v15
	s_or_b32 s12, s15, 27
	s_min_i32 s12, s12, s28
	v_fma_f32 v17, -v15, v16, 1.0
	v_fmac_f32_e32 v16, v17, v16
	v_div_scale_f32 v17, vcc, v2, v10, v2
	v_mul_f32_e32 v18, v17, v16
	v_fma_f32 v19, -v15, v18, v17
	v_fmac_f32_e32 v18, v19, v16
	v_fma_f32 v15, -v15, v18, v17
	v_div_fmas_f32 v15, v15, v16, v18
	v_div_fixup_f32 v2, v15, v10, v2
	v_sub_f32_e32 v2, v2, v0
	v_bfe_u32 v10, v2, 16, 1
	v_add3_u32 v2, v2, v10, s49
	ds_write_b16_d16_hi v134, v2
	ds_read_u16 v2, v35 offset:43008
	s_waitcnt lgkmcnt(0)
	v_lshlrev_b32_e32 v2, 16, v2
	v_add_f32_e32 v15, v0, v2
	v_add_f32_e32 v10, v13, v15
	v_add_f32_e32 v0, v11, v10
	v_add_f32_e32 v3, v3, v0
	v_cndmask_b32_e64 v0, v3, v0, s[10:11]
	v_cvt_f32_i32_e32 v3, s12
	v_cndmask_b32_e64 v0, v0, v10, s[8:9]
	v_cndmask_b32_e64 v0, v0, v15, s[6:7]
	v_div_scale_f32 v11, s[12:13], v3, v3, v0
	v_rcp_f32_e32 v13, v11
	s_or_b32 s12, s15, 28
	s_min_i32 s12, s12, s28
	v_fma_f32 v16, -v11, v13, 1.0
	v_fmac_f32_e32 v13, v16, v13
	v_div_scale_f32 v16, vcc, v0, v3, v0
	v_mul_f32_e32 v17, v16, v13
	v_fma_f32 v18, -v11, v17, v16
	v_fmac_f32_e32 v17, v18, v13
	v_fma_f32 v11, -v11, v17, v16
	v_div_fmas_f32 v11, v11, v13, v17
	v_div_fixup_f32 v0, v11, v3, v0
	v_sub_f32_e32 v0, v0, v2
	v_bfe_u32 v3, v0, 16, 1
	v_add3_u32 v0, v0, v3, s49
	ds_write_b16_d16_hi v135, v0
	ds_read_u16 v0, v35 offset:44032
	s_waitcnt lgkmcnt(0)
	v_lshlrev_b32_e32 v3, 16, v0
	v_add_f32_e32 v2, v2, v3
	v_add_f32_e32 v0, v12, v2
	v_add_f32_e32 v11, v14, v0
	v_add_f32_e32 v4, v4, v11
	v_cndmask_b32_e64 v4, v4, v11, s[10:11]
	v_cvt_f32_i32_e32 v11, s12
	v_cndmask_b32_e64 v4, v4, v0, s[8:9]
	v_cndmask_b32_e64 v4, v4, v2, s[6:7]
	v_div_scale_f32 v12, s[12:13], v11, v11, v4
	v_rcp_f32_e32 v13, v12
	s_or_b32 s12, s15, 29
	s_min_i32 s12, s12, s28
	v_fma_f32 v14, -v12, v13, 1.0
	v_fmac_f32_e32 v13, v14, v13
	v_div_scale_f32 v14, vcc, v4, v11, v4
	v_mul_f32_e32 v16, v14, v13
	v_fma_f32 v17, -v12, v16, v14
	v_fmac_f32_e32 v16, v17, v13
	v_fma_f32 v12, -v12, v16, v14
	v_div_fmas_f32 v12, v12, v13, v16
	v_div_fixup_f32 v4, v12, v11, v4
	v_sub_f32_e32 v4, v4, v3
	v_bfe_u32 v11, v4, 16, 1
	v_add3_u32 v4, v4, v11, s49
	ds_write_b16_d16_hi v136, v4
	ds_read_u16 v4, v35 offset:45056
	s_waitcnt lgkmcnt(0)
	v_lshlrev_b32_e32 v4, 16, v4
	v_add_f32_e32 v3, v3, v4
	v_add_f32_e32 v11, v15, v3
	v_add_f32_e32 v1, v1, v11
	v_add_f32_e32 v5, v5, v1
	v_cndmask_b32_e64 v1, v5, v1, s[10:11]
	v_cvt_f32_i32_e32 v5, s12
	v_cndmask_b32_e64 v1, v1, v11, s[8:9]
	v_cndmask_b32_e64 v1, v1, v3, s[6:7]
	v_div_scale_f32 v11, s[12:13], v5, v5, v1
	v_rcp_f32_e32 v12, v11
	s_or_b32 s12, s15, 30
	s_min_i32 s12, s12, s28
	v_fma_f32 v13, -v11, v12, 1.0
	v_fmac_f32_e32 v12, v13, v12
	v_div_scale_f32 v13, vcc, v1, v5, v1
	v_mul_f32_e32 v14, v13, v12
	v_fma_f32 v15, -v11, v14, v13
	v_fmac_f32_e32 v14, v15, v12
	v_fma_f32 v11, -v11, v14, v13
	v_div_fmas_f32 v11, v11, v12, v14
	v_div_fixup_f32 v1, v11, v5, v1
	v_sub_f32_e32 v1, v1, v4
	v_bfe_u32 v5, v1, 16, 1
	v_add3_u32 v1, v1, v5, s49
	ds_write_b16_d16_hi v137, v1
	ds_read_u16 v1, v35 offset:46080
	s_waitcnt lgkmcnt(0)
	v_lshlrev_b32_e32 v5, 16, v1
	v_add_f32_e32 v1, v4, v5
	v_add_f32_e32 v2, v2, v1
	v_add_f32_e32 v4, v9, v2
	v_add_f32_e32 v6, v6, v4
	v_cndmask_b32_e64 v4, v6, v4, s[10:11]
	v_cndmask_b32_e64 v2, v4, v2, s[8:9]
	v_cvt_f32_i32_e32 v4, s12
	v_cndmask_b32_e64 v2, v2, v1, s[6:7]
	v_div_scale_f32 v6, s[12:13], v4, v4, v2
	v_rcp_f32_e32 v9, v6
	s_or_b32 s12, s15, 31
	s_min_i32 s12, s12, s28
	s_add_i32 s15, s15, 32
	v_fma_f32 v11, -v6, v9, 1.0
	v_fmac_f32_e32 v9, v11, v9
	v_div_scale_f32 v11, vcc, v2, v4, v2
	v_mul_f32_e32 v12, v11, v9
	v_fma_f32 v13, -v6, v12, v11
	v_fmac_f32_e32 v12, v13, v9
	v_fma_f32 v6, -v6, v12, v11
	v_div_fmas_f32 v6, v6, v9, v12
	v_div_fixup_f32 v2, v6, v4, v2
	v_sub_f32_e32 v2, v2, v5
	v_bfe_u32 v4, v2, 16, 1
	v_add3_u32 v2, v2, v4, s49
	ds_write_b16_d16_hi v138, v2
	ds_read_u16 v2, v35 offset:47104
	s_waitcnt lgkmcnt(0)
	v_lshlrev_b32_e32 v2, 16, v2
	v_add_f32_e32 v4, v5, v2
	v_add_f32_e32 v3, v3, v4
	v_add_f32_e32 v5, v10, v3
	v_add_f32_e32 v6, v7, v5
	v_cndmask_b32_e64 v5, v6, v5, s[10:11]
	v_cndmask_b32_e64 v3, v5, v3, s[8:9]
	v_cndmask_b32_e64 v3, v3, v4, s[6:7]
	v_cvt_f32_i32_e32 v4, s12
	v_div_scale_f32 v5, s[12:13], v4, v4, v3
	v_rcp_f32_e32 v6, v5
	s_min_i32 s12, s15, s28
	v_fma_f32 v7, -v5, v6, 1.0
	v_fmac_f32_e32 v6, v7, v6
	v_div_scale_f32 v7, vcc, v3, v4, v3
	v_mul_f32_e32 v9, v7, v6
	v_fma_f32 v10, -v5, v9, v7
	v_fmac_f32_e32 v9, v10, v6
	v_fma_f32 v5, -v5, v9, v7
	v_div_fmas_f32 v5, v5, v6, v9
	v_div_fixup_f32 v3, v5, v4, v3
	v_sub_f32_e32 v3, v3, v2
	v_bfe_u32 v4, v3, 16, 1
	v_add3_u32 v3, v3, v4, s49
	ds_write_b16_d16_hi v139, v3
	ds_read_u16 v3, v35 offset:48128
	s_waitcnt lgkmcnt(0)
	v_lshlrev_b32_e32 v3, 16, v3
	v_add_f32_e32 v2, v2, v3
	v_add_f32_e32 v1, v1, v2
	v_add_f32_e32 v0, v0, v1
	v_add_f32_e32 v4, v8, v0
	v_cndmask_b32_e64 v0, v4, v0, s[10:11]
	v_cndmask_b32_e64 v0, v0, v1, s[8:9]
	v_cvt_f32_i32_e32 v1, s12
	v_cndmask_b32_e64 v0, v0, v2, s[6:7]
	v_div_scale_f32 v2, s[12:13], v1, v1, v0
	v_rcp_f32_e32 v4, v2
	s_lshl_b64 s[12:13], s[94:95], 2
	s_add_u32 s12, s16, s12
	s_addc_u32 s13, s17, s13
	v_fma_f32 v5, -v2, v4, 1.0
	v_fmac_f32_e32 v4, v5, v4
	v_div_scale_f32 v5, vcc, v0, v1, v0
	v_mul_f32_e32 v6, v5, v4
	v_fma_f32 v7, -v2, v6, v5
	v_fmac_f32_e32 v6, v7, v4
	v_fma_f32 v2, -v2, v6, v5
	v_div_fmas_f32 v2, v2, v4, v6
	v_div_fixup_f32 v0, v2, v1, v0
	v_sub_f32_e32 v0, v0, v3
	v_bfe_u32 v1, v0, 16, 1
	v_add3_u32 v0, v0, v1, s49
	ds_write_b16_d16_hi v140, v0
	s_waitcnt lgkmcnt(0)
	s_barrier
; #define LAS __attribute__((address_space(3)))
; __device__ __forceinline__ unsigned pk2(float lo, float hi) { unsigned r; asm("v_cvt_pk_bf16_f32 %0, %1, %2" : "=v"(r) : "v"(lo), "v"(hi)); return r; }
; __device__ __forceinline__ void phase_even_mix(CArgs a, LAS unsigned char* lds, int i2, int wv, int xw  ) {
;     ...
;         {
;             const int g = wave >> 1, nh = wave & 1, fr = lane & 15, fq = lane >> 4;
;             const bf16* wp = (const bf16*)(a->ws + WS_WPOOL) + ((size_t)i2 * 4 + g) * 128 * 128;
;             f32x4 acc[2][4];
; #pragma unroll
;             for (int m = 0; m < 2; ++m)
; #pragma unroll
;                 for (int n = 0; n < 4; ++n) acc[m][n] = (f32x4){0.f, 0.f, 0.f, 0.f};
; #pragma unroll
;             for (int ks = 0; ks < 4; ++ks) {
;                 bf16x8 af[2], bfr[4];
; #pragma unroll
;                 for (int m = 0; m < 2; ++m) af[m] = *(const LAS bf16x8*)(pl + (m * 16 + fr) * PLS + g * 128 + ks * 32 + fq * 8);
; #pragma unroll
;                 for (int n = 0; n < 4; ++n) bfr[n] = *(const bf16x8*)(wp + (size_t)(nh * 64 + n * 16 + fr) * 128 + ks * 32 + fq * 8);
; #pragma unroll
;                 for (int m = 0; m < 2; ++m)
; #pragma unroll
;                     for (int n = 0; n < 4; ++n) acc[m][n] = __builtin_amdgcn_mfma_f32_16x16x32_bf16(bfr[n], af[m], acc[m][n], 0, 0, 0);
;             }
; #pragma unroll
;             for (int n = 0; n < 4; ++n) { const int d = nh * 64 + n * 16 + 4 * fq;
;                 const f32x4 pb = *(const f32x4*)(a->in[I_POOLB] + ((size_t)i2 * 4 + g) * 128 + d), ps = *(const f32x4*)(a->in[I_POOLS] + (size_t)i2 * 512 + g * 128 + d);
; #pragma unroll
;                 for (int m = 0; m < 2; ++m) { const f32x4 v = (acc[m][n] + pb) * ps; u32x2 wv2; wv2.x = pk2(v.x, v.y); wv2.y = pk2(v.z, v.w);
;                     *(u32x2*)(YB + (tokbase + m * 16 + fr) * DM + g * 128 + d) = wv2; } }
;         }
;         __syncthreads();
	ds_read_b128 v[0:3], v144
	ds_read_b128 v[4:7], v144 offset:16640
	global_load_dwordx4 v[8:11], v[36:37], off
	global_load_dwordx4 v[12:15], v[38:39], off
	global_load_dwordx4 v[16:19], v[40:41], off
	global_load_dwordx4 v[20:23], v[42:43], off
	s_waitcnt vmcnt(3) lgkmcnt(1)
	v_mfma_f32_16x16x32_bf16 v[154:157], v[8:11], v[0:3], 0
	s_add_u32 s15, s18, s96
	s_addc_u32 s17, s19, s97
	s_add_u32 s16, s15, s58
	s_waitcnt vmcnt(2)
	v_mfma_f32_16x16x32_bf16 v[158:161], v[12:15], v[0:3], 0
	s_addc_u32 s17, s17, s59
	s_andn2_b64 vcc, exec, s[68:69]
	s_waitcnt vmcnt(1)
	v_mfma_f32_16x16x32_bf16 v[162:165], v[16:19], v[0:3], 0
	s_waitcnt vmcnt(0)
	v_mfma_f32_16x16x32_bf16 v[0:3], v[20:23], v[0:3], 0
	s_waitcnt lgkmcnt(0)
	v_mfma_f32_16x16x32_bf16 v[8:11], v[8:11], v[4:7], 0
	v_mfma_f32_16x16x32_bf16 v[12:15], v[12:15], v[4:7], 0
	v_mfma_f32_16x16x32_bf16 v[16:19], v[16:19], v[4:7], 0
	v_mfma_f32_16x16x32_bf16 v[4:7], v[20:23], v[4:7], 0
	ds_read_b128 v[20:23], v144 offset:64
	ds_read_b128 v[166:169], v144 offset:16704
	global_load_dwordx4 v[170:173], v[36:37], off offset:64
	global_load_dwordx4 v[174:177], v[44:45], off
	global_load_dwordx4 v[192:195], v[46:47], off
	global_load_dwordx4 v[196:199], v[48:49], off
	s_waitcnt vmcnt(3) lgkmcnt(1)
	v_mfma_f32_16x16x32_bf16 v[154:157], v[170:173], v[20:23], v[154:157]
	s_waitcnt vmcnt(2)
	v_mfma_f32_16x16x32_bf16 v[158:161], v[174:177], v[20:23], v[158:161]
	s_waitcnt vmcnt(1)
	v_mfma_f32_16x16x32_bf16 v[162:165], v[192:195], v[20:23], v[162:165]
	s_waitcnt vmcnt(0)
	v_mfma_f32_16x16x32_bf16 v[0:3], v[196:199], v[20:23], v[0:3]
	s_waitcnt lgkmcnt(0)
	v_mfma_f32_16x16x32_bf16 v[8:11], v[170:173], v[166:169], v[8:11]
	v_mfma_f32_16x16x32_bf16 v[12:15], v[174:177], v[166:169], v[12:15]
	v_mfma_f32_16x16x32_bf16 v[16:19], v[192:195], v[166:169], v[16:19]
	v_mfma_f32_16x16x32_bf16 v[4:7], v[196:199], v[166:169], v[4:7]
	ds_read_b128 v[20:23], v144 offset:128
	ds_read_b128 v[166:169], v144 offset:16768
	global_load_dwordx4 v[170:173], v[36:37], off offset:128
	global_load_dwordx4 v[174:177], v[50:51], off
	global_load_dwordx4 v[192:195], v[52:53], off
	global_load_dwordx4 v[196:199], v[54:55], off
	s_waitcnt vmcnt(3) lgkmcnt(1)
	v_mfma_f32_16x16x32_bf16 v[154:157], v[170:173], v[20:23], v[154:157]
	s_waitcnt vmcnt(2)
	v_mfma_f32_16x16x32_bf16 v[158:161], v[174:177], v[20:23], v[158:161]
	s_waitcnt vmcnt(1)
	v_mfma_f32_16x16x32_bf16 v[162:165], v[192:195], v[20:23], v[162:165]
	s_waitcnt vmcnt(0)
	v_mfma_f32_16x16x32_bf16 v[0:3], v[196:199], v[20:23], v[0:3]
	s_waitcnt lgkmcnt(0)
	v_mfma_f32_16x16x32_bf16 v[8:11], v[170:173], v[166:169], v[8:11]
	v_mfma_f32_16x16x32_bf16 v[12:15], v[174:177], v[166:169], v[12:15]
	v_mfma_f32_16x16x32_bf16 v[16:19], v[192:195], v[166:169], v[16:19]
	v_mfma_f32_16x16x32_bf16 v[4:7], v[196:199], v[166:169], v[4:7]
	ds_read_b128 v[20:23], v144 offset:192
	ds_read_b128 v[166:169], v144 offset:16832
	global_load_dwordx4 v[170:173], v[36:37], off offset:192
	global_load_dwordx4 v[174:177], v[56:57], off
	global_load_dwordx4 v[192:195], v[58:59], off
	global_load_dwordx4 v[196:199], v[60:61], off
	s_waitcnt vmcnt(3) lgkmcnt(1)
	v_mfma_f32_16x16x32_bf16 v[154:157], v[170:173], v[20:23], v[154:157]
	s_waitcnt vmcnt(2)
	v_mfma_f32_16x16x32_bf16 v[158:161], v[174:177], v[20:23], v[158:161]
	s_waitcnt vmcnt(1)
	v_mfma_f32_16x16x32_bf16 v[162:165], v[192:195], v[20:23], v[162:165]
	s_waitcnt vmcnt(0)
	v_mfma_f32_16x16x32_bf16 v[20:23], v[196:199], v[20:23], v[0:3]
	s_waitcnt lgkmcnt(0)
	v_mfma_f32_16x16x32_bf16 v[8:11], v[170:173], v[166:169], v[8:11]
	v_mfma_f32_16x16x32_bf16 v[12:15], v[174:177], v[166:169], v[12:15]
	v_mfma_f32_16x16x32_bf16 v[16:19], v[192:195], v[166:169], v[16:19]
	v_mfma_f32_16x16x32_bf16 v[0:3], v[196:199], v[166:169], v[4:7]
	s_nop 2
	global_load_dwordx4 v[4:7], v145, s[12:13]
	global_load_dwordx4 v[166:169], v145, s[16:17]
	s_waitcnt vmcnt(1)
	v_pk_add_f32 v[156:157], v[156:157], v[6:7]
	v_pk_add_f32 v[154:155], v[154:155], v[4:5]
	s_waitcnt vmcnt(0)
	v_pk_mul_f32 v[156:157], v[168:169], v[156:157]
	v_pk_mul_f32 v[154:155], v[166:167], v[154:155]
	v_pk_add_f32 v[6:7], v[10:11], v[6:7]
	v_pk_add_f32 v[4:5], v[8:9], v[4:5]
	v_cvt_pk_bf16_f32 v154, v154, v155
	v_cvt_pk_bf16_f32 v155, v156, v157
	v_mov_b32_e32 v157, s23
	v_or_b32_e32 v156, s22, v28
	v_pk_mul_f32 v[6:7], v[168:169], v[6:7]
	v_pk_mul_f32 v[4:5], v[166:167], v[4:5]
	v_lshlrev_b64 v[156:157], 11, v[156:157]
	v_cvt_pk_bf16_f32 v4, v4, v5
	v_cvt_pk_bf16_f32 v5, v6, v7
	v_mov_b32_e32 v7, s23
	v_or_b32_e32 v6, s22, v34
	v_lshl_add_u64 v[156:157], v[30:31], 0, v[156:157]
	v_lshlrev_b64 v[6:7], 11, v[6:7]
	global_store_dwordx2 v[156:157], v[154:155], off
	v_lshl_add_u64 v[154:155], v[30:31], 0, v[6:7]
	global_store_dwordx2 v[154:155], v[4:5], off
	global_load_dwordx4 v[4:7], v145, s[12:13] offset:64
	s_nop 0
	global_load_dwordx4 v[8:11], v145, s[16:17] offset:64
	s_waitcnt vmcnt(1)
	v_pk_add_f32 v[158:159], v[158:159], v[4:5]
	v_pk_add_f32 v[4:5], v[12:13], v[4:5]
	v_pk_add_f32 v[160:161], v[160:161], v[6:7]
	s_waitcnt vmcnt(0)
	v_pk_mul_f32 v[158:159], v[8:9], v[158:159]
	v_pk_add_f32 v[6:7], v[14:15], v[6:7]
	v_pk_mul_f32 v[4:5], v[8:9], v[4:5]
	v_pk_mul_f32 v[160:161], v[10:11], v[160:161]
	v_cvt_pk_bf16_f32 v158, v158, v159
	v_pk_mul_f32 v[6:7], v[10:11], v[6:7]
	v_cvt_pk_bf16_f32 v159, v160, v161
	global_store_dwordx2 v[156:157], v[158:159], off offset:32
	v_cvt_pk_bf16_f32 v4, v4, v5
	v_cvt_pk_bf16_f32 v5, v6, v7
	global_store_dwordx2 v[154:155], v[4:5], off offset:32
	global_load_dwordx4 v[4:7], v145, s[12:13] offset:128
	s_nop 0
	global_load_dwordx4 v[8:11], v145, s[16:17] offset:128
	s_waitcnt vmcnt(1)
	v_pk_add_f32 v[14:15], v[162:163], v[4:5]
	v_pk_add_f32 v[4:5], v[16:17], v[4:5]
	v_pk_add_f32 v[12:13], v[164:165], v[6:7]
	s_waitcnt vmcnt(0)
	v_pk_mul_f32 v[14:15], v[8:9], v[14:15]
	v_pk_add_f32 v[6:7], v[18:19], v[6:7]
	v_pk_mul_f32 v[4:5], v[8:9], v[4:5]
	v_pk_mul_f32 v[12:13], v[10:11], v[12:13]
	v_cvt_pk_bf16_f32 v14, v14, v15
	v_pk_mul_f32 v[6:7], v[10:11], v[6:7]
	v_cvt_pk_bf16_f32 v15, v12, v13
	global_store_dwordx2 v[156:157], v[14:15], off offset:64
	v_cvt_pk_bf16_f32 v4, v4, v5
	v_cvt_pk_bf16_f32 v5, v6, v7
	global_store_dwordx2 v[154:155], v[4:5], off offset:64
	global_load_dwordx4 v[4:7], v145, s[12:13] offset:192
	s_nop 0
	global_load_dwordx4 v[8:11], v145, s[16:17] offset:192
	s_mov_b64 s[12:13], 0
	s_waitcnt vmcnt(1)
	v_pk_add_f32 v[14:15], v[20:21], v[4:5]
	v_pk_add_f32 v[0:1], v[0:1], v[4:5]
	v_pk_add_f32 v[12:13], v[22:23], v[6:7]
	s_waitcnt vmcnt(0)
	v_pk_mul_f32 v[14:15], v[8:9], v[14:15]
	v_pk_add_f32 v[2:3], v[2:3], v[6:7]
	v_pk_mul_f32 v[0:1], v[8:9], v[0:1]
	v_pk_mul_f32 v[12:13], v[10:11], v[12:13]
	v_cvt_pk_bf16_f32 v14, v14, v15
	v_pk_mul_f32 v[2:3], v[10:11], v[2:3]
	v_cvt_pk_bf16_f32 v15, v12, v13
	global_store_dwordx2 v[156:157], v[14:15], off offset:96
	v_cvt_pk_bf16_f32 v0, v0, v1
	v_cvt_pk_bf16_f32 v1, v2, v3
	global_store_dwordx2 v[154:155], v[0:1], off offset:96
	s_barrier
	s_cbranch_vccz .LBB0_489
; #define LAS __attribute__((address_space(3)))
; __device__ __forceinline__ unsigned pk2(float lo, float hi) { unsigned r; asm("v_cvt_pk_bf16_f32 %0, %1, %2" : "=v"(r) : "v"(lo), "v"(hi)); return r; }
; __device__ __forceinline__ float sigmoidf_(float x) { return __builtin_amdgcn_rcpf(1.0f + __builtin_amdgcn_exp2f(x * -1.44269504089f)); }
; __device__ __forceinline__ void phase_even_mix(CArgs a, LAS unsigned char* lds, int i2, int wv, int xw  ) {
;     ...
;     for (int kk = 0; kk < 2; ++kk) { const int chunk = 64 * (xw >> 5) + (xw & 31) + 32 * kk; (void)G;
;         const int b = chunk >> 6, t0 = (chunk & 63) * 32; const size_t tokbase = (size_t)chunk * 32;
; #pragma unroll
;         for (int it = 0; it < 8; ++it) { const int item = it * NTHR + tid, tt = item >> 6, cg = item & 63, p = t0 - 32 + tt;
;             u32x4 o = (u32x4){0u, 0u, 0u, 0u};
;             if (p >= 0) { const bf16* hp = HB + ((size_t)b * SEQ + p) * EVEN_IN + cg * 8; const u32x4 ra = *(const u32x4*)(hp + 512), rg = *(const u32x4*)(hp + 1024);
;                 o.x = pk2(bflo(ra.x) * sigmoidf_(bflo(rg.x)), bfhi(ra.x) * sigmoidf_(bfhi(rg.x))); o.y = pk2(bflo(ra.y) * sigmoidf_(bflo(rg.y)), bfhi(ra.y) * sigmoidf_(bfhi(rg.y)));
;                 o.z = pk2(bflo(ra.z) * sigmoidf_(bflo(rg.z)), bfhi(ra.z) * sigmoidf_(bfhi(rg.z))); o.w = pk2(bflo(ra.w) * sigmoidf_(bflo(rg.w)), bfhi(ra.w) * sigmoidf_(bfhi(rg.w))); }
;             *(LAS u32x4*)(glu + tt * 512 + cg * 8) = o; }
.LBB0_461:
	v_readlane_b32 s15, v254, 30
	s_or_b32 s18, s64, s15
	s_lshl_b32 s15, s18, 5
	s_sub_i32 s19, s15, 32
	v_add_u32_e32 v152, s19, v69
	v_cmp_lt_i32_e32 vcc, -1, v152
	v_mov_b64_e32 v[208:209], 0
	v_mov_b64_e32 v[210:211], 0
	v_mov_b64_e32 v[212:213], 0
	v_mov_b64_e32 v[214:215], 0
	s_and_saveexec_b64 s[16:17], vcc
	s_cbranch_execz .Le2st_skip0
	v_lshl_add_u64 v[248:249], s[92:93], 0, v[152:153]
	v_mad_u64_u32 v[250:251], s[22:23], v248, s53, v[24:25]
	v_mad_i32_i24 v251, v249, s53, v251
	global_load_dwordx4 v[208:211], v[250:251], off offset:1024
	global_load_dwordx4 v[212:215], v[250:251], off offset:2048
.Le2st_skip0:
	s_or_b64 exec, exec, s[16:17]
	v_add_u32_e32 v152, s19, v70
	v_cmp_lt_i32_e32 vcc, -1, v152
	v_mov_b64_e32 v[216:217], 0
	v_mov_b64_e32 v[218:219], 0
	v_mov_b64_e32 v[220:221], 0
	v_mov_b64_e32 v[222:223], 0
	s_and_saveexec_b64 s[16:17], vcc
	s_cbranch_execz .Le2st_skip1
	v_lshl_add_u64 v[248:249], s[92:93], 0, v[152:153]
	v_mad_u64_u32 v[250:251], s[22:23], v248, s53, v[24:25]
	v_mad_i32_i24 v251, v249, s53, v251
	global_load_dwordx4 v[216:219], v[250:251], off offset:1024
	global_load_dwordx4 v[220:223], v[250:251], off offset:2048
.Le2st_skip1:
	s_or_b64 exec, exec, s[16:17]
	v_add_u32_e32 v152, s19, v71
	v_cmp_lt_i32_e32 vcc, -1, v152
	v_mov_b64_e32 v[224:225], 0
	v_mov_b64_e32 v[226:227], 0
	v_mov_b64_e32 v[228:229], 0
	v_mov_b64_e32 v[230:231], 0
	s_and_saveexec_b64 s[16:17], vcc
	s_cbranch_execz .Le2st_skip2
	v_lshl_add_u64 v[248:249], s[92:93], 0, v[152:153]
	v_mad_u64_u32 v[250:251], s[22:23], v248, s53, v[24:25]
	v_mad_i32_i24 v251, v249, s53, v251
	global_load_dwordx4 v[224:227], v[250:251], off offset:1024
	global_load_dwordx4 v[228:231], v[250:251], off offset:2048
.Le2st_skip2:
	s_or_b64 exec, exec, s[16:17]
	v_add_u32_e32 v152, s19, v72
	v_cmp_lt_i32_e32 vcc, -1, v152
	v_mov_b64_e32 v[232:233], 0
	v_mov_b64_e32 v[234:235], 0
	v_mov_b64_e32 v[236:237], 0
	v_mov_b64_e32 v[238:239], 0
	s_and_saveexec_b64 s[16:17], vcc
	s_cbranch_execz .Le2st_skip3
	v_lshl_add_u64 v[248:249], s[92:93], 0, v[152:153]
	v_mad_u64_u32 v[250:251], s[22:23], v248, s53, v[24:25]
	v_mad_i32_i24 v251, v249, s53, v251
	global_load_dwordx4 v[232:235], v[250:251], off offset:1024
	global_load_dwordx4 v[236:239], v[250:251], off offset:2048
.Le2st_skip3:
	s_or_b64 exec, exec, s[16:17]
	v_add_u32_e32 v152, s19, v73
	v_cmp_lt_i32_e32 vcc, -1, v152
	v_mov_b64_e32 v[240:241], 0
	v_mov_b64_e32 v[242:243], 0
	v_mov_b64_e32 v[244:245], 0
	v_mov_b64_e32 v[246:247], 0
	s_and_saveexec_b64 s[16:17], vcc
	s_cbranch_execz .Le2st_skip4
	v_lshl_add_u64 v[248:249], s[92:93], 0, v[152:153]
	v_mad_u64_u32 v[250:251], s[22:23], v248, s53, v[24:25]
	v_mad_i32_i24 v251, v249, s53, v251
	global_load_dwordx4 v[240:243], v[250:251], off offset:1024
	global_load_dwordx4 v[244:247], v[250:251], off offset:2048
.Le2st_skip4:
	s_or_b64 exec, exec, s[16:17]
	s_waitcnt vmcnt(8)
	v_lshlrev_b32_e32 v1, 16, v208
	v_lshlrev_b32_e32 v10, 16, v212
	v_and_b32_e32 v212, 0xffff0000, v212
	v_lshlrev_b32_e32 v12, 16, v213
	v_and_b32_e32 v213, 0xffff0000, v213
	v_lshlrev_b32_e32 v14, 16, v214
	v_and_b32_e32 v214, 0xffff0000, v214
	v_lshlrev_b32_e32 v16, 16, v215
	v_and_b32_e32 v215, 0xffff0000, v215
	v_mul_f32_e32 v212, 0xbfb8aa3b, v212
	v_mul_f32_e32 v213, 0xbfb8aa3b, v213
	v_mul_f32_e32 v214, 0xbfb8aa3b, v214
	v_mul_f32_e32 v215, 0xbfb8aa3b, v215
	v_mul_f32_e32 v10, 0xbfb8aa3b, v10
	v_mul_f32_e32 v12, 0xbfb8aa3b, v12
	v_mul_f32_e32 v14, 0xbfb8aa3b, v14
	v_mul_f32_e32 v16, 0xbfb8aa3b, v16
	v_exp_f32_e32 v212, v212
	v_exp_f32_e32 v213, v213
	v_exp_f32_e32 v214, v214
	v_exp_f32_e32 v215, v215
	v_exp_f32_e32 v10, v10
	v_exp_f32_e32 v12, v12
	v_exp_f32_e32 v14, v14
	v_exp_f32_e32 v16, v16
	v_add_f32_e32 v212, 1.0, v212
	v_add_f32_e32 v213, 1.0, v213
	v_add_f32_e32 v214, 1.0, v214
	v_add_f32_e32 v215, 1.0, v215
	v_add_f32_e32 v10, 1.0, v10
	v_add_f32_e32 v12, 1.0, v12
	v_add_f32_e32 v14, 1.0, v14
	v_add_f32_e32 v16, 1.0, v16
	v_rcp_f32_e32 v212, v212
	v_rcp_f32_e32 v213, v213
	v_rcp_f32_e32 v214, v214
	v_rcp_f32_e32 v215, v215
	v_rcp_f32_e32 v10, v10
	v_rcp_f32_e32 v12, v12
	v_rcp_f32_e32 v14, v14
	v_rcp_f32_e32 v16, v16
	v_and_b32_e32 v208, 0xffff0000, v208
	v_lshlrev_b32_e32 v11, 16, v209
	v_and_b32_e32 v209, 0xffff0000, v209
	v_lshlrev_b32_e32 v13, 16, v210
	v_and_b32_e32 v210, 0xffff0000, v210
	v_lshlrev_b32_e32 v15, 16, v211
	v_and_b32_e32 v211, 0xffff0000, v211
	v_mul_f32_e32 v208, v212, v208
	v_mul_f32_e32 v209, v213, v209
	v_mul_f32_e32 v210, v214, v210
	v_mul_f32_e32 v211, v215, v211
	v_mul_f32_e32 v1, v10, v1
	v_mul_f32_e32 v212, v12, v11
	v_mul_f32_e32 v213, v14, v13
	v_mul_f32_e32 v214, v16, v15
	v_cvt_pk_bf16_f32 v208, v1, v208
	v_cvt_pk_bf16_f32 v209, v212, v209
	v_cvt_pk_bf16_f32 v210, v213, v210
	v_cvt_pk_bf16_f32 v211, v214, v211
	ds_write_b128 v146, v[208:211]
	v_add_u32_e32 v152, s19, v74
	v_cmp_lt_i32_e32 vcc, -1, v152
	v_mov_b64_e32 v[208:209], 0
	v_mov_b64_e32 v[210:211], 0
	v_mov_b64_e32 v[212:213], 0
	v_mov_b64_e32 v[214:215], 0
	s_and_saveexec_b64 s[16:17], vcc
	s_cbranch_execz .Le2st_skip5
	v_lshl_add_u64 v[248:249], s[92:93], 0, v[152:153]
	v_mad_u64_u32 v[250:251], s[22:23], v248, s53, v[24:25]
	v_mad_i32_i24 v251, v249, s53, v251
	global_load_dwordx4 v[208:211], v[250:251], off offset:1024
	global_load_dwordx4 v[212:215], v[250:251], off offset:2048
; #define LAS __attribute__((address_space(3)))
; __device__ __forceinline__ unsigned pk2(float lo, float hi) { unsigned r; asm("v_cvt_pk_bf16_f32 %0, %1, %2" : "=v"(r) : "v"(lo), "v"(hi)); return r; }
; __device__ __forceinline__ float sigmoidf_(float x) { return __builtin_amdgcn_rcpf(1.0f + __builtin_amdgcn_exp2f(x * -1.44269504089f)); }
; __device__ __forceinline__ void phase_even_mix(CArgs a, LAS unsigned char* lds, int i2, int wv, int xw  ) {
;     ...
;         for (int it = 0; it < 8; ++it) { const int item = it * NTHR + tid, tt = item >> 6, cg = item & 63, p = t0 - 32 + tt;
;             u32x4 o = (u32x4){0u, 0u, 0u, 0u};
;             if (p >= 0) { const bf16* hp = HB + ((size_t)b * SEQ + p) * EVEN_IN + cg * 8; const u32x4 ra = *(const u32x4*)(hp + 512), rg = *(const u32x4*)(hp + 1024);
;                 o.x = pk2(bflo(ra.x) * sigmoidf_(bflo(rg.x)), bfhi(ra.x) * sigmoidf_(bfhi(rg.x))); o.y = pk2(bflo(ra.y) * sigmoidf_(bflo(rg.y)), bfhi(ra.y) * sigmoidf_(bfhi(rg.y)));
;                 o.z = pk2(bflo(ra.z) * sigmoidf_(bflo(rg.z)), bfhi(ra.z) * sigmoidf_(bfhi(rg.z))); o.w = pk2(bflo(ra.w) * sigmoidf_(bflo(rg.w)), bfhi(ra.w) * sigmoidf_(bfhi(rg.w))); }
;             *(LAS u32x4*)(glu + tt * 512 + cg * 8) = o; }
.Le2st_skip5:
	s_or_b64 exec, exec, s[16:17]
	s_waitcnt vmcnt(8)
	v_lshlrev_b32_e32 v1, 16, v216
	v_lshlrev_b32_e32 v10, 16, v220
	v_and_b32_e32 v220, 0xffff0000, v220
	v_lshlrev_b32_e32 v12, 16, v221
	v_and_b32_e32 v221, 0xffff0000, v221
	v_lshlrev_b32_e32 v14, 16, v222
	v_and_b32_e32 v222, 0xffff0000, v222
	v_lshlrev_b32_e32 v16, 16, v223
	v_and_b32_e32 v223, 0xffff0000, v223
	v_mul_f32_e32 v220, 0xbfb8aa3b, v220
	v_mul_f32_e32 v221, 0xbfb8aa3b, v221
	v_mul_f32_e32 v222, 0xbfb8aa3b, v222
	v_mul_f32_e32 v223, 0xbfb8aa3b, v223
	v_mul_f32_e32 v10, 0xbfb8aa3b, v10
	v_mul_f32_e32 v12, 0xbfb8aa3b, v12
	v_mul_f32_e32 v14, 0xbfb8aa3b, v14
	v_mul_f32_e32 v16, 0xbfb8aa3b, v16
	v_exp_f32_e32 v220, v220
	v_exp_f32_e32 v221, v221
	v_exp_f32_e32 v222, v222
	v_exp_f32_e32 v223, v223
	v_exp_f32_e32 v10, v10
	v_exp_f32_e32 v12, v12
	v_exp_f32_e32 v14, v14
	v_exp_f32_e32 v16, v16
	v_add_f32_e32 v220, 1.0, v220
	v_add_f32_e32 v221, 1.0, v221
	v_add_f32_e32 v222, 1.0, v222
	v_add_f32_e32 v223, 1.0, v223
	v_add_f32_e32 v10, 1.0, v10
	v_add_f32_e32 v12, 1.0, v12
	v_add_f32_e32 v14, 1.0, v14
	v_add_f32_e32 v16, 1.0, v16
	v_rcp_f32_e32 v220, v220
	v_rcp_f32_e32 v221, v221
	v_rcp_f32_e32 v222, v222
	v_rcp_f32_e32 v223, v223
	v_rcp_f32_e32 v10, v10
	v_rcp_f32_e32 v12, v12
	v_rcp_f32_e32 v14, v14
	v_rcp_f32_e32 v16, v16
	v_and_b32_e32 v216, 0xffff0000, v216
	v_lshlrev_b32_e32 v11, 16, v217
	v_and_b32_e32 v217, 0xffff0000, v217
	v_lshlrev_b32_e32 v13, 16, v218
	v_and_b32_e32 v218, 0xffff0000, v218
	v_lshlrev_b32_e32 v15, 16, v219
	v_and_b32_e32 v219, 0xffff0000, v219
	v_mul_f32_e32 v216, v220, v216
	v_mul_f32_e32 v217, v221, v217
	v_mul_f32_e32 v218, v222, v218
	v_mul_f32_e32 v219, v223, v219
	v_mul_f32_e32 v1, v10, v1
	v_mul_f32_e32 v220, v12, v11
	v_mul_f32_e32 v221, v14, v13
	v_mul_f32_e32 v222, v16, v15
	v_cvt_pk_bf16_f32 v216, v1, v216
	v_cvt_pk_bf16_f32 v217, v220, v217
	v_cvt_pk_bf16_f32 v218, v221, v218
	v_cvt_pk_bf16_f32 v219, v222, v219
	ds_write_b128 v147, v[216:219]
	v_add_u32_e32 v152, s19, v75
	v_cmp_lt_i32_e32 vcc, -1, v152
	v_mov_b64_e32 v[216:217], 0
	v_mov_b64_e32 v[218:219], 0
	v_mov_b64_e32 v[220:221], 0
	v_mov_b64_e32 v[222:223], 0
	s_and_saveexec_b64 s[16:17], vcc
	s_cbranch_execz .Le2st_skip6
	v_lshl_add_u64 v[248:249], s[92:93], 0, v[152:153]
	v_mad_u64_u32 v[250:251], s[22:23], v248, s53, v[24:25]
	v_mad_i32_i24 v251, v249, s53, v251
	global_load_dwordx4 v[216:219], v[250:251], off offset:1024
	global_load_dwordx4 v[220:223], v[250:251], off offset:2048
.Le2st_skip6:
	s_or_b64 exec, exec, s[16:17]
	s_waitcnt vmcnt(8)
	v_lshlrev_b32_e32 v1, 16, v224
	v_lshlrev_b32_e32 v10, 16, v228
	v_and_b32_e32 v228, 0xffff0000, v228
	v_lshlrev_b32_e32 v12, 16, v229
	v_and_b32_e32 v229, 0xffff0000, v229
	v_lshlrev_b32_e32 v14, 16, v230
	v_and_b32_e32 v230, 0xffff0000, v230
	v_lshlrev_b32_e32 v16, 16, v231
	v_and_b32_e32 v231, 0xffff0000, v231
	v_mul_f32_e32 v228, 0xbfb8aa3b, v228
	v_mul_f32_e32 v229, 0xbfb8aa3b, v229
	v_mul_f32_e32 v230, 0xbfb8aa3b, v230
	v_mul_f32_e32 v231, 0xbfb8aa3b, v231
	v_mul_f32_e32 v10, 0xbfb8aa3b, v10
	v_mul_f32_e32 v12, 0xbfb8aa3b, v12
	v_mul_f32_e32 v14, 0xbfb8aa3b, v14
	v_mul_f32_e32 v16, 0xbfb8aa3b, v16
	v_exp_f32_e32 v228, v228
	v_exp_f32_e32 v229, v229
	v_exp_f32_e32 v230, v230
	v_exp_f32_e32 v231, v231
	v_exp_f32_e32 v10, v10
	v_exp_f32_e32 v12, v12
	v_exp_f32_e32 v14, v14
	v_exp_f32_e32 v16, v16
	v_add_f32_e32 v228, 1.0, v228
	v_add_f32_e32 v229, 1.0, v229
	v_add_f32_e32 v230, 1.0, v230
	v_add_f32_e32 v231, 1.0, v231
	v_add_f32_e32 v10, 1.0, v10
	v_add_f32_e32 v12, 1.0, v12
	v_add_f32_e32 v14, 1.0, v14
	v_add_f32_e32 v16, 1.0, v16
	v_rcp_f32_e32 v228, v228
	v_rcp_f32_e32 v229, v229
	v_rcp_f32_e32 v230, v230
	v_rcp_f32_e32 v231, v231
	v_rcp_f32_e32 v10, v10
	v_rcp_f32_e32 v12, v12
	v_rcp_f32_e32 v14, v14
	v_rcp_f32_e32 v16, v16
	v_and_b32_e32 v224, 0xffff0000, v224
	v_lshlrev_b32_e32 v11, 16, v225
	v_and_b32_e32 v225, 0xffff0000, v225
	v_lshlrev_b32_e32 v13, 16, v226
	v_and_b32_e32 v226, 0xffff0000, v226
	v_lshlrev_b32_e32 v15, 16, v227
	v_and_b32_e32 v227, 0xffff0000, v227
	v_mul_f32_e32 v224, v228, v224
	v_mul_f32_e32 v225, v229, v225
	v_mul_f32_e32 v226, v230, v226
	v_mul_f32_e32 v227, v231, v227
	v_mul_f32_e32 v1, v10, v1
	v_mul_f32_e32 v228, v12, v11
	v_mul_f32_e32 v229, v14, v13
	v_mul_f32_e32 v230, v16, v15
	v_cvt_pk_bf16_f32 v224, v1, v224
	v_cvt_pk_bf16_f32 v225, v228, v225
	v_cvt_pk_bf16_f32 v226, v229, v226
	v_cvt_pk_bf16_f32 v227, v230, v227
	ds_write_b128 v148, v[224:227]
	v_add_u32_e32 v152, s19, v76
	v_cmp_lt_i32_e32 vcc, -1, v152
	v_mov_b64_e32 v[224:225], 0
	v_mov_b64_e32 v[226:227], 0
	v_mov_b64_e32 v[228:229], 0
	v_mov_b64_e32 v[230:231], 0
	s_and_saveexec_b64 s[16:17], vcc
	s_cbranch_execz .Le2st_skip7
	v_lshl_add_u64 v[248:249], s[92:93], 0, v[152:153]
	v_mad_u64_u32 v[250:251], s[22:23], v248, s53, v[24:25]
	v_mad_i32_i24 v251, v249, s53, v251
	global_load_dwordx4 v[224:227], v[250:251], off offset:1024
	global_load_dwordx4 v[228:231], v[250:251], off offset:2048
; #define LAS __attribute__((address_space(3)))
; __device__ __forceinline__ unsigned pk2(float lo, float hi) { unsigned r; asm("v_cvt_pk_bf16_f32 %0, %1, %2" : "=v"(r) : "v"(lo), "v"(hi)); return r; }
; __device__ __forceinline__ float sigmoidf_(float x) { return __builtin_amdgcn_rcpf(1.0f + __builtin_amdgcn_exp2f(x * -1.44269504089f)); }
; __device__ __forceinline__ void phase_even_mix(CArgs a, LAS unsigned char* lds, int i2, int wv, int xw  ) {
;     ...
;         for (int it = 0; it < 8; ++it) { const int item = it * NTHR + tid, tt = item >> 6, cg = item & 63, p = t0 - 32 + tt;
;             u32x4 o = (u32x4){0u, 0u, 0u, 0u};
;             if (p >= 0) { const bf16* hp = HB + ((size_t)b * SEQ + p) * EVEN_IN + cg * 8; const u32x4 ra = *(const u32x4*)(hp + 512), rg = *(const u32x4*)(hp + 1024);
;                 o.x = pk2(bflo(ra.x) * sigmoidf_(bflo(rg.x)), bfhi(ra.x) * sigmoidf_(bfhi(rg.x))); o.y = pk2(bflo(ra.y) * sigmoidf_(bflo(rg.y)), bfhi(ra.y) * sigmoidf_(bfhi(rg.y)));
;                 o.z = pk2(bflo(ra.z) * sigmoidf_(bflo(rg.z)), bfhi(ra.z) * sigmoidf_(bfhi(rg.z))); o.w = pk2(bflo(ra.w) * sigmoidf_(bflo(rg.w)), bfhi(ra.w) * sigmoidf_(bfhi(rg.w))); }
;             *(LAS u32x4*)(glu + tt * 512 + cg * 8) = o; }
.Le2st_skip7:
	s_or_b64 exec, exec, s[16:17]
	s_waitcnt vmcnt(8)
	v_lshlrev_b32_e32 v1, 16, v232
	v_lshlrev_b32_e32 v10, 16, v236
	v_and_b32_e32 v236, 0xffff0000, v236
	v_lshlrev_b32_e32 v12, 16, v237
	v_and_b32_e32 v237, 0xffff0000, v237
	v_lshlrev_b32_e32 v14, 16, v238
	v_and_b32_e32 v238, 0xffff0000, v238
	v_lshlrev_b32_e32 v16, 16, v239
	v_and_b32_e32 v239, 0xffff0000, v239
	v_mul_f32_e32 v236, 0xbfb8aa3b, v236
	v_mul_f32_e32 v237, 0xbfb8aa3b, v237
	v_mul_f32_e32 v238, 0xbfb8aa3b, v238
	v_mul_f32_e32 v239, 0xbfb8aa3b, v239
	v_mul_f32_e32 v10, 0xbfb8aa3b, v10
	v_mul_f32_e32 v12, 0xbfb8aa3b, v12
	v_mul_f32_e32 v14, 0xbfb8aa3b, v14
	v_mul_f32_e32 v16, 0xbfb8aa3b, v16
	v_exp_f32_e32 v236, v236
	v_exp_f32_e32 v237, v237
	v_exp_f32_e32 v238, v238
	v_exp_f32_e32 v239, v239
	v_exp_f32_e32 v10, v10
	v_exp_f32_e32 v12, v12
	v_exp_f32_e32 v14, v14
	v_exp_f32_e32 v16, v16
	v_add_f32_e32 v236, 1.0, v236
	v_add_f32_e32 v237, 1.0, v237
	v_add_f32_e32 v238, 1.0, v238
	v_add_f32_e32 v239, 1.0, v239
	v_add_f32_e32 v10, 1.0, v10
	v_add_f32_e32 v12, 1.0, v12
	v_add_f32_e32 v14, 1.0, v14
	v_add_f32_e32 v16, 1.0, v16
	v_rcp_f32_e32 v236, v236
	v_rcp_f32_e32 v237, v237
	v_rcp_f32_e32 v238, v238
	v_rcp_f32_e32 v239, v239
	v_rcp_f32_e32 v10, v10
	v_rcp_f32_e32 v12, v12
	v_rcp_f32_e32 v14, v14
	v_rcp_f32_e32 v16, v16
	v_and_b32_e32 v232, 0xffff0000, v232
	v_lshlrev_b32_e32 v11, 16, v233
	v_and_b32_e32 v233, 0xffff0000, v233
	v_lshlrev_b32_e32 v13, 16, v234
	v_and_b32_e32 v234, 0xffff0000, v234
	v_lshlrev_b32_e32 v15, 16, v235
	v_and_b32_e32 v235, 0xffff0000, v235
	v_mul_f32_e32 v232, v236, v232
	v_mul_f32_e32 v233, v237, v233
	v_mul_f32_e32 v234, v238, v234
	v_mul_f32_e32 v235, v239, v235
	v_mul_f32_e32 v1, v10, v1
	v_mul_f32_e32 v236, v12, v11
	v_mul_f32_e32 v237, v14, v13
	v_mul_f32_e32 v238, v16, v15
	v_cvt_pk_bf16_f32 v232, v1, v232
	v_cvt_pk_bf16_f32 v233, v236, v233
	v_cvt_pk_bf16_f32 v234, v237, v234
	v_cvt_pk_bf16_f32 v235, v238, v235
	ds_write_b128 v149, v[232:235]
	s_waitcnt vmcnt(6)
	v_lshlrev_b32_e32 v1, 16, v240
	v_lshlrev_b32_e32 v10, 16, v244
	v_and_b32_e32 v244, 0xffff0000, v244
	v_lshlrev_b32_e32 v12, 16, v245
	v_and_b32_e32 v245, 0xffff0000, v245
	v_lshlrev_b32_e32 v14, 16, v246
	v_and_b32_e32 v246, 0xffff0000, v246
	v_lshlrev_b32_e32 v16, 16, v247
	v_and_b32_e32 v247, 0xffff0000, v247
	v_mul_f32_e32 v244, 0xbfb8aa3b, v244
	v_mul_f32_e32 v245, 0xbfb8aa3b, v245
	v_mul_f32_e32 v246, 0xbfb8aa3b, v246
	v_mul_f32_e32 v247, 0xbfb8aa3b, v247
	v_mul_f32_e32 v10, 0xbfb8aa3b, v10
	v_mul_f32_e32 v12, 0xbfb8aa3b, v12
	v_mul_f32_e32 v14, 0xbfb8aa3b, v14
	v_mul_f32_e32 v16, 0xbfb8aa3b, v16
	v_exp_f32_e32 v244, v244
	v_exp_f32_e32 v245, v245
	v_exp_f32_e32 v246, v246
	v_exp_f32_e32 v247, v247
	v_exp_f32_e32 v10, v10
	v_exp_f32_e32 v12, v12
	v_exp_f32_e32 v14, v14
	v_exp_f32_e32 v16, v16
	v_add_f32_e32 v244, 1.0, v244
	v_add_f32_e32 v245, 1.0, v245
	v_add_f32_e32 v246, 1.0, v246
	v_add_f32_e32 v247, 1.0, v247
	v_add_f32_e32 v10, 1.0, v10
	v_add_f32_e32 v12, 1.0, v12
	v_add_f32_e32 v14, 1.0, v14
	v_add_f32_e32 v16, 1.0, v16
	v_rcp_f32_e32 v244, v244
	v_rcp_f32_e32 v245, v245
	v_rcp_f32_e32 v246, v246
	v_rcp_f32_e32 v247, v247
	v_rcp_f32_e32 v10, v10
	v_rcp_f32_e32 v12, v12
	v_rcp_f32_e32 v14, v14
	v_rcp_f32_e32 v16, v16
	v_and_b32_e32 v240, 0xffff0000, v240
	v_lshlrev_b32_e32 v11, 16, v241
	v_and_b32_e32 v241, 0xffff0000, v241
	v_lshlrev_b32_e32 v13, 16, v242
	v_and_b32_e32 v242, 0xffff0000, v242
	v_lshlrev_b32_e32 v15, 16, v243
	v_and_b32_e32 v243, 0xffff0000, v243
	v_mul_f32_e32 v240, v244, v240
	v_mul_f32_e32 v241, v245, v241
	v_mul_f32_e32 v242, v246, v242
	v_mul_f32_e32 v243, v247, v243
	v_mul_f32_e32 v1, v10, v1
	v_mul_f32_e32 v244, v12, v11
	v_mul_f32_e32 v245, v14, v13
	v_mul_f32_e32 v246, v16, v15
	v_cvt_pk_bf16_f32 v240, v1, v240
	v_cvt_pk_bf16_f32 v241, v244, v241
	v_cvt_pk_bf16_f32 v242, v245, v242
	v_cvt_pk_bf16_f32 v243, v246, v243
	ds_write_b128 v150, v[240:243]
	s_waitcnt vmcnt(4)
	v_lshlrev_b32_e32 v1, 16, v208
	v_lshlrev_b32_e32 v10, 16, v212
	v_and_b32_e32 v212, 0xffff0000, v212
	v_lshlrev_b32_e32 v12, 16, v213
	v_and_b32_e32 v213, 0xffff0000, v213
	v_lshlrev_b32_e32 v14, 16, v214
	v_and_b32_e32 v214, 0xffff0000, v214
	v_lshlrev_b32_e32 v16, 16, v215
	v_and_b32_e32 v215, 0xffff0000, v215
	v_mul_f32_e32 v212, 0xbfb8aa3b, v212
	v_mul_f32_e32 v213, 0xbfb8aa3b, v213
	v_mul_f32_e32 v214, 0xbfb8aa3b, v214
	v_mul_f32_e32 v215, 0xbfb8aa3b, v215
	v_mul_f32_e32 v10, 0xbfb8aa3b, v10
	v_mul_f32_e32 v12, 0xbfb8aa3b, v12
	v_mul_f32_e32 v14, 0xbfb8aa3b, v14
	v_mul_f32_e32 v16, 0xbfb8aa3b, v16
	v_exp_f32_e32 v212, v212
	v_exp_f32_e32 v213, v213
	v_exp_f32_e32 v214, v214
	v_exp_f32_e32 v215, v215
	v_exp_f32_e32 v10, v10
	v_exp_f32_e32 v12, v12
	v_exp_f32_e32 v14, v14
	v_exp_f32_e32 v16, v16
	v_add_f32_e32 v212, 1.0, v212
	v_add_f32_e32 v213, 1.0, v213
	v_add_f32_e32 v214, 1.0, v214
	v_add_f32_e32 v215, 1.0, v215
	v_add_f32_e32 v10, 1.0, v10
	v_add_f32_e32 v12, 1.0, v12
	v_add_f32_e32 v14, 1.0, v14
	v_add_f32_e32 v16, 1.0, v16
	v_rcp_f32_e32 v212, v212
	v_rcp_f32_e32 v213, v213
	v_rcp_f32_e32 v214, v214
	v_rcp_f32_e32 v215, v215
	v_rcp_f32_e32 v10, v10
	v_rcp_f32_e32 v12, v12
	v_rcp_f32_e32 v14, v14
	v_rcp_f32_e32 v16, v16
	v_and_b32_e32 v208, 0xffff0000, v208
	v_lshlrev_b32_e32 v11, 16, v209
	v_and_b32_e32 v209, 0xffff0000, v209
	v_lshlrev_b32_e32 v13, 16, v210
	v_and_b32_e32 v210, 0xffff0000, v210
	v_lshlrev_b32_e32 v15, 16, v211
	v_and_b32_e32 v211, 0xffff0000, v211
	v_mul_f32_e32 v208, v212, v208
	v_mul_f32_e32 v209, v213, v209
	v_mul_f32_e32 v210, v214, v210
	v_mul_f32_e32 v211, v215, v211
	v_mul_f32_e32 v1, v10, v1
	v_mul_f32_e32 v212, v12, v11
	v_mul_f32_e32 v213, v14, v13
	v_mul_f32_e32 v214, v16, v15
	v_cvt_pk_bf16_f32 v208, v1, v208
	v_cvt_pk_bf16_f32 v209, v212, v209
	v_cvt_pk_bf16_f32 v210, v213, v210
	v_cvt_pk_bf16_f32 v211, v214, v211
	ds_write_b128 v151, v[208:211]
	s_waitcnt vmcnt(2)
; #define LAS __attribute__((address_space(3)))
; __device__ __forceinline__ unsigned pk2(float lo, float hi) { unsigned r; asm("v_cvt_pk_bf16_f32 %0, %1, %2" : "=v"(r) : "v"(lo), "v"(hi)); return r; }
; __device__ __forceinline__ float sigmoidf_(float x) { return __builtin_amdgcn_rcpf(1.0f + __builtin_amdgcn_exp2f(x * -1.44269504089f)); }
; __device__ __forceinline__ void phase_even_mix(CArgs a, LAS unsigned char* lds, int i2, int wv, int xw  ) {
;     ...
;         for (int it = 0; it < 8; ++it) { const int item = it * NTHR + tid, tt = item >> 6, cg = item & 63, p = t0 - 32 + tt;
;             u32x4 o = (u32x4){0u, 0u, 0u, 0u};
;             if (p >= 0) { const bf16* hp = HB + ((size_t)b * SEQ + p) * EVEN_IN + cg * 8; const u32x4 ra = *(const u32x4*)(hp + 512), rg = *(const u32x4*)(hp + 1024);
;                 o.x = pk2(bflo(ra.x) * sigmoidf_(bflo(rg.x)), bfhi(ra.x) * sigmoidf_(bfhi(rg.x))); o.y = pk2(bflo(ra.y) * sigmoidf_(bflo(rg.y)), bfhi(ra.y) * sigmoidf_(bfhi(rg.y)));
;                 o.z = pk2(bflo(ra.z) * sigmoidf_(bflo(rg.z)), bfhi(ra.z) * sigmoidf_(bfhi(rg.z))); o.w = pk2(bflo(ra.w) * sigmoidf_(bflo(rg.w)), bfhi(ra.w) * sigmoidf_(bfhi(rg.w))); }
;             *(LAS u32x4*)(glu + tt * 512 + cg * 8) = o; }
;         __syncthreads();
;         {
;             float w[31];
; #pragma unroll
;             for (int k = 0; k < 31; ++k) { unsigned off = (unsigned)c * 4u; asm volatile("" : "+v"(off)); w[k] = *(const float*)((const char*)(cw + k * 512) + off); }
	v_lshlrev_b32_e32 v1, 16, v216
	v_lshlrev_b32_e32 v10, 16, v220
	v_and_b32_e32 v220, 0xffff0000, v220
	v_lshlrev_b32_e32 v12, 16, v221
	v_and_b32_e32 v221, 0xffff0000, v221
	v_lshlrev_b32_e32 v14, 16, v222
	v_and_b32_e32 v222, 0xffff0000, v222
	v_lshlrev_b32_e32 v16, 16, v223
	v_and_b32_e32 v223, 0xffff0000, v223
	v_mul_f32_e32 v220, 0xbfb8aa3b, v220
	v_mul_f32_e32 v221, 0xbfb8aa3b, v221
	v_mul_f32_e32 v222, 0xbfb8aa3b, v222
	v_mul_f32_e32 v223, 0xbfb8aa3b, v223
	v_mul_f32_e32 v10, 0xbfb8aa3b, v10
	v_mul_f32_e32 v12, 0xbfb8aa3b, v12
	v_mul_f32_e32 v14, 0xbfb8aa3b, v14
	v_mul_f32_e32 v16, 0xbfb8aa3b, v16
	v_exp_f32_e32 v220, v220
	v_exp_f32_e32 v221, v221
	v_exp_f32_e32 v222, v222
	v_exp_f32_e32 v223, v223
	v_exp_f32_e32 v10, v10
	v_exp_f32_e32 v12, v12
	v_exp_f32_e32 v14, v14
	v_exp_f32_e32 v16, v16
	v_add_f32_e32 v220, 1.0, v220
	v_add_f32_e32 v221, 1.0, v221
	v_add_f32_e32 v222, 1.0, v222
	v_add_f32_e32 v223, 1.0, v223
	v_add_f32_e32 v10, 1.0, v10
	v_add_f32_e32 v12, 1.0, v12
	v_add_f32_e32 v14, 1.0, v14
	v_add_f32_e32 v16, 1.0, v16
	v_rcp_f32_e32 v220, v220
	v_rcp_f32_e32 v221, v221
	v_rcp_f32_e32 v222, v222
	v_rcp_f32_e32 v223, v223
	v_rcp_f32_e32 v10, v10
	v_rcp_f32_e32 v12, v12
	v_rcp_f32_e32 v14, v14
	v_rcp_f32_e32 v16, v16
	v_and_b32_e32 v216, 0xffff0000, v216
	v_lshlrev_b32_e32 v11, 16, v217
	v_and_b32_e32 v217, 0xffff0000, v217
	v_lshlrev_b32_e32 v13, 16, v218
	v_and_b32_e32 v218, 0xffff0000, v218
	v_lshlrev_b32_e32 v15, 16, v219
	v_and_b32_e32 v219, 0xffff0000, v219
	v_mul_f32_e32 v216, v220, v216
	v_mul_f32_e32 v217, v221, v217
	v_mul_f32_e32 v218, v222, v218
	v_mul_f32_e32 v219, v223, v219
	v_mul_f32_e32 v1, v10, v1
	v_mul_f32_e32 v220, v12, v11
	v_mul_f32_e32 v221, v14, v13
	v_mul_f32_e32 v222, v16, v15
	v_cvt_pk_bf16_f32 v216, v1, v216
	v_cvt_pk_bf16_f32 v217, v220, v217
	v_cvt_pk_bf16_f32 v218, v221, v218
	v_cvt_pk_bf16_f32 v219, v222, v219
	ds_write_b128 v141, v[216:219]
	s_waitcnt vmcnt(0)
	v_lshlrev_b32_e32 v1, 16, v224
	v_lshlrev_b32_e32 v10, 16, v228
	v_and_b32_e32 v228, 0xffff0000, v228
	v_lshlrev_b32_e32 v12, 16, v229
	v_and_b32_e32 v229, 0xffff0000, v229
	v_lshlrev_b32_e32 v14, 16, v230
	v_and_b32_e32 v230, 0xffff0000, v230
	v_lshlrev_b32_e32 v16, 16, v231
	v_and_b32_e32 v231, 0xffff0000, v231
	v_mul_f32_e32 v228, 0xbfb8aa3b, v228
	v_mul_f32_e32 v229, 0xbfb8aa3b, v229
	v_mul_f32_e32 v230, 0xbfb8aa3b, v230
	v_mul_f32_e32 v231, 0xbfb8aa3b, v231
	v_mul_f32_e32 v10, 0xbfb8aa3b, v10
	v_mul_f32_e32 v12, 0xbfb8aa3b, v12
	v_mul_f32_e32 v14, 0xbfb8aa3b, v14
	v_mul_f32_e32 v16, 0xbfb8aa3b, v16
	v_exp_f32_e32 v228, v228
	v_exp_f32_e32 v229, v229
	v_exp_f32_e32 v230, v230
	v_exp_f32_e32 v231, v231
	v_exp_f32_e32 v10, v10
	v_exp_f32_e32 v12, v12
	v_exp_f32_e32 v14, v14
	v_exp_f32_e32 v16, v16
	v_add_f32_e32 v228, 1.0, v228
	v_add_f32_e32 v229, 1.0, v229
	v_add_f32_e32 v230, 1.0, v230
	v_add_f32_e32 v231, 1.0, v231
	v_add_f32_e32 v10, 1.0, v10
	v_add_f32_e32 v12, 1.0, v12
	v_add_f32_e32 v14, 1.0, v14
	v_add_f32_e32 v16, 1.0, v16
	v_rcp_f32_e32 v228, v228
	v_rcp_f32_e32 v229, v229
	v_rcp_f32_e32 v230, v230
	v_rcp_f32_e32 v231, v231
	v_rcp_f32_e32 v10, v10
	v_rcp_f32_e32 v12, v12
	v_rcp_f32_e32 v14, v14
	v_rcp_f32_e32 v16, v16
	v_and_b32_e32 v224, 0xffff0000, v224
	v_lshlrev_b32_e32 v11, 16, v225
	v_and_b32_e32 v225, 0xffff0000, v225
	v_lshlrev_b32_e32 v13, 16, v226
	v_and_b32_e32 v226, 0xffff0000, v226
	v_lshlrev_b32_e32 v15, 16, v227
	v_and_b32_e32 v227, 0xffff0000, v227
	v_mul_f32_e32 v224, v228, v224
	v_mul_f32_e32 v225, v229, v225
	v_mul_f32_e32 v226, v230, v226
	v_mul_f32_e32 v227, v231, v227
	v_mul_f32_e32 v1, v10, v1
	v_mul_f32_e32 v228, v12, v11
	v_mul_f32_e32 v229, v14, v13
	v_mul_f32_e32 v230, v16, v15
	v_cvt_pk_bf16_f32 v224, v1, v224
	v_cvt_pk_bf16_f32 v225, v228, v225
	v_cvt_pk_bf16_f32 v226, v229, v226
	v_cvt_pk_bf16_f32 v227, v230, v227
	ds_write_b128 v142, v[224:227]
	v_mov_b32_e32 v0, v29
	s_waitcnt vmcnt(0) lgkmcnt(0)
	s_barrier
	v_mov_b32_e32 v1, v29
	global_load_dword v0, v0, s[90:91]
	v_mov_b32_e32 v2, v29
	v_readlane_b32 s16, v254, 33
	global_load_dword v1, v1, s[90:91] offset:2048
	v_readlane_b32 s17, v254, 34
	v_mov_b32_e32 v3, v29
	v_mov_b32_e32 v4, v29
	v_mov_b32_e32 v5, v29
	v_mov_b32_e32 v6, v29
	v_mov_b32_e32 v7, v29
	global_load_dword v2, v2, s[16:17]
	v_readlane_b32 s16, v254, 35
	v_readlane_b32 s17, v254, 36
	v_mov_b32_e32 v8, v29
	v_mov_b32_e32 v9, v29
	v_mov_b32_e32 v10, v29
	v_mov_b32_e32 v11, v29
	v_mov_b32_e32 v12, v29
	global_load_dword v3, v3, s[16:17]
	v_readlane_b32 s16, v254, 37
	v_readlane_b32 s17, v254, 38
	v_mov_b32_e32 v13, v29
	v_mov_b32_e32 v14, v29
	v_mov_b32_e32 v15, v29
	v_mov_b32_e32 v16, v29
	v_mov_b32_e32 v17, v29
	global_load_dword v4, v4, s[16:17]
	v_readlane_b32 s16, v254, 39
	v_readlane_b32 s17, v254, 40
	v_mov_b32_e32 v18, v29
	v_mov_b32_e32 v19, v29
	v_mov_b32_e32 v20, v29
	v_mov_b32_e32 v21, v29
	v_mov_b32_e32 v22, v29
	global_load_dword v5, v5, s[16:17]
	v_readlane_b32 s16, v254, 41
	v_readlane_b32 s17, v254, 42
	v_mov_b32_e32 v23, v29
	v_mov_b32_e32 v152, v29
	v_mov_b32_e32 v154, v29
	v_mov_b32_e32 v155, v29
	v_mov_b32_e32 v156, v29
	global_load_dword v6, v6, s[16:17]
	v_readlane_b32 s16, v254, 43
	v_readlane_b32 s17, v254, 44
	v_mov_b32_e32 v157, v29
	v_mov_b32_e32 v158, v29
	v_mov_b32_e32 v159, v29
	s_add_i32 s19, s15, -16
	s_nop 0
	global_load_dword v7, v7, s[16:17]
	v_readlane_b32 s16, v254, 45
	v_readlane_b32 s17, v254, 46
	s_nop 4
	global_load_dword v8, v8, s[16:17]
	v_readlane_b32 s16, v254, 47
	v_readlane_b32 s17, v254, 48
	s_nop 4
	global_load_dword v9, v9, s[16:17]
	v_readlane_b32 s16, v254, 49
	v_readlane_b32 s17, v254, 50
	s_nop 4
	global_load_dword v10, v10, s[16:17]
; __device__ __forceinline__ void phase_even_mix(CArgs a, LAS unsigned char* lds, int i2, int wv, int xw  ) {
;     ...
;             for (int k = 0; k < 31; ++k) { unsigned off = (unsigned)c * 4u; asm volatile("" : "+v"(off)); w[k] = *(const float*)((const char*)(cw + k * 512) + off); }
;             const float cb = a->in[I_CONVB][i2 * 512 + c];
;             float win[34];
; #pragma clang loop unroll(full)
;             for (int r = 0; r < 64; ++r) {
;                 win[r % 34] = bf2f(glu[r * 512 + c]);
;                 if (r >= 32) { float y = cb;
; #pragma unroll
;                     for (int k = 0; k < 31; ++k) y += w[k] * win[(r - 30 + k) % 34];
;                     ybuf[(r - 32) * 512 + c] = y; }
	v_readlane_b32 s16, v254, 51
	v_readlane_b32 s17, v254, 52
	s_nop 4
	global_load_dword v11, v11, s[16:17]
	v_readlane_b32 s16, v254, 53
	v_readlane_b32 s17, v254, 54
	s_nop 4
	global_load_dword v12, v12, s[16:17]
	v_readlane_b32 s16, v254, 55
	v_readlane_b32 s17, v254, 56
	s_nop 4
	global_load_dword v13, v13, s[16:17]
	v_readlane_b32 s16, v254, 57
	v_readlane_b32 s17, v254, 58
	s_nop 4
	global_load_dword v14, v14, s[16:17]
	v_readlane_b32 s16, v254, 59
	v_readlane_b32 s17, v254, 60
	s_nop 4
	global_load_dword v15, v15, s[16:17]
	v_readlane_b32 s16, v254, 61
	v_readlane_b32 s17, v254, 62
	s_nop 4
	global_load_dword v16, v16, s[16:17]
	v_readlane_b32 s16, v254, 63
	v_readlane_b32 s17, v255, 0
	s_nop 4
	global_load_dword v17, v17, s[16:17]
	v_readlane_b32 s16, v255, 1
	v_readlane_b32 s17, v255, 2
	s_nop 4
	global_load_dword v18, v18, s[16:17]
	global_load_dword v19, v19, s[40:41]
	global_load_dword v20, v20, s[84:85]
	global_load_dword v21, v21, s[26:27]
	global_load_dword v22, v22, s[20:21]
	global_load_dword v23, v23, s[4:5]
	global_load_dword v152, v152, s[2:3]
	global_load_dword v154, v154, s[24:25]
	global_load_dword v155, v155, s[30:31]
	global_load_dword v156, v156, s[0:1]
	global_load_dword v157, v157, s[72:73]
	global_load_dword v158, v158, s[74:75]
	s_load_dwordx2 s[16:17], s[88:89], 0x38
	ds_read_u16 v162, v35 offset:3072
	ds_read_u16 v163, v35 offset:4096
	ds_read_u16 v164, v35 offset:5120
	ds_read_u16 v165, v35 offset:6144
	ds_read_u16 v166, v35 offset:7168
	s_waitcnt lgkmcnt(0)
	v_lshl_add_u64 v[160:161], v[26:27], 2, s[16:17]
	global_load_dword v160, v[160:161], off
	ds_read_u16 v161, v35 offset:2048
	global_load_dword v159, v159, s[76:77]
	v_lshlrev_b32_e32 v167, 16, v166
	ds_read_u16 v166, v35 offset:8192
	v_lshlrev_b32_e32 v162, 16, v162
	v_lshlrev_b32_e32 v163, 16, v163
	v_lshlrev_b32_e32 v164, 16, v164
	v_lshlrev_b32_e32 v165, 16, v165
	s_waitcnt lgkmcnt(0)
	v_lshlrev_b32_e32 v174, 16, v166
	ds_read_u16 v166, v35 offset:9216
	s_waitcnt lgkmcnt(0)
	v_lshlrev_b32_e32 v176, 16, v166
	ds_read_u16 v166, v35 offset:10240
	s_waitcnt lgkmcnt(0)
	v_lshlrev_b32_e32 v177, 16, v166
	ds_read_u16 v166, v35 offset:11264
	s_waitcnt lgkmcnt(0)
	v_lshlrev_b32_e32 v192, 16, v166
	ds_read_u16 v166, v35 offset:12288
	s_waitcnt lgkmcnt(0)
	v_lshlrev_b32_e32 v193, 16, v166
	ds_read_u16 v166, v35 offset:13312
	s_waitcnt lgkmcnt(0)
	v_lshlrev_b32_e32 v194, 16, v166
	ds_read_u16 v166, v35 offset:14336
	s_waitcnt lgkmcnt(0)
	v_lshlrev_b32_e32 v196, 16, v166
	ds_read_u16 v166, v35 offset:15360
	s_waitcnt lgkmcnt(0)
	v_lshlrev_b32_e32 v198, 16, v166
	ds_read_u16 v166, v35 offset:16384
	s_waitcnt lgkmcnt(0)
	v_lshlrev_b32_e32 v205, 16, v166
	ds_read_u16 v166, v35 offset:17408
	s_waitcnt lgkmcnt(0)
	v_lshlrev_b32_e32 v204, 16, v166
	ds_read_u16 v166, v35 offset:18432
	s_waitcnt lgkmcnt(0)
	v_lshlrev_b32_e32 v203, 16, v166
	ds_read_u16 v166, v35 offset:19456
	s_waitcnt lgkmcnt(0)
	v_lshlrev_b32_e32 v202, 16, v166
	ds_read_u16 v166, v35 offset:20480
	s_waitcnt vmcnt(1)
	v_fma_f32 v178, v0, v192, v160
	s_waitcnt lgkmcnt(0)
	v_lshlrev_b32_e32 v201, 16, v166
	ds_read_u16 v166, v35 offset:21504
	v_fmac_f32_e32 v178, v1, v193
	v_fmac_f32_e32 v178, v2, v194
	v_fmac_f32_e32 v178, v3, v196
	v_fmac_f32_e32 v178, v4, v198
	s_waitcnt lgkmcnt(0)
	v_lshlrev_b32_e32 v200, 16, v166
	ds_read_u16 v166, v35 offset:22528
	v_fmac_f32_e32 v178, v5, v205
	v_fmac_f32_e32 v178, v6, v204
	v_fmac_f32_e32 v178, v7, v203
	v_fmac_f32_e32 v178, v8, v202
	s_waitcnt lgkmcnt(0)
	v_lshlrev_b32_e32 v199, 16, v166
	ds_read_u16 v166, v35 offset:23552
	v_fmac_f32_e32 v178, v9, v201
	v_fmac_f32_e32 v178, v10, v200
	v_fmac_f32_e32 v178, v11, v199
	s_waitcnt lgkmcnt(0)
	v_lshlrev_b32_e32 v197, 16, v166
	ds_read_u16 v166, v35 offset:24576
	v_fmac_f32_e32 v178, v12, v197
	s_waitcnt lgkmcnt(0)
	v_lshlrev_b32_e32 v195, 16, v166
	ds_read_u16 v166, v35 offset:25600
	v_fmac_f32_e32 v178, v13, v195
	s_waitcnt lgkmcnt(0)
	v_lshlrev_b32_e32 v175, 16, v166
	ds_read_u16 v166, v35 offset:26624
	v_fmac_f32_e32 v178, v14, v175
	s_waitcnt lgkmcnt(0)
	v_lshlrev_b32_e32 v173, 16, v166
	ds_read_u16 v166, v35 offset:27648
	v_fmac_f32_e32 v178, v15, v173
	s_waitcnt lgkmcnt(0)
	v_lshlrev_b32_e32 v172, 16, v166
	ds_read_u16 v166, v35 offset:28672
	v_fmac_f32_e32 v178, v16, v172
	s_waitcnt lgkmcnt(0)
	v_lshlrev_b32_e32 v171, 16, v166
	ds_read_u16 v166, v35 offset:29696
	v_fmac_f32_e32 v178, v17, v171
	s_waitcnt lgkmcnt(0)
	v_lshlrev_b32_e32 v170, 16, v166
	ds_read_u16 v166, v35 offset:30720
	v_fmac_f32_e32 v178, v18, v170
	s_waitcnt lgkmcnt(0)
	v_lshlrev_b32_e32 v169, 16, v166
	ds_read_u16 v166, v35 offset:31744
	v_fmac_f32_e32 v178, v19, v169
	s_waitcnt lgkmcnt(0)
; __device__ __forceinline__ void phase_even_mix(CArgs a, LAS unsigned char* lds, int i2, int wv, int xw  ) {
;     ...
; #pragma clang loop unroll(full)
;             for (int r = 0; r < 64; ++r) {
;                 win[r % 34] = bf2f(glu[r * 512 + c]);
;                 if (r >= 32) { float y = cb;
; #pragma unroll
;                     for (int k = 0; k < 31; ++k) y += w[k] * win[(r - 30 + k) % 34];
;                     ybuf[(r - 32) * 512 + c] = y; }
	v_lshlrev_b32_e32 v168, 16, v166
	ds_read_u16 v166, v35 offset:32768
	v_lshlrev_b32_e32 v161, 16, v161
	v_fma_f32 v161, v0, v161, v160
	v_fmac_f32_e32 v161, v1, v162
	v_fmac_f32_e32 v161, v2, v163
	v_fmac_f32_e32 v161, v3, v164
	v_fmac_f32_e32 v161, v4, v165
	v_fmac_f32_e32 v161, v5, v167
	v_fmac_f32_e32 v161, v6, v174
	v_fmac_f32_e32 v161, v7, v176
	v_fma_f32 v162, v0, v162, v160
	v_fmac_f32_e32 v161, v8, v177
	v_fmac_f32_e32 v162, v1, v163
	v_fmac_f32_e32 v161, v9, v192
	v_fmac_f32_e32 v162, v2, v164
	v_fmac_f32_e32 v161, v10, v193
	v_fmac_f32_e32 v162, v3, v165
	v_fmac_f32_e32 v161, v11, v194
	v_fmac_f32_e32 v162, v4, v167
	v_fmac_f32_e32 v161, v12, v196
	v_fmac_f32_e32 v162, v5, v174
	v_fmac_f32_e32 v161, v13, v198
	v_fmac_f32_e32 v162, v6, v176
	v_fmac_f32_e32 v161, v14, v205
	v_fmac_f32_e32 v162, v7, v177
	v_fma_f32 v163, v0, v163, v160
	v_fmac_f32_e32 v161, v15, v204
	v_fmac_f32_e32 v162, v8, v192
	v_fmac_f32_e32 v163, v1, v164
	v_fmac_f32_e32 v161, v16, v203
	v_fmac_f32_e32 v162, v9, v193
	v_fmac_f32_e32 v163, v2, v165
	v_fmac_f32_e32 v161, v17, v202
	v_fmac_f32_e32 v162, v10, v194
	v_fmac_f32_e32 v163, v3, v167
	v_fmac_f32_e32 v161, v18, v201
	v_fmac_f32_e32 v162, v11, v196
	v_fmac_f32_e32 v163, v4, v174
	v_fmac_f32_e32 v161, v19, v200
	v_fmac_f32_e32 v162, v12, v198
	v_fmac_f32_e32 v163, v5, v176
	v_fmac_f32_e32 v161, v20, v199
	v_fmac_f32_e32 v162, v13, v205
	v_fmac_f32_e32 v163, v6, v177
	v_fmac_f32_e32 v161, v21, v197
	v_fmac_f32_e32 v162, v14, v204
	v_fmac_f32_e32 v163, v7, v192
	v_fma_f32 v164, v0, v164, v160
	v_fmac_f32_e32 v161, v22, v195
	v_fmac_f32_e32 v162, v15, v203
	v_fmac_f32_e32 v163, v8, v193
	v_fmac_f32_e32 v164, v1, v165
	v_fmac_f32_e32 v161, v23, v175
	v_fmac_f32_e32 v162, v16, v202
	v_fmac_f32_e32 v163, v9, v194
	v_fmac_f32_e32 v164, v2, v167
	v_fmac_f32_e32 v161, v152, v173
	v_fmac_f32_e32 v162, v17, v201
	v_fmac_f32_e32 v163, v10, v196
	v_fmac_f32_e32 v164, v3, v174
	v_fmac_f32_e32 v161, v154, v172
	v_fmac_f32_e32 v162, v18, v200
	v_fmac_f32_e32 v163, v11, v198
	v_fmac_f32_e32 v164, v4, v176
	v_fmac_f32_e32 v161, v155, v171
	v_fmac_f32_e32 v162, v19, v199
	v_fmac_f32_e32 v163, v12, v205
	v_fmac_f32_e32 v164, v5, v177
	v_fmac_f32_e32 v161, v156, v170
	v_fmac_f32_e32 v162, v20, v197
	v_fmac_f32_e32 v163, v13, v204
	v_fmac_f32_e32 v164, v6, v192
	v_fmac_f32_e32 v161, v157, v169
	v_fmac_f32_e32 v162, v21, v195
	v_fmac_f32_e32 v163, v14, v203
	v_fmac_f32_e32 v164, v7, v193
	v_fma_f32 v165, v0, v165, v160
	s_waitcnt lgkmcnt(0)
	v_lshlrev_b32_e32 v166, 16, v166
	v_fmac_f32_e32 v161, v158, v168
	v_fmac_f32_e32 v162, v22, v175
	v_fmac_f32_e32 v163, v15, v202
	v_fmac_f32_e32 v164, v8, v194
	v_fmac_f32_e32 v165, v1, v167
	s_waitcnt vmcnt(0)
	v_fmac_f32_e32 v161, v159, v166
	v_fmac_f32_e32 v162, v23, v173
	v_fmac_f32_e32 v163, v16, v201
	v_fmac_f32_e32 v164, v9, v196
	v_fmac_f32_e32 v165, v2, v174
	ds_write_b32 v78, v161
	ds_read_u16 v161, v35 offset:33792
	v_fmac_f32_e32 v162, v152, v172
	v_fmac_f32_e32 v163, v17, v200
	v_fmac_f32_e32 v164, v10, v198
	v_fmac_f32_e32 v165, v3, v176
	v_fmac_f32_e32 v162, v154, v171
	v_fmac_f32_e32 v163, v18, v199
	v_fmac_f32_e32 v164, v11, v205
	v_fmac_f32_e32 v165, v4, v177
	v_fmac_f32_e32 v162, v155, v170
	v_fmac_f32_e32 v163, v19, v197
	v_fmac_f32_e32 v164, v12, v204
	v_fmac_f32_e32 v165, v5, v192
	v_fmac_f32_e32 v162, v156, v169
	v_fmac_f32_e32 v163, v20, v195
	v_fmac_f32_e32 v164, v13, v203
	v_fmac_f32_e32 v165, v6, v193
	v_fmac_f32_e32 v162, v157, v168
	v_fmac_f32_e32 v163, v21, v175
	v_fmac_f32_e32 v164, v14, v202
	v_fmac_f32_e32 v165, v7, v194
	v_fma_f32 v167, v0, v167, v160
	s_waitcnt lgkmcnt(0)
	v_lshlrev_b32_e32 v161, 16, v161
	v_fmac_f32_e32 v162, v158, v166
	v_fmac_f32_e32 v163, v22, v173
	v_fmac_f32_e32 v164, v15, v201
	v_fmac_f32_e32 v165, v8, v196
	v_fmac_f32_e32 v167, v1, v174
	v_fmac_f32_e32 v162, v159, v161
	v_fmac_f32_e32 v163, v23, v172
	v_fmac_f32_e32 v164, v16, v200
	v_fmac_f32_e32 v165, v9, v198
	v_fmac_f32_e32 v167, v2, v176
	ds_write_b32 v79, v162
	ds_read_u16 v162, v35 offset:34816
	v_fmac_f32_e32 v163, v152, v171
	v_fmac_f32_e32 v164, v17, v199
	v_fmac_f32_e32 v165, v10, v205
	v_fmac_f32_e32 v167, v3, v177
	v_fmac_f32_e32 v163, v154, v170
	v_fmac_f32_e32 v164, v18, v197
	v_fmac_f32_e32 v165, v11, v204
	v_fmac_f32_e32 v167, v4, v192
	v_fmac_f32_e32 v163, v155, v169
	v_fmac_f32_e32 v164, v19, v195
	v_fmac_f32_e32 v165, v12, v203
	v_fmac_f32_e32 v167, v5, v193
	v_fmac_f32_e32 v163, v156, v168
	v_fmac_f32_e32 v164, v20, v175
	v_fmac_f32_e32 v165, v13, v202
	v_fmac_f32_e32 v167, v6, v194
	v_fmac_f32_e32 v163, v157, v166
	v_fmac_f32_e32 v164, v21, v173
	v_fmac_f32_e32 v165, v14, v201
	v_fmac_f32_e32 v167, v7, v196
	v_fma_f32 v174, v0, v174, v160
	s_waitcnt lgkmcnt(0)
	v_lshlrev_b32_e32 v162, 16, v162
	v_fmac_f32_e32 v163, v158, v161
	v_fmac_f32_e32 v164, v22, v172
	v_fmac_f32_e32 v165, v15, v200
	v_fmac_f32_e32 v167, v8, v198
	v_fmac_f32_e32 v174, v1, v176
	v_fmac_f32_e32 v163, v159, v162
	v_fmac_f32_e32 v164, v23, v171
	v_fmac_f32_e32 v165, v16, v199
	v_fmac_f32_e32 v167, v9, v205
	v_fmac_f32_e32 v174, v2, v177
	ds_write_b32 v80, v163
	ds_read_u16 v163, v35 offset:35840
	v_fmac_f32_e32 v164, v152, v170
	v_fmac_f32_e32 v165, v17, v197
	v_fmac_f32_e32 v167, v10, v204
	v_fmac_f32_e32 v174, v3, v192
	v_fmac_f32_e32 v164, v154, v169
	v_fmac_f32_e32 v165, v18, v195
	v_fmac_f32_e32 v167, v11, v203
	v_fmac_f32_e32 v174, v4, v193
	v_fmac_f32_e32 v164, v155, v168
	v_fmac_f32_e32 v165, v19, v175
	v_fmac_f32_e32 v167, v12, v202
	v_fmac_f32_e32 v174, v5, v194
	v_fmac_f32_e32 v164, v156, v166
	v_fmac_f32_e32 v165, v20, v173
	v_fmac_f32_e32 v167, v13, v201
	v_fmac_f32_e32 v174, v6, v196
	v_fmac_f32_e32 v164, v157, v161
	v_fmac_f32_e32 v165, v21, v172
	v_fmac_f32_e32 v167, v14, v200
	v_fmac_f32_e32 v174, v7, v198
	v_fma_f32 v176, v0, v176, v160
	s_waitcnt lgkmcnt(0)
; __device__ __forceinline__ void phase_even_mix(CArgs a, LAS unsigned char* lds, int i2, int wv, int xw  ) {
;     ...
; #pragma clang loop unroll(full)
;             for (int r = 0; r < 64; ++r) {
;                 win[r % 34] = bf2f(glu[r * 512 + c]);
;                 if (r >= 32) { float y = cb;
; #pragma unroll
;                     for (int k = 0; k < 31; ++k) y += w[k] * win[(r - 30 + k) % 34];
;                     ybuf[(r - 32) * 512 + c] = y; }
	v_lshlrev_b32_e32 v163, 16, v163
	v_fmac_f32_e32 v164, v158, v162
	v_fmac_f32_e32 v165, v22, v171
	v_fmac_f32_e32 v167, v15, v199
	v_fmac_f32_e32 v174, v8, v205
	v_fmac_f32_e32 v176, v1, v177
	v_fmac_f32_e32 v164, v159, v163
	v_fmac_f32_e32 v165, v23, v170
	v_fmac_f32_e32 v167, v16, v197
	v_fmac_f32_e32 v174, v9, v204
	v_fmac_f32_e32 v176, v2, v192
	ds_write_b32 v81, v164
	ds_read_u16 v164, v35 offset:36864
	v_fmac_f32_e32 v165, v152, v169
	v_fmac_f32_e32 v167, v17, v195
	v_fmac_f32_e32 v174, v10, v203
	v_fmac_f32_e32 v176, v3, v193
	v_fmac_f32_e32 v165, v154, v168
	v_fmac_f32_e32 v167, v18, v175
	v_fmac_f32_e32 v174, v11, v202
	v_fmac_f32_e32 v176, v4, v194
	v_fmac_f32_e32 v165, v155, v166
	v_fmac_f32_e32 v167, v19, v173
	v_fmac_f32_e32 v174, v12, v201
	v_fmac_f32_e32 v176, v5, v196
	v_fmac_f32_e32 v165, v156, v161
	v_fmac_f32_e32 v167, v20, v172
	v_fmac_f32_e32 v174, v13, v200
	v_fmac_f32_e32 v176, v6, v198
	v_fmac_f32_e32 v165, v157, v162
	v_fmac_f32_e32 v167, v21, v171
	v_fmac_f32_e32 v174, v14, v199
	v_fmac_f32_e32 v176, v7, v205
	v_fma_f32 v177, v0, v177, v160
	s_waitcnt lgkmcnt(0)
	v_lshlrev_b32_e32 v164, 16, v164
	v_fmac_f32_e32 v165, v158, v163
	v_fmac_f32_e32 v167, v22, v170
	v_fmac_f32_e32 v174, v15, v197
	v_fmac_f32_e32 v176, v8, v204
	v_fmac_f32_e32 v177, v1, v192
	v_fmac_f32_e32 v165, v159, v164
	v_fmac_f32_e32 v167, v23, v169
	v_fmac_f32_e32 v174, v16, v195
	v_fmac_f32_e32 v176, v9, v203
	v_fmac_f32_e32 v177, v2, v193
	ds_write_b32 v82, v165
	ds_read_u16 v165, v35 offset:37888
	v_fmac_f32_e32 v167, v152, v168
	v_fmac_f32_e32 v174, v17, v175
	v_fmac_f32_e32 v176, v10, v202
	v_fmac_f32_e32 v177, v3, v194
	v_fmac_f32_e32 v167, v154, v166
	v_fmac_f32_e32 v174, v18, v173
	v_fmac_f32_e32 v176, v11, v201
	v_fmac_f32_e32 v177, v4, v196
	v_fmac_f32_e32 v167, v155, v161
	v_fmac_f32_e32 v174, v19, v172
	v_fmac_f32_e32 v176, v12, v200
	v_fmac_f32_e32 v177, v5, v198
	v_fmac_f32_e32 v167, v156, v162
	v_fmac_f32_e32 v174, v20, v171
	v_fmac_f32_e32 v176, v13, v199
	v_fmac_f32_e32 v177, v6, v205
	v_fmac_f32_e32 v167, v157, v163
	v_fmac_f32_e32 v174, v21, v170
	v_fmac_f32_e32 v176, v14, v197
	v_fmac_f32_e32 v177, v7, v204
	s_waitcnt lgkmcnt(0)
	v_lshlrev_b32_e32 v165, 16, v165
	v_fmac_f32_e32 v167, v158, v164
	v_fmac_f32_e32 v174, v22, v169
	v_fmac_f32_e32 v176, v15, v195
	v_fmac_f32_e32 v177, v8, v203
	v_fmac_f32_e32 v167, v159, v165
	v_fmac_f32_e32 v174, v23, v168
	v_fmac_f32_e32 v176, v16, v175
	v_fmac_f32_e32 v177, v9, v202
	ds_write_b32 v83, v167
	ds_read_u16 v167, v35 offset:38912
	v_fmac_f32_e32 v174, v152, v166
	v_fmac_f32_e32 v176, v17, v173
	v_fmac_f32_e32 v177, v10, v201
	v_fmac_f32_e32 v174, v154, v161
	v_fmac_f32_e32 v176, v18, v172
	v_fmac_f32_e32 v177, v11, v200
	v_fmac_f32_e32 v174, v155, v162
	v_fmac_f32_e32 v176, v19, v171
	v_fmac_f32_e32 v177, v12, v199
	v_fmac_f32_e32 v174, v156, v163
	v_fmac_f32_e32 v176, v20, v170
	v_fmac_f32_e32 v177, v13, v197
	v_fmac_f32_e32 v174, v157, v164
	v_fmac_f32_e32 v176, v21, v169
	v_fmac_f32_e32 v177, v14, v195
	s_waitcnt lgkmcnt(0)
	v_lshlrev_b32_e32 v167, 16, v167
	v_fmac_f32_e32 v174, v158, v165
	v_fmac_f32_e32 v176, v22, v168
	v_fmac_f32_e32 v177, v15, v175
	v_fmac_f32_e32 v174, v159, v167
	v_fmac_f32_e32 v176, v23, v166
	v_fmac_f32_e32 v177, v16, v173
	ds_write_b32 v84, v174
	ds_read_u16 v174, v35 offset:39936
	v_fmac_f32_e32 v176, v152, v161
	v_fmac_f32_e32 v177, v17, v172
	v_fmac_f32_e32 v176, v154, v162
	v_fmac_f32_e32 v177, v18, v171
	v_fmac_f32_e32 v176, v155, v163
	v_fmac_f32_e32 v177, v19, v170
	v_fmac_f32_e32 v176, v156, v164
	v_fmac_f32_e32 v177, v20, v169
	v_fmac_f32_e32 v176, v157, v165
	v_fmac_f32_e32 v177, v21, v168
	s_waitcnt lgkmcnt(0)
	v_lshlrev_b32_e32 v174, 16, v174
	v_fmac_f32_e32 v176, v158, v167
	v_fmac_f32_e32 v177, v22, v166
	v_fmac_f32_e32 v176, v159, v174
	v_fmac_f32_e32 v177, v23, v161
	ds_write_b32 v85, v176
	ds_read_u16 v176, v35 offset:40960
	v_fmac_f32_e32 v177, v152, v162
	v_fmac_f32_e32 v177, v154, v163
	v_fmac_f32_e32 v177, v155, v164
	v_fmac_f32_e32 v177, v156, v165
	v_fmac_f32_e32 v178, v20, v168
	v_fmac_f32_e32 v177, v157, v167
	v_fmac_f32_e32 v178, v21, v166
	s_waitcnt lgkmcnt(0)
	v_lshlrev_b32_e32 v176, 16, v176
	v_fmac_f32_e32 v177, v158, v174
	v_fmac_f32_e32 v178, v22, v161
	v_fmac_f32_e32 v177, v159, v176
	v_fmac_f32_e32 v178, v23, v162
	ds_write_b32 v86, v177
	ds_read_u16 v177, v35 offset:41984
	v_fmac_f32_e32 v178, v152, v163
	v_fmac_f32_e32 v178, v154, v164
	v_fmac_f32_e32 v178, v155, v165
	v_fmac_f32_e32 v178, v156, v167
	v_fmac_f32_e32 v178, v157, v174
	s_waitcnt lgkmcnt(0)
	v_lshlrev_b32_e32 v177, 16, v177
	v_fmac_f32_e32 v178, v158, v176
	v_fmac_f32_e32 v178, v159, v177
	ds_write_b32 v87, v178
	ds_read_u16 v178, v35 offset:43008
	s_waitcnt lgkmcnt(0)
	v_lshlrev_b32_e32 v192, 16, v178
	v_fma_f32 v178, v0, v193, v160
	v_fmac_f32_e32 v178, v1, v194
	v_fmac_f32_e32 v178, v2, v196
	v_fmac_f32_e32 v178, v3, v198
	v_fmac_f32_e32 v178, v4, v205
	v_fmac_f32_e32 v178, v5, v204
	v_fmac_f32_e32 v178, v6, v203
	v_fmac_f32_e32 v178, v7, v202
	v_fmac_f32_e32 v178, v8, v201
	v_fmac_f32_e32 v178, v9, v200
	v_fmac_f32_e32 v178, v10, v199
	v_fmac_f32_e32 v178, v11, v197
	v_fmac_f32_e32 v178, v12, v195
	v_fmac_f32_e32 v178, v13, v175
	v_fmac_f32_e32 v178, v14, v173
	v_fmac_f32_e32 v178, v15, v172
	v_fmac_f32_e32 v178, v16, v171
	v_fmac_f32_e32 v178, v17, v170
	v_fmac_f32_e32 v178, v18, v169
	v_fmac_f32_e32 v178, v19, v168
	v_fmac_f32_e32 v178, v20, v166
	v_fmac_f32_e32 v178, v21, v161
	v_fmac_f32_e32 v178, v22, v162
	v_fmac_f32_e32 v178, v23, v163
	v_fmac_f32_e32 v178, v152, v164
	v_fmac_f32_e32 v178, v154, v165
	v_fmac_f32_e32 v178, v155, v167
	v_fmac_f32_e32 v178, v156, v174
	v_fmac_f32_e32 v178, v157, v176
	v_fmac_f32_e32 v178, v158, v177
	v_fmac_f32_e32 v178, v159, v192
	ds_write_b32 v88, v178
	ds_read_u16 v178, v35 offset:44032
	s_waitcnt lgkmcnt(0)
; __device__ __forceinline__ void phase_even_mix(CArgs a, LAS unsigned char* lds, int i2, int wv, int xw  ) {
;     ...
; #pragma clang loop unroll(full)
;             for (int r = 0; r < 64; ++r) {
;                 win[r % 34] = bf2f(glu[r * 512 + c]);
;                 if (r >= 32) { float y = cb;
; #pragma unroll
;                     for (int k = 0; k < 31; ++k) y += w[k] * win[(r - 30 + k) % 34];
;                     ybuf[(r - 32) * 512 + c] = y; }
	v_lshlrev_b32_e32 v193, 16, v178
	v_fma_f32 v178, v0, v194, v160
	v_fmac_f32_e32 v178, v1, v196
	v_fmac_f32_e32 v178, v2, v198
	v_fmac_f32_e32 v178, v3, v205
	v_fmac_f32_e32 v178, v4, v204
	v_fmac_f32_e32 v178, v5, v203
	v_fmac_f32_e32 v178, v6, v202
	v_fmac_f32_e32 v178, v7, v201
	v_fmac_f32_e32 v178, v8, v200
	v_fmac_f32_e32 v178, v9, v199
	v_fmac_f32_e32 v178, v10, v197
	v_fmac_f32_e32 v178, v11, v195
	v_fmac_f32_e32 v178, v12, v175
	v_fmac_f32_e32 v178, v13, v173
	v_fmac_f32_e32 v178, v14, v172
	v_fmac_f32_e32 v178, v15, v171
	v_fmac_f32_e32 v178, v16, v170
	v_fmac_f32_e32 v178, v17, v169
	v_fmac_f32_e32 v178, v18, v168
	v_fmac_f32_e32 v178, v19, v166
	v_fmac_f32_e32 v178, v20, v161
	v_fmac_f32_e32 v178, v21, v162
	v_fmac_f32_e32 v178, v22, v163
	v_fmac_f32_e32 v178, v23, v164
	v_fmac_f32_e32 v178, v152, v165
	v_fmac_f32_e32 v178, v154, v167
	v_fmac_f32_e32 v178, v155, v174
	v_fmac_f32_e32 v178, v156, v176
	v_fmac_f32_e32 v178, v157, v177
	v_fmac_f32_e32 v178, v158, v192
	v_fmac_f32_e32 v178, v159, v193
	ds_write_b32 v89, v178
	ds_read_u16 v178, v35 offset:45056
	s_waitcnt lgkmcnt(0)
	v_lshlrev_b32_e32 v194, 16, v178
	v_fma_f32 v178, v0, v196, v160
	v_fmac_f32_e32 v178, v1, v198
	v_fmac_f32_e32 v178, v2, v205
	v_fmac_f32_e32 v178, v3, v204
	v_fmac_f32_e32 v178, v4, v203
	v_fmac_f32_e32 v178, v5, v202
	v_fmac_f32_e32 v178, v6, v201
	v_fmac_f32_e32 v178, v7, v200
	v_fmac_f32_e32 v178, v8, v199
	v_fmac_f32_e32 v178, v9, v197
	v_fmac_f32_e32 v178, v10, v195
	v_fmac_f32_e32 v178, v11, v175
	v_fmac_f32_e32 v178, v12, v173
	v_fmac_f32_e32 v178, v13, v172
	v_fmac_f32_e32 v178, v14, v171
	v_fmac_f32_e32 v178, v15, v170
	v_fmac_f32_e32 v178, v16, v169
	v_fmac_f32_e32 v178, v17, v168
	v_fmac_f32_e32 v178, v18, v166
	v_fmac_f32_e32 v178, v19, v161
	v_fmac_f32_e32 v178, v20, v162
	v_fmac_f32_e32 v178, v21, v163
	v_fmac_f32_e32 v178, v22, v164
	v_fmac_f32_e32 v178, v23, v165
	v_fmac_f32_e32 v178, v152, v167
	v_fmac_f32_e32 v178, v154, v174
	v_fmac_f32_e32 v178, v155, v176
	v_fmac_f32_e32 v178, v156, v177
	v_fmac_f32_e32 v178, v157, v192
	v_fmac_f32_e32 v178, v158, v193
	v_fmac_f32_e32 v178, v159, v194
	ds_write_b32 v90, v178
	ds_read_u16 v178, v35 offset:46080
	s_waitcnt lgkmcnt(0)
	v_lshlrev_b32_e32 v196, 16, v178
	v_fma_f32 v178, v0, v198, v160
	v_fmac_f32_e32 v178, v1, v205
	v_fmac_f32_e32 v178, v2, v204
	v_fmac_f32_e32 v178, v3, v203
	v_fmac_f32_e32 v178, v4, v202
	v_fmac_f32_e32 v178, v5, v201
	v_fmac_f32_e32 v178, v6, v200
	v_fmac_f32_e32 v178, v7, v199
	v_fmac_f32_e32 v178, v8, v197
	v_fmac_f32_e32 v178, v9, v195
	v_fmac_f32_e32 v178, v10, v175
	v_fmac_f32_e32 v178, v11, v173
	v_fmac_f32_e32 v178, v12, v172
	v_fmac_f32_e32 v178, v13, v171
	v_fmac_f32_e32 v178, v14, v170
	v_fmac_f32_e32 v178, v15, v169
	v_fmac_f32_e32 v178, v16, v168
	v_fmac_f32_e32 v178, v17, v166
	v_fmac_f32_e32 v178, v18, v161
	v_fmac_f32_e32 v178, v19, v162
	v_fmac_f32_e32 v178, v20, v163
	v_fmac_f32_e32 v178, v21, v164
	v_fmac_f32_e32 v178, v22, v165
	v_fmac_f32_e32 v178, v23, v167
	v_fmac_f32_e32 v178, v152, v174
	v_fmac_f32_e32 v178, v154, v176
	v_fmac_f32_e32 v178, v155, v177
	v_fmac_f32_e32 v178, v156, v192
	v_fmac_f32_e32 v178, v157, v193
	v_fmac_f32_e32 v178, v158, v194
	v_fmac_f32_e32 v178, v159, v196
	ds_write_b32 v91, v178
	ds_read_u16 v178, v35 offset:47104
	s_waitcnt lgkmcnt(0)
	v_lshlrev_b32_e32 v198, 16, v178
	v_fma_f32 v178, v0, v205, v160
	v_fmac_f32_e32 v178, v1, v204
	v_fmac_f32_e32 v178, v2, v203
	v_fmac_f32_e32 v178, v3, v202
	v_fmac_f32_e32 v178, v4, v201
	v_fmac_f32_e32 v178, v5, v200
	v_fmac_f32_e32 v178, v6, v199
	v_fmac_f32_e32 v178, v7, v197
	v_fmac_f32_e32 v178, v8, v195
	v_fmac_f32_e32 v178, v9, v175
	v_fmac_f32_e32 v178, v10, v173
	v_fmac_f32_e32 v178, v11, v172
	v_fmac_f32_e32 v178, v12, v171
	v_fmac_f32_e32 v178, v13, v170
	v_fmac_f32_e32 v178, v14, v169
	v_fmac_f32_e32 v178, v15, v168
	v_fmac_f32_e32 v178, v16, v166
	v_fmac_f32_e32 v178, v17, v161
	v_fmac_f32_e32 v178, v18, v162
	v_fmac_f32_e32 v178, v19, v163
	v_fmac_f32_e32 v178, v20, v164
	v_fmac_f32_e32 v178, v21, v165
	v_fmac_f32_e32 v178, v22, v167
	v_fmac_f32_e32 v178, v23, v174
	v_fmac_f32_e32 v178, v152, v176
	v_fmac_f32_e32 v178, v154, v177
	v_fmac_f32_e32 v178, v155, v192
	v_fmac_f32_e32 v178, v156, v193
	v_fmac_f32_e32 v178, v157, v194
	v_fmac_f32_e32 v178, v158, v196
	v_fmac_f32_e32 v178, v159, v198
	ds_write_b32 v92, v178
	v_fma_f32 v178, v0, v204, v160
	v_fmac_f32_e32 v178, v1, v203
	v_fmac_f32_e32 v178, v2, v202
	v_fmac_f32_e32 v178, v3, v201
	v_fmac_f32_e32 v178, v4, v200
	v_fmac_f32_e32 v178, v5, v199
	v_fmac_f32_e32 v178, v6, v197
	v_fmac_f32_e32 v178, v7, v195
	v_fmac_f32_e32 v178, v8, v175
	v_fmac_f32_e32 v178, v9, v173
	v_fmac_f32_e32 v178, v10, v172
	v_fmac_f32_e32 v178, v11, v171
	v_fmac_f32_e32 v178, v12, v170
	v_fmac_f32_e32 v178, v13, v169
	v_fmac_f32_e32 v178, v14, v168
	v_fmac_f32_e32 v178, v15, v166
	v_fmac_f32_e32 v178, v16, v161
	v_fmac_f32_e32 v178, v17, v162
	v_fmac_f32_e32 v178, v18, v163
	v_fmac_f32_e32 v178, v19, v164
	v_fmac_f32_e32 v178, v20, v165
	v_fmac_f32_e32 v178, v21, v167
	v_fmac_f32_e32 v178, v22, v174
	v_fmac_f32_e32 v178, v23, v176
	ds_read_u16 v205, v35 offset:48128
	v_fmac_f32_e32 v178, v152, v177
	v_fmac_f32_e32 v178, v154, v192
	v_fmac_f32_e32 v178, v155, v193
	v_fmac_f32_e32 v178, v156, v194
	v_fmac_f32_e32 v178, v157, v196
	s_waitcnt lgkmcnt(0)
	v_lshlrev_b32_e32 v205, 16, v205
	v_fmac_f32_e32 v178, v158, v198
	v_fmac_f32_e32 v178, v159, v205
	ds_write_b32 v93, v178
	ds_read_u16 v178, v35 offset:49152
	s_waitcnt lgkmcnt(0)
; __device__ __forceinline__ void phase_even_mix(CArgs a, LAS unsigned char* lds, int i2, int wv, int xw  ) {
;     ...
; #pragma clang loop unroll(full)
;             for (int r = 0; r < 64; ++r) {
;                 win[r % 34] = bf2f(glu[r * 512 + c]);
;                 if (r >= 32) { float y = cb;
; #pragma unroll
;                     for (int k = 0; k < 31; ++k) y += w[k] * win[(r - 30 + k) % 34];
;                     ybuf[(r - 32) * 512 + c] = y; }
	v_lshlrev_b32_e32 v204, 16, v178
	v_fma_f32 v178, v0, v203, v160
	v_fmac_f32_e32 v178, v1, v202
	v_fmac_f32_e32 v178, v2, v201
	v_fmac_f32_e32 v178, v3, v200
	v_fmac_f32_e32 v178, v4, v199
	v_fmac_f32_e32 v178, v5, v197
	v_fmac_f32_e32 v178, v6, v195
	v_fmac_f32_e32 v178, v7, v175
	v_fmac_f32_e32 v178, v8, v173
	v_fmac_f32_e32 v178, v9, v172
	v_fmac_f32_e32 v178, v10, v171
	v_fmac_f32_e32 v178, v11, v170
	v_fmac_f32_e32 v178, v12, v169
	v_fmac_f32_e32 v178, v13, v168
	v_fmac_f32_e32 v178, v14, v166
	v_fmac_f32_e32 v178, v15, v161
	v_fmac_f32_e32 v178, v16, v162
	v_fmac_f32_e32 v178, v17, v163
	v_fmac_f32_e32 v178, v18, v164
	v_fmac_f32_e32 v178, v19, v165
	v_fmac_f32_e32 v178, v20, v167
	v_fmac_f32_e32 v178, v21, v174
	v_fmac_f32_e32 v178, v22, v176
	v_fmac_f32_e32 v178, v23, v177
	v_fmac_f32_e32 v178, v152, v192
	v_fmac_f32_e32 v178, v154, v193
	v_fmac_f32_e32 v178, v155, v194
	v_fmac_f32_e32 v178, v156, v196
	v_fmac_f32_e32 v178, v157, v198
	v_fmac_f32_e32 v178, v158, v205
	v_fmac_f32_e32 v178, v159, v204
	ds_write_b32 v94, v178
	ds_read_u16 v178, v35 offset:50176
	s_waitcnt lgkmcnt(0)
	v_lshlrev_b32_e32 v203, 16, v178
	v_fma_f32 v178, v0, v202, v160
	v_fmac_f32_e32 v178, v1, v201
	v_fmac_f32_e32 v178, v2, v200
	v_fmac_f32_e32 v178, v3, v199
	v_fmac_f32_e32 v178, v4, v197
	v_fmac_f32_e32 v178, v5, v195
	v_fmac_f32_e32 v178, v6, v175
	v_fmac_f32_e32 v178, v7, v173
	v_fmac_f32_e32 v178, v8, v172
	v_fmac_f32_e32 v178, v9, v171
	v_fmac_f32_e32 v178, v10, v170
	v_fmac_f32_e32 v178, v11, v169
	v_fmac_f32_e32 v178, v12, v168
	v_fmac_f32_e32 v178, v13, v166
	v_fmac_f32_e32 v178, v14, v161
	v_fmac_f32_e32 v178, v15, v162
	v_fmac_f32_e32 v178, v16, v163
	v_fmac_f32_e32 v178, v17, v164
	v_fmac_f32_e32 v178, v18, v165
	v_fmac_f32_e32 v178, v19, v167
	v_fmac_f32_e32 v178, v20, v174
	v_fmac_f32_e32 v178, v21, v176
	v_fmac_f32_e32 v178, v22, v177
	v_fmac_f32_e32 v178, v23, v192
	v_fmac_f32_e32 v178, v152, v193
	v_fmac_f32_e32 v178, v154, v194
	v_fmac_f32_e32 v178, v155, v196
	v_fmac_f32_e32 v178, v156, v198
	v_fmac_f32_e32 v178, v157, v205
	v_fmac_f32_e32 v178, v158, v204
	v_fmac_f32_e32 v178, v159, v203
	ds_write_b32 v95, v178
	ds_read_u16 v178, v35 offset:51200
	s_waitcnt lgkmcnt(0)
	v_lshlrev_b32_e32 v202, 16, v178
	v_fma_f32 v178, v0, v201, v160
	v_fmac_f32_e32 v178, v1, v200
	v_fmac_f32_e32 v178, v2, v199
	v_fmac_f32_e32 v178, v3, v197
	v_fmac_f32_e32 v178, v4, v195
	v_fmac_f32_e32 v178, v5, v175
	v_fmac_f32_e32 v178, v6, v173
	v_fmac_f32_e32 v178, v7, v172
	v_fmac_f32_e32 v178, v8, v171
	v_fmac_f32_e32 v178, v9, v170
	v_fmac_f32_e32 v178, v10, v169
	v_fmac_f32_e32 v178, v11, v168
	v_fmac_f32_e32 v178, v12, v166
	v_fmac_f32_e32 v178, v13, v161
	v_fmac_f32_e32 v178, v14, v162
	v_fmac_f32_e32 v178, v15, v163
	v_fmac_f32_e32 v178, v16, v164
	v_fmac_f32_e32 v178, v17, v165
	v_fmac_f32_e32 v178, v18, v167
	v_fmac_f32_e32 v178, v19, v174
	v_fmac_f32_e32 v178, v20, v176
	v_fmac_f32_e32 v178, v21, v177
	v_fmac_f32_e32 v178, v22, v192
	v_fmac_f32_e32 v178, v23, v193
	v_fmac_f32_e32 v178, v152, v194
	v_fmac_f32_e32 v178, v154, v196
	v_fmac_f32_e32 v178, v155, v198
	v_fmac_f32_e32 v178, v156, v205
	v_fmac_f32_e32 v178, v157, v204
	v_fmac_f32_e32 v178, v158, v203
	v_fmac_f32_e32 v178, v159, v202
	ds_write_b32 v96, v178
	ds_read_u16 v178, v35 offset:52224
	s_waitcnt lgkmcnt(0)
	v_lshlrev_b32_e32 v201, 16, v178
	v_fma_f32 v178, v0, v200, v160
	v_fmac_f32_e32 v178, v1, v199
	v_fmac_f32_e32 v178, v2, v197
	v_fmac_f32_e32 v178, v3, v195
	v_fmac_f32_e32 v178, v4, v175
	v_fmac_f32_e32 v178, v5, v173
	v_fmac_f32_e32 v178, v6, v172
	v_fmac_f32_e32 v178, v7, v171
	v_fmac_f32_e32 v178, v8, v170
	v_fmac_f32_e32 v178, v9, v169
	v_fmac_f32_e32 v178, v10, v168
	v_fmac_f32_e32 v178, v11, v166
	v_fmac_f32_e32 v178, v12, v161
	v_fmac_f32_e32 v178, v13, v162
	v_fmac_f32_e32 v178, v14, v163
	v_fmac_f32_e32 v178, v15, v164
	v_fmac_f32_e32 v178, v16, v165
	v_fmac_f32_e32 v178, v17, v167
	v_fmac_f32_e32 v178, v18, v174
	v_fmac_f32_e32 v178, v19, v176
	v_fmac_f32_e32 v178, v20, v177
	v_fmac_f32_e32 v178, v21, v192
	v_fmac_f32_e32 v178, v22, v193
	v_fmac_f32_e32 v178, v23, v194
	v_fmac_f32_e32 v178, v152, v196
	v_fmac_f32_e32 v178, v154, v198
	v_fmac_f32_e32 v178, v155, v205
	v_fmac_f32_e32 v178, v156, v204
	v_fmac_f32_e32 v178, v157, v203
	v_fmac_f32_e32 v178, v158, v202
	v_fmac_f32_e32 v178, v159, v201
	ds_write_b32 v97, v178
	ds_read_u16 v178, v35 offset:53248
	s_waitcnt lgkmcnt(0)
	v_lshlrev_b32_e32 v200, 16, v178
	v_fma_f32 v178, v0, v199, v160
	v_fmac_f32_e32 v178, v1, v197
	v_fmac_f32_e32 v178, v2, v195
	v_fmac_f32_e32 v178, v3, v175
	v_fmac_f32_e32 v178, v4, v173
	v_fmac_f32_e32 v178, v5, v172
	v_fmac_f32_e32 v178, v6, v171
	v_fmac_f32_e32 v178, v7, v170
	v_fmac_f32_e32 v178, v8, v169
	v_fmac_f32_e32 v178, v9, v168
	v_fmac_f32_e32 v178, v10, v166
	v_fmac_f32_e32 v178, v11, v161
	v_fmac_f32_e32 v178, v12, v162
	v_fmac_f32_e32 v178, v13, v163
	v_fmac_f32_e32 v178, v14, v164
	v_fmac_f32_e32 v178, v15, v165
	v_fmac_f32_e32 v178, v16, v167
	v_fmac_f32_e32 v178, v17, v174
	v_fmac_f32_e32 v178, v18, v176
	v_fmac_f32_e32 v178, v19, v177
	v_fmac_f32_e32 v178, v20, v192
	v_fmac_f32_e32 v178, v21, v193
	v_fmac_f32_e32 v178, v22, v194
	v_fmac_f32_e32 v178, v23, v196
	v_fmac_f32_e32 v178, v152, v198
	v_fmac_f32_e32 v178, v154, v205
	v_fmac_f32_e32 v178, v155, v204
	v_fmac_f32_e32 v178, v156, v203
	v_fmac_f32_e32 v178, v157, v202
	v_fmac_f32_e32 v178, v158, v201
	v_fmac_f32_e32 v178, v159, v200
	ds_write_b32 v98, v178
	ds_read_u16 v178, v35 offset:54272
	s_waitcnt lgkmcnt(0)
; __device__ __forceinline__ void phase_even_mix(CArgs a, LAS unsigned char* lds, int i2, int wv, int xw  ) {
;     ...
;             for (int r = 0; r < 64; ++r) {
;                 win[r % 34] = bf2f(glu[r * 512 + c]);
;                 if (r >= 32) { float y = cb;
; #pragma unroll
;                     for (int k = 0; k < 31; ++k) y += w[k] * win[(r - 30 + k) % 34];
;                     ybuf[(r - 32) * 512 + c] = y; }
	v_lshlrev_b32_e32 v199, 16, v178
	v_fma_f32 v178, v0, v197, v160
	v_fmac_f32_e32 v178, v1, v195
	v_fmac_f32_e32 v178, v2, v175
	v_fmac_f32_e32 v178, v3, v173
	v_fmac_f32_e32 v178, v4, v172
	v_fmac_f32_e32 v178, v5, v171
	v_fmac_f32_e32 v178, v6, v170
	v_fmac_f32_e32 v178, v7, v169
	v_fmac_f32_e32 v178, v8, v168
	v_fmac_f32_e32 v178, v9, v166
	v_fmac_f32_e32 v178, v10, v161
	v_fmac_f32_e32 v178, v11, v162
	v_fmac_f32_e32 v178, v12, v163
	v_fmac_f32_e32 v178, v13, v164
	v_fmac_f32_e32 v178, v14, v165
	v_fmac_f32_e32 v178, v15, v167
	v_fmac_f32_e32 v178, v16, v174
	v_fmac_f32_e32 v178, v17, v176
	v_fmac_f32_e32 v178, v18, v177
	v_fmac_f32_e32 v178, v19, v192
	v_fmac_f32_e32 v178, v20, v193
	v_fmac_f32_e32 v178, v21, v194
	v_fmac_f32_e32 v178, v22, v196
	v_fmac_f32_e32 v178, v23, v198
	v_fmac_f32_e32 v178, v152, v205
	v_fmac_f32_e32 v178, v154, v204
	v_fmac_f32_e32 v178, v155, v203
	v_fmac_f32_e32 v178, v156, v202
	v_fmac_f32_e32 v178, v157, v201
	v_fmac_f32_e32 v178, v158, v200
	v_fmac_f32_e32 v178, v159, v199
	ds_write_b32 v99, v178
	ds_read_u16 v178, v35 offset:55296
	s_waitcnt lgkmcnt(0)
	v_lshlrev_b32_e32 v197, 16, v178
	v_fma_f32 v178, v0, v195, v160
	v_fmac_f32_e32 v178, v1, v175
	v_fma_f32 v175, v0, v175, v160
	v_fmac_f32_e32 v175, v1, v173
	v_fmac_f32_e32 v175, v2, v172
	v_fmac_f32_e32 v175, v3, v171
	v_fmac_f32_e32 v175, v4, v170
	v_fmac_f32_e32 v175, v5, v169
	v_fmac_f32_e32 v175, v6, v168
	v_fmac_f32_e32 v178, v2, v173
	v_fmac_f32_e32 v175, v7, v166
	v_fma_f32 v173, v0, v173, v160
	v_fmac_f32_e32 v175, v8, v161
	v_fmac_f32_e32 v173, v1, v172
	v_fmac_f32_e32 v175, v9, v162
	v_fmac_f32_e32 v173, v2, v171
	v_fmac_f32_e32 v175, v10, v163
	v_fmac_f32_e32 v173, v3, v170
	v_fmac_f32_e32 v175, v11, v164
	v_fmac_f32_e32 v173, v4, v169
	v_fmac_f32_e32 v175, v12, v165
	v_fmac_f32_e32 v173, v5, v168
	v_fmac_f32_e32 v175, v13, v167
	v_fmac_f32_e32 v173, v6, v166
	v_fmac_f32_e32 v178, v3, v172
	v_fmac_f32_e32 v175, v14, v174
	v_fmac_f32_e32 v173, v7, v161
	v_fma_f32 v172, v0, v172, v160
	v_fmac_f32_e32 v175, v15, v176
	v_fmac_f32_e32 v173, v8, v162
	v_fmac_f32_e32 v172, v1, v171
	v_fmac_f32_e32 v175, v16, v177
	v_fmac_f32_e32 v173, v9, v163
	v_fmac_f32_e32 v172, v2, v170
	v_fmac_f32_e32 v175, v17, v192
	v_fmac_f32_e32 v173, v10, v164
	v_fmac_f32_e32 v172, v3, v169
	v_fmac_f32_e32 v175, v18, v193
	v_fmac_f32_e32 v173, v11, v165
	v_fmac_f32_e32 v172, v4, v168
	v_fmac_f32_e32 v175, v19, v194
	v_fmac_f32_e32 v173, v12, v167
	v_fmac_f32_e32 v172, v5, v166
	v_fmac_f32_e32 v175, v20, v196
	v_fmac_f32_e32 v173, v13, v174
	v_fmac_f32_e32 v172, v6, v161
	v_fmac_f32_e32 v178, v4, v171
	v_fmac_f32_e32 v175, v21, v198
	v_fmac_f32_e32 v173, v14, v176
	v_fmac_f32_e32 v172, v7, v162
	v_fma_f32 v171, v0, v171, v160
	v_fmac_f32_e32 v175, v22, v205
	v_fmac_f32_e32 v173, v15, v177
	v_fmac_f32_e32 v172, v8, v163
	v_fmac_f32_e32 v171, v1, v170
	v_fmac_f32_e32 v175, v23, v204
	v_fmac_f32_e32 v173, v16, v192
	v_fmac_f32_e32 v172, v9, v164
	v_fmac_f32_e32 v171, v2, v169
	ds_read_u16 v195, v35 offset:56320
	v_fmac_f32_e32 v175, v152, v203
	v_fmac_f32_e32 v173, v17, v193
	v_fmac_f32_e32 v172, v10, v165
	v_fmac_f32_e32 v171, v3, v168
	v_fmac_f32_e32 v175, v154, v202
	v_fmac_f32_e32 v173, v18, v194
	v_fmac_f32_e32 v172, v11, v167
	v_fmac_f32_e32 v171, v4, v166
	v_fmac_f32_e32 v175, v155, v201
	v_fmac_f32_e32 v173, v19, v196
	v_fmac_f32_e32 v172, v12, v174
	v_fmac_f32_e32 v171, v5, v161
	v_fmac_f32_e32 v175, v156, v200
	v_fmac_f32_e32 v173, v20, v198
	v_fmac_f32_e32 v172, v13, v176
	v_fmac_f32_e32 v171, v6, v162
	v_fmac_f32_e32 v178, v5, v170
	v_fmac_f32_e32 v175, v157, v199
	v_fmac_f32_e32 v173, v21, v205
	v_fmac_f32_e32 v172, v14, v177
	v_fmac_f32_e32 v171, v7, v163
	v_fma_f32 v170, v0, v170, v160
	s_waitcnt lgkmcnt(0)
	v_lshlrev_b32_e32 v195, 16, v195
	v_fmac_f32_e32 v175, v158, v197
	v_fmac_f32_e32 v173, v22, v204
	v_fmac_f32_e32 v172, v15, v192
	v_fmac_f32_e32 v171, v8, v164
	v_fmac_f32_e32 v170, v1, v169
	v_fmac_f32_e32 v175, v159, v195
	v_fmac_f32_e32 v173, v23, v203
	v_fmac_f32_e32 v172, v16, v193
	v_fmac_f32_e32 v171, v9, v165
	v_fmac_f32_e32 v170, v2, v168
	ds_write_b32 v101, v175
	ds_read_u16 v175, v35 offset:57344
	v_fmac_f32_e32 v173, v152, v202
	v_fmac_f32_e32 v172, v17, v194
	v_fmac_f32_e32 v171, v10, v167
	v_fmac_f32_e32 v170, v3, v166
	v_fmac_f32_e32 v173, v154, v201
	v_fmac_f32_e32 v172, v18, v196
	v_fmac_f32_e32 v171, v11, v174
	v_fmac_f32_e32 v170, v4, v161
	v_fmac_f32_e32 v173, v155, v200
	v_fmac_f32_e32 v172, v19, v198
	v_fmac_f32_e32 v171, v12, v176
	v_fmac_f32_e32 v170, v5, v162
	v_fmac_f32_e32 v173, v156, v199
	v_fmac_f32_e32 v172, v20, v205
	v_fmac_f32_e32 v171, v13, v177
	v_fmac_f32_e32 v170, v6, v163
	v_fmac_f32_e32 v178, v6, v169
	v_fmac_f32_e32 v173, v157, v197
	v_fmac_f32_e32 v172, v21, v204
	v_fmac_f32_e32 v171, v14, v192
	v_fmac_f32_e32 v170, v7, v164
	v_fma_f32 v169, v0, v169, v160
	s_waitcnt lgkmcnt(0)
	v_lshlrev_b32_e32 v175, 16, v175
	v_fmac_f32_e32 v173, v158, v195
	v_fmac_f32_e32 v172, v22, v203
	v_fmac_f32_e32 v171, v15, v193
	v_fmac_f32_e32 v170, v8, v165
	v_fmac_f32_e32 v169, v1, v168
	v_fmac_f32_e32 v173, v159, v175
	v_fmac_f32_e32 v172, v23, v202
	v_fmac_f32_e32 v171, v16, v194
	v_fmac_f32_e32 v170, v9, v167
	v_fmac_f32_e32 v169, v2, v166
	ds_write_b32 v102, v173
	ds_read_u16 v173, v35 offset:58368
	v_fmac_f32_e32 v172, v152, v201
	v_fmac_f32_e32 v171, v17, v196
	v_fmac_f32_e32 v170, v10, v174
	v_fmac_f32_e32 v169, v3, v161
	v_fmac_f32_e32 v172, v154, v200
	v_fmac_f32_e32 v171, v18, v198
	v_fmac_f32_e32 v170, v11, v176
	v_fmac_f32_e32 v169, v4, v162
	v_fmac_f32_e32 v172, v155, v199
	v_fmac_f32_e32 v171, v19, v205
	v_fmac_f32_e32 v170, v12, v177
	v_fmac_f32_e32 v169, v5, v163
	v_fmac_f32_e32 v172, v156, v197
	v_fmac_f32_e32 v171, v20, v204
	v_fmac_f32_e32 v170, v13, v192
	v_fmac_f32_e32 v169, v6, v164
	v_fmac_f32_e32 v178, v7, v168
	v_fmac_f32_e32 v172, v157, v195
	v_fmac_f32_e32 v171, v21, v203
	v_fmac_f32_e32 v170, v14, v193
	v_fmac_f32_e32 v169, v7, v165
	v_fma_f32 v168, v0, v168, v160
	s_waitcnt lgkmcnt(0)
; #define LAS __attribute__((address_space(3)))
; __device__ __forceinline__ void phase_even_mix(CArgs a, LAS unsigned char* lds, int i2, int wv, int xw  ) {
;     ...
;             for (int r = 0; r < 64; ++r) {
;                 win[r % 34] = bf2f(glu[r * 512 + c]);
;                 if (r >= 32) { float y = cb;
; #pragma unroll
;                     for (int k = 0; k < 31; ++k) y += w[k] * win[(r - 30 + k) % 34];
;                     ybuf[(r - 32) * 512 + c] = y; }
;             }
;         }
;         __syncthreads();
; #pragma unroll
;         for (int it = 0; it < 6; ++it) { const int item = it * NTHR + tid, tt = item >> 6, cg = item & 63, p = t0 - 16 + tt;
;             u32x4 o = (u32x4){0u, 0u, 0u, 0u};
;             if (p >= 0) o = *(const u32x4*)(HB + ((size_t)b * SEQ + p) * EVEN_IN + cg * 8);
;             *(LAS u32x4*)(glu + tt * 512 + cg * 8) = o; }
	v_lshlrev_b32_e32 v173, 16, v173
	v_fmac_f32_e32 v172, v158, v175
	v_fmac_f32_e32 v171, v22, v202
	v_fmac_f32_e32 v170, v15, v194
	v_fmac_f32_e32 v169, v8, v167
	v_fmac_f32_e32 v168, v1, v166
	v_fmac_f32_e32 v172, v159, v173
	v_fmac_f32_e32 v171, v23, v201
	v_fmac_f32_e32 v170, v16, v196
	v_fmac_f32_e32 v169, v9, v174
	v_fmac_f32_e32 v168, v2, v161
	ds_write_b32 v103, v172
	ds_read_u16 v172, v35 offset:59392
	v_fmac_f32_e32 v171, v152, v200
	v_fmac_f32_e32 v170, v17, v198
	v_fmac_f32_e32 v169, v10, v176
	v_fmac_f32_e32 v168, v3, v162
	v_fmac_f32_e32 v171, v154, v199
	v_fmac_f32_e32 v170, v18, v205
	v_fmac_f32_e32 v169, v11, v177
	v_fmac_f32_e32 v168, v4, v163
	v_fmac_f32_e32 v171, v155, v197
	v_fmac_f32_e32 v170, v19, v204
	v_fmac_f32_e32 v169, v12, v192
	v_fmac_f32_e32 v168, v5, v164
	v_fmac_f32_e32 v171, v156, v195
	v_fmac_f32_e32 v170, v20, v203
	v_fmac_f32_e32 v169, v13, v193
	v_fmac_f32_e32 v168, v6, v165
	v_fmac_f32_e32 v178, v8, v166
	v_fmac_f32_e32 v171, v157, v175
	v_fmac_f32_e32 v170, v21, v202
	v_fmac_f32_e32 v169, v14, v194
	v_fmac_f32_e32 v168, v7, v167
	v_fma_f32 v166, v0, v166, v160
	s_waitcnt lgkmcnt(0)
	v_lshlrev_b32_e32 v172, 16, v172
	v_fmac_f32_e32 v171, v158, v173
	v_fmac_f32_e32 v170, v22, v201
	v_fmac_f32_e32 v169, v15, v196
	v_fmac_f32_e32 v168, v8, v174
	v_fmac_f32_e32 v166, v1, v161
	v_fmac_f32_e32 v171, v159, v172
	v_fmac_f32_e32 v170, v23, v200
	v_fmac_f32_e32 v169, v16, v198
	v_fmac_f32_e32 v168, v9, v176
	v_fmac_f32_e32 v166, v2, v162
	ds_write_b32 v104, v171
	ds_read_u16 v171, v35 offset:60416
	v_fmac_f32_e32 v170, v152, v199
	v_fmac_f32_e32 v169, v17, v205
	v_fmac_f32_e32 v168, v10, v177
	v_fmac_f32_e32 v166, v3, v163
	v_fmac_f32_e32 v170, v154, v197
	v_fmac_f32_e32 v169, v18, v204
	v_fmac_f32_e32 v168, v11, v192
	v_fmac_f32_e32 v166, v4, v164
	v_fmac_f32_e32 v170, v155, v195
	v_fmac_f32_e32 v169, v19, v203
	v_fmac_f32_e32 v168, v12, v193
	v_fmac_f32_e32 v166, v5, v165
	v_fmac_f32_e32 v170, v156, v175
	v_fmac_f32_e32 v169, v20, v202
	v_fmac_f32_e32 v168, v13, v194
	v_fmac_f32_e32 v166, v6, v167
	v_fmac_f32_e32 v170, v157, v173
	v_fmac_f32_e32 v169, v21, v201
	v_fmac_f32_e32 v168, v14, v196
	v_fmac_f32_e32 v166, v7, v174
	v_fmac_f32_e32 v160, v0, v161
	s_waitcnt lgkmcnt(0)
	v_lshlrev_b32_e32 v171, 16, v171
	v_fmac_f32_e32 v170, v158, v172
	v_fmac_f32_e32 v169, v22, v200
	v_fmac_f32_e32 v168, v15, v198
	v_fmac_f32_e32 v166, v8, v176
	v_fmac_f32_e32 v160, v1, v162
	v_fmac_f32_e32 v170, v159, v171
	v_fmac_f32_e32 v169, v23, v199
	v_fmac_f32_e32 v168, v16, v205
	v_fmac_f32_e32 v166, v9, v177
	v_fmac_f32_e32 v160, v2, v163
	ds_write_b32 v105, v170
	ds_read_u16 v170, v35 offset:61440
	v_fmac_f32_e32 v169, v152, v197
	v_fmac_f32_e32 v168, v17, v204
	v_fmac_f32_e32 v166, v10, v192
	v_fmac_f32_e32 v160, v3, v164
	v_fmac_f32_e32 v169, v154, v195
	v_fmac_f32_e32 v168, v18, v203
	v_fmac_f32_e32 v166, v11, v193
	v_fmac_f32_e32 v160, v4, v165
	v_fmac_f32_e32 v169, v155, v175
	v_fmac_f32_e32 v168, v19, v202
	v_fmac_f32_e32 v166, v12, v194
	v_fmac_f32_e32 v160, v5, v167
	v_fmac_f32_e32 v169, v156, v173
	v_fmac_f32_e32 v168, v20, v201
	v_fmac_f32_e32 v166, v13, v196
	v_fmac_f32_e32 v160, v6, v174
	v_fmac_f32_e32 v169, v157, v172
	v_fmac_f32_e32 v168, v21, v200
	v_fmac_f32_e32 v166, v14, v198
	v_fmac_f32_e32 v160, v7, v176
	s_waitcnt lgkmcnt(0)
	v_lshlrev_b32_e32 v170, 16, v170
	v_fmac_f32_e32 v169, v158, v171
	v_fmac_f32_e32 v168, v22, v199
	v_fmac_f32_e32 v166, v15, v205
	v_fmac_f32_e32 v160, v8, v177
	v_fmac_f32_e32 v178, v9, v161
	v_fmac_f32_e32 v169, v159, v170
	v_fmac_f32_e32 v168, v23, v197
	v_fmac_f32_e32 v166, v16, v204
	v_fmac_f32_e32 v160, v9, v192
	v_fmac_f32_e32 v178, v10, v162
	ds_write_b32 v106, v169
	ds_read_u16 v169, v35 offset:62464
	v_fmac_f32_e32 v168, v152, v195
	v_fmac_f32_e32 v166, v17, v203
	v_fmac_f32_e32 v160, v10, v193
	v_fmac_f32_e32 v178, v11, v163
	v_fmac_f32_e32 v168, v154, v175
	v_fmac_f32_e32 v166, v18, v202
	v_fmac_f32_e32 v160, v11, v194
	v_fmac_f32_e32 v178, v12, v164
	v_fmac_f32_e32 v168, v155, v173
	v_fmac_f32_e32 v166, v19, v201
	v_fmac_f32_e32 v160, v12, v196
	v_fmac_f32_e32 v178, v13, v165
	v_fmac_f32_e32 v168, v156, v172
	v_fmac_f32_e32 v166, v20, v200
	v_fmac_f32_e32 v160, v13, v198
	v_fmac_f32_e32 v178, v14, v167
	v_fmac_f32_e32 v168, v157, v171
	v_fmac_f32_e32 v166, v21, v199
	v_fmac_f32_e32 v160, v14, v205
	v_fmac_f32_e32 v178, v15, v174
	s_waitcnt lgkmcnt(0)
	v_lshlrev_b32_e32 v169, 16, v169
	v_fmac_f32_e32 v168, v158, v170
	v_fmac_f32_e32 v166, v22, v197
	v_fmac_f32_e32 v160, v15, v204
	v_fmac_f32_e32 v178, v16, v176
	v_fmac_f32_e32 v168, v159, v169
	v_fmac_f32_e32 v166, v23, v195
	v_fmac_f32_e32 v160, v16, v203
	v_fmac_f32_e32 v178, v17, v177
	ds_write_b32 v107, v168
	ds_read_u16 v168, v35 offset:63488
	v_fmac_f32_e32 v166, v152, v175
	v_fmac_f32_e32 v160, v17, v202
	v_fmac_f32_e32 v178, v18, v192
	v_fmac_f32_e32 v166, v154, v173
	v_fmac_f32_e32 v160, v18, v201
	v_fmac_f32_e32 v178, v19, v193
	v_fmac_f32_e32 v166, v155, v172
	v_fmac_f32_e32 v160, v19, v200
	v_fmac_f32_e32 v178, v20, v194
	v_fmac_f32_e32 v166, v156, v171
	v_fmac_f32_e32 v160, v20, v199
	v_fmac_f32_e32 v178, v21, v196
	v_fmac_f32_e32 v166, v157, v170
	v_fmac_f32_e32 v160, v21, v197
	v_fmac_f32_e32 v178, v22, v198
	s_waitcnt lgkmcnt(0)
	v_lshlrev_b32_e32 v168, 16, v168
	v_fmac_f32_e32 v166, v158, v169
	v_fmac_f32_e32 v160, v22, v195
	v_fmac_f32_e32 v178, v23, v205
	v_fmac_f32_e32 v166, v159, v168
	v_fmac_f32_e32 v160, v23, v175
	v_fmac_f32_e32 v178, v152, v204
	ds_write_b32 v108, v166
	ds_read_u16 v166, v35 offset:64512
	v_fmac_f32_e32 v160, v152, v173
	v_fmac_f32_e32 v178, v154, v203
	v_fmac_f32_e32 v160, v154, v172
	v_fmac_f32_e32 v178, v155, v202
	v_fmac_f32_e32 v160, v155, v171
	v_fmac_f32_e32 v178, v156, v201
	v_fmac_f32_e32 v160, v156, v170
	v_fmac_f32_e32 v178, v157, v200
	v_fmac_f32_e32 v160, v157, v169
	v_fmac_f32_e32 v178, v158, v199
	s_waitcnt lgkmcnt(0)
	v_lshlrev_b32_e32 v166, 16, v166
	v_fmac_f32_e32 v160, v158, v168
	v_add_u32_e32 v152, s19, v69
	v_fmac_f32_e32 v178, v159, v197
	v_fmac_f32_e32 v160, v159, v166
	v_cmp_lt_i32_e32 vcc, -1, v152
	v_mov_b32_e32 v0, 0
	v_mov_b32_e32 v2, 0
	v_mov_b32_e32 v3, 0
	v_mov_b32_e32 v4, 0
	v_mov_b32_e32 v5, 0
	ds_write_b32 v100, v178
	ds_write_b32 v109, v160
	s_waitcnt lgkmcnt(0)
	s_barrier
	s_and_saveexec_b64 s[16:17], vcc
	s_cbranch_execz .LBB0_479
	v_lshl_add_u64 v[2:3], s[92:93], 0, v[152:153]
	v_mad_u64_u32 v[4:5], s[22:23], v2, s53, v[24:25]
	v_mad_i32_i24 v5, v3, s53, v5
	global_load_dwordx4 v[2:5], v[4:5], off

; #define PG8_STAGE_B(bufoff, gbase) do { _Pragma("unroll") for (int _i = 0; _i < 2; ++_i) { unsigned _o = voffB[_i]; asm volatile("" : "+v"(_o)); \
;         __builtin_amdgcn_global_load_lds((const unsigned*)((const char*)(gbase) + _o), (LAS unsigned*)(lds + (bufoff) + ldsw + _i * 8192), 16, 0, 0); } } while (0)
; #define PG8_STAGE_A(bufoff, gbase, h) do { _Pragma("unroll") for (int _i = 0; _i < 2; ++_i) { unsigned _o = (GATHER ? aoffs[h][_i] : voffA[_i]); asm volatile("" : "+v"(_o)); \
;         __builtin_amdgcn_global_load_lds((const unsigned*)((const char*)(gbase) + _o), (LAS unsigned*)(lds + (bufoff) + ldsw + _i * 8192), 16, 0, 0); } } while (0)
; #define PG8_WAIT_V(n) asm volatile("s_waitcnt vmcnt(" #n ")" ::: "memory")
; #define PG8_WAIT_L(n) asm volatile("s_waitcnt lgkmcnt(" #n ")" ::: "memory")
; #define PG8_BAR __builtin_amdgcn_s_barrier()
; #define PG8_SCHED __builtin_amdgcn_sched_barrier(0)
; template <int K, bool PERM, bool GATHER, int MODE  , class Sched, class Epi>
; __device__ __forceinline__ void gemm_phase(LAS unsigned char* lds, const Sched& S, const Epi& E, const LAS int* gtab, int wv) {
;     ...
;             PG8_LDB(B0, 0, 0); PG8_LDB(B1, 0, 1); PG8_SCHED; PG8_LDA(At, 0, 0); PG8_STAGE_A(PG8_SA(1, 1), a1 + hstep, 1);
;             PG8_WAIT_V(8); PG8_WAIT_L(0); PG8_BAR; PG8_MMA(0, 0, At, B0); PG8_MMA(0, 1, At, B1); PG8_BAR; PG8_SCHED;
;             if (last && has_next) PG8_GOFFS(ui + 1);
;             PG8_LDA(At, 0, 1); PG8_STAGE_B(PG8_SB(0, 0), b2); PG8_STAGE_B(PG8_SB(0, 1), b2 + BH); PG8_STAGE_A(PG8_SA(0, 0), a2, 0);
;             PG8_WAIT_V(8); PG8_WAIT_L(0); PG8_BAR; PG8_MMA(1, 0, At, B0); PG8_MMA(1, 1, At, B1); PG8_BAR; PG8_SCHED;
;             PG8_LDB(B0, 1, 0); PG8_LDB(B1, 1, 1); PG8_SCHED; PG8_LDA(At, 1, 0); PG8_STAGE_A(PG8_SA(0, 1), a2 + hstep, 1);
;             PG8_WAIT_V(8); PG8_WAIT_L(0); PG8_BAR; PG8_MMA(0, 0, At, B0); PG8_MMA(0, 1, At, B1); PG8_BAR; PG8_SCHED;
;             if constexpr (Epi::PUBLISH) {
;                 if (t == 0 && pmt >= 0) { int tp = tid; asm volatile("" : "+v"(tp)); if (tp == 0) E.publish(pmt); } }
;             PG8_LDA(At, 1, 1); PG8_STAGE_B(PG8_SB(1, 0), b3); PG8_STAGE_B(PG8_SB(1, 1), b3 + BH); PG8_STAGE_A(PG8_SA(1, 0), a3, 0);
;             PG8_WAIT_V(8); PG8_WAIT_L(0); PG8_BAR; PG8_MMA(1, 0, At, B0); PG8_MMA(1, 1, At, B1); PG8_BAR; PG8_SCHED;
.LBB0_746:
	ds_read_b128 v[192:195], v168 offset:49152
	ds_read_b64 v[196:197], v173 offset:50176
	ds_read_b128 v[198:201], v168 offset:51200
	ds_read_b64 v[202:203], v173 offset:52224
	ds_read_b128 v[204:207], v168 offset:53248
	ds_read_b64 v[208:209], v173 offset:54272
	ds_read_b128 v[210:213], v168 offset:55296
	ds_read_b64 v[214:215], v173 offset:56320
	s_add_u32 s30, s26, 0x80
	s_addc_u32 s31, s27, 0
	s_add_u32 s26, s26, 0x100080
	s_addc_u32 s27, s27, 0
	s_add_i32 m0, s3, 0x18000
	s_nop 0
	global_load_lds_dwordx4 v157, s[30:31]
	s_add_i32 m0, s3, 0x1a000
	s_nop 0
	global_load_lds_dwordx4 v160, s[30:31]
	s_add_i32 m0, s3, 0x1c000
	s_add_u32 s30, s24, 0x80
	s_addc_u32 s31, s25, 0
	global_load_lds_dwordx4 v157, s[26:27]
	s_add_i32 m0, s3, 0x1e000
	s_nop 0
	global_load_lds_dwordx4 v160, s[26:27]
	s_mov_b32 m0, s74
	s_nop 0
	global_load_lds_dwordx4 v161, s[30:31]
	s_mov_b32 m0, s75
	s_nop 0
	global_load_lds_dwordx4 v163, s[30:31]
	s_waitcnt vmcnt(8)
	s_waitcnt lgkmcnt(0)
	s_barrier
	s_setprio 1
	s_waitcnt lgkmcnt(0)
	v_mfma_f32_16x16x128_f8f6f4 v[84:87], v[12:17], v[192:197], v[84:87] cbsz:2 blgp:2
	v_mfma_f32_16x16x128_f8f6f4 v[80:83], v[18:23], v[192:197], v[80:83] cbsz:2 blgp:2
	v_mfma_f32_16x16x128_f8f6f4 v[76:79], v[12:17], v[198:203], v[76:79] cbsz:2 blgp:2
	v_mfma_f32_16x16x128_f8f6f4 v[72:75], v[18:23], v[198:203], v[72:75] cbsz:2 blgp:2
	v_mfma_f32_16x16x128_f8f6f4 v[68:71], v[12:17], v[204:209], v[68:71] cbsz:2 blgp:2
	v_mfma_f32_16x16x128_f8f6f4 v[64:67], v[18:23], v[204:209], v[64:67] cbsz:2 blgp:2
	v_mfma_f32_16x16x128_f8f6f4 v[60:63], v[12:17], v[210:215], v[60:63] cbsz:2 blgp:2
	v_mfma_f32_16x16x128_f8f6f4 v[56:59], v[18:23], v[210:215], v[56:59] cbsz:2 blgp:2
	s_setprio 0
	s_setprio 1
	v_mfma_f32_16x16x128_f8f6f4 v[52:55], v[0:5], v[192:197], v[52:55] cbsz:2 blgp:2
	v_mfma_f32_16x16x128_f8f6f4 v[48:51], v[6:11], v[192:197], v[48:51] cbsz:2 blgp:2
	v_mfma_f32_16x16x128_f8f6f4 v[44:47], v[0:5], v[198:203], v[44:47] cbsz:2 blgp:2
	v_mfma_f32_16x16x128_f8f6f4 v[40:43], v[6:11], v[198:203], v[40:43] cbsz:2 blgp:2
	v_mfma_f32_16x16x128_f8f6f4 v[36:39], v[0:5], v[204:209], v[36:39] cbsz:2 blgp:2
	v_mfma_f32_16x16x128_f8f6f4 v[32:35], v[6:11], v[204:209], v[32:35] cbsz:2 blgp:2
	v_mfma_f32_16x16x128_f8f6f4 v[28:31], v[0:5], v[210:215], v[28:31] cbsz:2 blgp:2
	v_mfma_f32_16x16x128_f8f6f4 v[24:27], v[6:11], v[210:215], v[24:27] cbsz:2 blgp:2
	s_setprio 0
	s_barrier
	s_add_i32 s91, s91, 2
	s_add_u32 s20, s20, 0x100
	s_addc_u32 s21, s21, 0
	s_cmp_gt_u32 s91, 5
	s_cbranch_scc1 .LBB0_753
.LBB0_747:
	v_add_u32_e32 v0, v166, v165
	ds_read_b128 v[12:15], v166
	ds_read_b64 v[16:17], v0 offset:1024
	ds_read_b128 v[18:21], v166 offset:2048
	ds_read_b64 v[22:23], v0 offset:3072
	ds_read_b128 v[0:3], v167
	v_add_u32_e32 v10, v167, v165
	ds_read_b64 v[4:5], v10 offset:1024
	ds_read_b128 v[6:9], v167 offset:2048
	ds_read_b64 v[10:11], v10 offset:3072
	s_cmpk_eq_i32 s20, 0x300
	s_cselect_b64 s[26:27], -1, 0
	s_add_u32 s24, s0, s20
	v_add_u32_e32 v173, v168, v165
	s_addc_u32 s25, s1, s21
	ds_read_b128 v[192:195], v168
	ds_read_b64 v[196:197], v173 offset:1024
	ds_read_b128 v[198:201], v168 offset:2048
	ds_read_b64 v[202:203], v173 offset:3072
	ds_read_b128 v[204:207], v168 offset:4096
	ds_read_b64 v[208:209], v173 offset:5120
	ds_read_b128 v[210:213], v168 offset:6144
	ds_read_b64 v[214:215], v173 offset:7168
	s_add_u32 s30, s24, 0x80
	s_addc_u32 s31, s25, 0
	s_add_i32 m0, s3, 0xc000
	s_nop 0
	global_load_lds_dwordx4 v162, s[30:31]
	s_add_i32 m0, s3, 0xe000
	s_nop 0
	global_load_lds_dwordx4 v164, s[30:31]
	s_waitcnt vmcnt(8)
	s_waitcnt lgkmcnt(0)
	s_barrier
	s_setprio 1
	s_waitcnt lgkmcnt(0)
	v_mfma_f32_16x16x128_f8f6f4 v[148:151], v[12:17], v[192:197], v[148:151] cbsz:2 blgp:2
	v_mfma_f32_16x16x128_f8f6f4 v[144:147], v[18:23], v[192:197], v[144:147] cbsz:2 blgp:2
	v_mfma_f32_16x16x128_f8f6f4 v[140:143], v[12:17], v[198:203], v[140:143] cbsz:2 blgp:2
	v_mfma_f32_16x16x128_f8f6f4 v[136:139], v[18:23], v[198:203], v[136:139] cbsz:2 blgp:2
	v_mfma_f32_16x16x128_f8f6f4 v[132:135], v[12:17], v[204:209], v[132:135] cbsz:2 blgp:2
	v_mfma_f32_16x16x128_f8f6f4 v[128:131], v[18:23], v[204:209], v[128:131] cbsz:2 blgp:2
	v_mfma_f32_16x16x128_f8f6f4 v[124:127], v[12:17], v[210:215], v[124:127] cbsz:2 blgp:2
	v_mfma_f32_16x16x128_f8f6f4 v[120:123], v[18:23], v[210:215], v[120:123] cbsz:2 blgp:2
	s_setprio 0
	s_setprio 1
	v_mfma_f32_16x16x128_f8f6f4 v[116:119], v[0:5], v[192:197], v[116:119] cbsz:2 blgp:2
	v_mfma_f32_16x16x128_f8f6f4 v[112:115], v[6:11], v[192:197], v[112:115] cbsz:2 blgp:2
	v_mfma_f32_16x16x128_f8f6f4 v[108:111], v[0:5], v[198:203], v[108:111] cbsz:2 blgp:2
	v_mfma_f32_16x16x128_f8f6f4 v[104:107], v[6:11], v[198:203], v[104:107] cbsz:2 blgp:2
	v_mfma_f32_16x16x128_f8f6f4 v[100:103], v[0:5], v[204:209], v[100:103] cbsz:2 blgp:2
	v_mfma_f32_16x16x128_f8f6f4 v[96:99], v[6:11], v[204:209], v[96:99] cbsz:2 blgp:2
	v_mfma_f32_16x16x128_f8f6f4 v[92:95], v[0:5], v[210:215], v[92:95] cbsz:2 blgp:2
	v_mfma_f32_16x16x128_f8f6f4 v[88:91], v[6:11], v[210:215], v[88:91] cbsz:2 blgp:2
	s_setprio 0
	s_barrier
	s_and_b64 s[24:25], s[16:17], s[26:27]
	s_andn2_b64 vcc, exec, s[24:25]
	s_cbranch_vccnz .LBB0_749
	ds_read2st64_b32 v[162:163], v171 offset1:2
	ds_read2st64_b32 v[174:175], v172 offset1:2
	s_waitcnt lgkmcnt(0)
	v_lshl_add_u32 v161, v162, 10, v156
	v_lshl_add_u32 v162, v163, 10, v156
	v_lshl_add_u32 v163, v174, 10, v159
	v_lshl_add_u32 v164, v175, 10, v159
; #define PG8_STAGE_B(bufoff, gbase) do { _Pragma("unroll") for (int _i = 0; _i < 2; ++_i) { unsigned _o = voffB[_i]; asm volatile("" : "+v"(_o)); \
;         __builtin_amdgcn_global_load_lds((const unsigned*)((const char*)(gbase) + _o), (LAS unsigned*)(lds + (bufoff) + ldsw + _i * 8192), 16, 0, 0); } } while (0)
; #define PG8_STAGE_A(bufoff, gbase, h) do { _Pragma("unroll") for (int _i = 0; _i < 2; ++_i) { unsigned _o = (GATHER ? aoffs[h][_i] : voffA[_i]); asm volatile("" : "+v"(_o)); \
;         __builtin_amdgcn_global_load_lds((const unsigned*)((const char*)(gbase) + _o), (LAS unsigned*)(lds + (bufoff) + ldsw + _i * 8192), 16, 0, 0); } } while (0)
; #define PG8_WAIT_V(n) asm volatile("s_waitcnt vmcnt(" #n ")" ::: "memory")
; template <int K, bool PERM, bool GATHER, int MODE  , class Sched, class Epi>
; __device__ __forceinline__ void gemm_phase(LAS unsigned char* lds, const Sched& S, const Epi& E, const LAS int* gtab, int wv) {
;     ...
;             const bool last = (t == nt - 2);
;             const char* a1 = cA + (size_t)(t + 1) * kstep;
;             const char* a2 = last ? nA : cA + (size_t)(t + 2) * kstep;
;             const char* b2 = last ? nB : cB + (size_t)(t + 2) * kstep;
;             const char* a3 = a2 + kstep; const char* b3 = b2 + kstep;
;             PG8_LDB(B0, 0, 0); PG8_LDB(B1, 0, 1); PG8_SCHED; PG8_LDA(At, 0, 0); PG8_STAGE_A(PG8_SA(1, 1), a1 + hstep, 1);
;             PG8_WAIT_V(8); PG8_WAIT_L(0); PG8_BAR; PG8_MMA(0, 0, At, B0); PG8_MMA(0, 1, At, B1); PG8_BAR; PG8_SCHED;
;             if (last && has_next) PG8_GOFFS(ui + 1);
;             PG8_LDA(At, 0, 1); PG8_STAGE_B(PG8_SB(0, 0), b2); PG8_STAGE_B(PG8_SB(0, 1), b2 + BH); PG8_STAGE_A(PG8_SA(0, 0), a2, 0);
;             PG8_WAIT_V(8); PG8_WAIT_L(0); PG8_BAR; PG8_MMA(1, 0, At, B0); PG8_MMA(1, 1, At, B1); PG8_BAR; PG8_SCHED;
;             PG8_LDB(B0, 1, 0); PG8_LDB(B1, 1, 1); PG8_SCHED; PG8_LDA(At, 1, 0); PG8_STAGE_A(PG8_SA(0, 1), a2 + hstep, 1);
;             PG8_WAIT_V(8); PG8_WAIT_L(0); PG8_BAR; PG8_MMA(0, 0, At, B0); PG8_MMA(0, 1, At, B1); PG8_BAR; PG8_SCHED;
;             if constexpr (Epi::PUBLISH) {
;                 if (t == 0 && pmt >= 0) { int tp = tid; asm volatile("" : "+v"(tp)); if (tp == 0) E.publish(pmt); } }
;             PG8_LDA(At, 1, 1); PG8_STAGE_B(PG8_SB(1, 0), b3); PG8_STAGE_B(PG8_SB(1, 1), b3 + BH); PG8_STAGE_A(PG8_SA(1, 0), a3, 0);
.LBB0_749:
	s_add_u32 s24, s0, s20
	s_addc_u32 s25, s1, s21
	s_add_u32 s30, s24, 0x100
	s_addc_u32 s31, s25, 0
	s_and_b64 s[24:25], s[26:27], exec
	s_cselect_b32 s25, s87, s31
	s_cselect_b32 s24, s88, s30
	s_add_u32 s30, s85, s20
	s_addc_u32 s31, s86, s21
	s_and_b64 s[26:27], s[26:27], exec
	s_mov_b32 m0, s58
	s_cselect_b32 s27, s89, s31
	s_cselect_b32 s26, s90, s30
	ds_read_b128 v[192:195], v168 offset:16384
	ds_read_b64 v[196:197], v173 offset:17408
	ds_read_b128 v[198:201], v168 offset:18432
	ds_read_b64 v[202:203], v173 offset:19456
	ds_read_b128 v[204:207], v168 offset:20480
	ds_read_b64 v[208:209], v173 offset:21504
	ds_read_b128 v[210:213], v168 offset:22528
	ds_read_b64 v[214:215], v173 offset:23552
	s_add_u32 s30, s26, 0x100000
	global_load_lds_dwordx4 v157, s[26:27]
	s_mov_b32 m0, s59
	s_addc_u32 s31, s27, 0
	global_load_lds_dwordx4 v160, s[26:27]
	s_mov_b32 m0, s64
	s_nop 0
	global_load_lds_dwordx4 v157, s[30:31]
	s_mov_b32 m0, s65
	s_nop 0
	global_load_lds_dwordx4 v160, s[30:31]
	s_mov_b32 m0, s3
	s_nop 0
	global_load_lds_dwordx4 v161, s[24:25]
	s_mov_b32 m0, s66
	s_nop 0
	global_load_lds_dwordx4 v163, s[24:25]
	s_waitcnt vmcnt(8)
	s_waitcnt lgkmcnt(0)
	s_barrier
	s_setprio 1
	s_waitcnt lgkmcnt(0)
	v_mfma_f32_16x16x128_f8f6f4 v[84:87], v[12:17], v[192:197], v[84:87] cbsz:2 blgp:2
	v_mfma_f32_16x16x128_f8f6f4 v[80:83], v[18:23], v[192:197], v[80:83] cbsz:2 blgp:2
	v_mfma_f32_16x16x128_f8f6f4 v[76:79], v[12:17], v[198:203], v[76:79] cbsz:2 blgp:2
	v_mfma_f32_16x16x128_f8f6f4 v[72:75], v[18:23], v[198:203], v[72:75] cbsz:2 blgp:2
	v_mfma_f32_16x16x128_f8f6f4 v[68:71], v[12:17], v[204:209], v[68:71] cbsz:2 blgp:2
	v_mfma_f32_16x16x128_f8f6f4 v[64:67], v[18:23], v[204:209], v[64:67] cbsz:2 blgp:2
	v_mfma_f32_16x16x128_f8f6f4 v[60:63], v[12:17], v[210:215], v[60:63] cbsz:2 blgp:2
	v_mfma_f32_16x16x128_f8f6f4 v[56:59], v[18:23], v[210:215], v[56:59] cbsz:2 blgp:2
	s_setprio 0
	s_setprio 1
	v_mfma_f32_16x16x128_f8f6f4 v[52:55], v[0:5], v[192:197], v[52:55] cbsz:2 blgp:2
	v_mfma_f32_16x16x128_f8f6f4 v[48:51], v[6:11], v[192:197], v[48:51] cbsz:2 blgp:2
	v_mfma_f32_16x16x128_f8f6f4 v[44:47], v[0:5], v[198:203], v[44:47] cbsz:2 blgp:2
	v_mfma_f32_16x16x128_f8f6f4 v[40:43], v[6:11], v[198:203], v[40:43] cbsz:2 blgp:2
	v_mfma_f32_16x16x128_f8f6f4 v[36:39], v[0:5], v[204:209], v[36:39] cbsz:2 blgp:2
	v_mfma_f32_16x16x128_f8f6f4 v[32:35], v[6:11], v[204:209], v[32:35] cbsz:2 blgp:2
	v_mfma_f32_16x16x128_f8f6f4 v[28:31], v[0:5], v[210:215], v[28:31] cbsz:2 blgp:2
	v_mfma_f32_16x16x128_f8f6f4 v[24:27], v[6:11], v[210:215], v[24:27] cbsz:2 blgp:2
	s_setprio 0
	s_barrier
	v_add_u32_e32 v0, v169, v165
	ds_read_b128 v[12:15], v169
	ds_read_b64 v[16:17], v0 offset:1024
	ds_read_b128 v[18:21], v169 offset:2048
	ds_read_b64 v[22:23], v0 offset:3072
	ds_read_b128 v[0:3], v170
	v_add_u32_e32 v10, v170, v165
	ds_read_b64 v[4:5], v10 offset:1024
	ds_read_b128 v[6:9], v170 offset:2048
	ds_read_b64 v[10:11], v10 offset:3072
	s_mov_b32 m0, s67
	ds_read_b128 v[192:195], v168 offset:32768
	ds_read_b64 v[196:197], v173 offset:33792
	ds_read_b128 v[198:201], v168 offset:34816
	ds_read_b64 v[202:203], v173 offset:35840
	ds_read_b128 v[204:207], v168 offset:36864
	ds_read_b64 v[208:209], v173 offset:37888
	ds_read_b128 v[210:213], v168 offset:38912
	ds_read_b64 v[214:215], v173 offset:39936
	s_nop 0
	global_load_lds_dwordx4 v162, s[24:25]
	s_mov_b32 m0, s73
	s_nop 0
	global_load_lds_dwordx4 v164, s[24:25]
	s_waitcnt vmcnt(8)
	s_waitcnt lgkmcnt(0)
	s_barrier
	s_setprio 1
	s_waitcnt lgkmcnt(0)
	v_mfma_f32_16x16x128_f8f6f4 v[148:151], v[12:17], v[192:197], v[148:151] cbsz:2 blgp:2
	v_mfma_f32_16x16x128_f8f6f4 v[144:147], v[18:23], v[192:197], v[144:147] cbsz:2 blgp:2
	v_mfma_f32_16x16x128_f8f6f4 v[140:143], v[12:17], v[198:203], v[140:143] cbsz:2 blgp:2
	v_mfma_f32_16x16x128_f8f6f4 v[136:139], v[18:23], v[198:203], v[136:139] cbsz:2 blgp:2
	v_mfma_f32_16x16x128_f8f6f4 v[132:135], v[12:17], v[204:209], v[132:135] cbsz:2 blgp:2
	v_mfma_f32_16x16x128_f8f6f4 v[128:131], v[18:23], v[204:209], v[128:131] cbsz:2 blgp:2
	v_mfma_f32_16x16x128_f8f6f4 v[124:127], v[12:17], v[210:215], v[124:127] cbsz:2 blgp:2
	v_mfma_f32_16x16x128_f8f6f4 v[120:123], v[18:23], v[210:215], v[120:123] cbsz:2 blgp:2
	s_setprio 0
	s_setprio 1
	v_mfma_f32_16x16x128_f8f6f4 v[116:119], v[0:5], v[192:197], v[116:119] cbsz:2 blgp:2
	v_mfma_f32_16x16x128_f8f6f4 v[112:115], v[6:11], v[192:197], v[112:115] cbsz:2 blgp:2
	v_mfma_f32_16x16x128_f8f6f4 v[108:111], v[0:5], v[198:203], v[108:111] cbsz:2 blgp:2
	v_mfma_f32_16x16x128_f8f6f4 v[104:107], v[6:11], v[198:203], v[104:107] cbsz:2 blgp:2
	v_mfma_f32_16x16x128_f8f6f4 v[100:103], v[0:5], v[204:209], v[100:103] cbsz:2 blgp:2
	v_mfma_f32_16x16x128_f8f6f4 v[96:99], v[6:11], v[204:209], v[96:99] cbsz:2 blgp:2
	v_mfma_f32_16x16x128_f8f6f4 v[92:95], v[0:5], v[210:215], v[92:95] cbsz:2 blgp:2
	v_mfma_f32_16x16x128_f8f6f4 v[88:91], v[6:11], v[210:215], v[88:91] cbsz:2 blgp:2
	s_setprio 0
	s_barrier
	s_cmp_eq_u32 s20, 0
	s_cselect_b64 s[30:31], -1, 0
	s_and_b64 s[30:31], s[30:31], s[18:19]
	s_andn2_b64 vcc, exec, s[30:31]
	s_cbranch_vccnz .LBB0_746
	v_mov_b32_e32 v152, v154
	s_nop 0
	v_cmp_eq_u32_e32 vcc, 0, v152
	s_and_saveexec_b64 s[30:31], vcc
	s_cbranch_execz .LBB0_745
	s_mov_b64 s[40:41], exec
	v_mbcnt_lo_u32_b32 v152, s40, 0
	v_mbcnt_hi_u32_b32 v152, s41, v152
	v_cmp_eq_u32_e32 vcc, 0, v152
	s_and_b64 s[92:93], exec, vcc
	s_mov_b64 exec, s[92:93]
	s_cbranch_execz .LBB0_745
	s_bcnt1_i32_b64 s40, s[40:41]
	v_mov_b32_e32 v152, s40
	global_atomic_add v153, v152, s[22:23]
	s_branch .LBB0_745

; __device__ __forceinline__ void phase_combine(CArgs a, LAS unsigned char* lds, int L, int wv, int xw  ) {
;     ...
;             for (int j = 0; j < 2; ++j) { const int c0 = lane * 8 + 512 * j; const u32x4 xr = *(const u32x4*)(Z + (size_t)tok * DM + c0); const f32x2 ms = *(const f32x2*)(MS + (size_t)tok * 2);
;                 const f32x4 z0 = (f32x4){bflo(xr.x), bfhi(xr.x), bflo(xr.y), bfhi(xr.y)}, z1 = (f32x4){bflo(xr.z), bfhi(xr.z), bflo(xr.w), bfhi(xr.w)};
;                 v[h][j][0] = DN_ALPHA * ((z0 - ms.x) * ms.y * *(const f32x4*)(lng0 + c0) + *(const f32x4*)(lnb0 + c0)); v[h][j][1] = DN_ALPHA * ((z1 - ms.x) * ms.y * *(const f32x4*)(lng0 + c0 + 4) + *(const f32x4*)(lnb0 + c0 + 4)); } }
; #pragma unroll
;         for (int k = 0; k < 4; ++k)
; #pragma unroll
;             for (int h = 0; h < 4; ++h) { const int ep = k == 0 ? ep4[h].x : k == 1 ? ep4[h].y : k == 2 ? ep4[h].z : ep4[h].w; const float g = g4[h][k];
;                 const size_t row = (size_t)misc[16 + (ep >> 16)] * 256 + (ep & 0xffff);
; #pragma unroll
;                 for (int j = 0; j < 2; ++j) { const u32x2 y = *(const u32x2*)(YS + row * DM + lane * 8 + 512 * j); const float gs = g * (1.f / QS_YS);
;                     const f32x2 y0 = __builtin_amdgcn_cvt_pk_f32_fp8((int)y.x, false), y1 = __builtin_amdgcn_cvt_pk_f32_fp8((int)y.x, true), y2 = __builtin_amdgcn_cvt_pk_f32_fp8((int)y.y, false), y3 = __builtin_amdgcn_cvt_pk_f32_fp8((int)y.y, true);
;                     v[h][j][0] += gs * (f32x4){y0.x, y0.y, y1.x, y1.y}; v[h][j][1] += gs * (f32x4){y2.x, y2.y, y3.x, y3.y}; } }
; #pragma unroll
;         for (int h = 0; h < 4; ++h) { const int tok = tk + h;
;             float s = 0.f;
; #pragma unroll
;             for (int j = 0; j < 2; ++j) s += ((v[h][j][0].x + v[h][j][0].y) + (v[h][j][0].z + v[h][j][0].w)) + ((v[h][j][1].x + v[h][j][1].y) + (v[h][j][1].z + v[h][j][1].w));
;             const float mean = wave_sum(s, lane) * (1.f / DM); float s2 = 0.f;
.LBB0_929:
	v_lshlrev_b32_e32 v10, 16, v76
	v_and_b32_e32 v11, 0xffff0000, v76
	v_lshlrev_b32_e32 v8, 16, v77
	v_and_b32_e32 v9, 0xffff0000, v77
	v_lshlrev_b32_e32 v14, 16, v78
	v_and_b32_e32 v15, 0xffff0000, v78
	v_lshlrev_b32_e32 v12, 16, v79
	v_and_b32_e32 v13, 0xffff0000, v79
	v_cvt_pk_f32_fp8_e32 v[76:77], v168
	v_cvt_pk_f32_fp8_sdwa v[78:79], v168 src0_sel:WORD_1
	v_lshlrev_b32_e32 v2, 16, v80
	v_and_b32_e32 v3, 0xffff0000, v80
	v_lshlrev_b32_e32 v0, 16, v81
	v_and_b32_e32 v1, 0xffff0000, v81
	v_lshlrev_b32_e32 v6, 16, v82
	v_and_b32_e32 v7, 0xffff0000, v82
	v_lshlrev_b32_e32 v4, 16, v83
	v_and_b32_e32 v5, 0xffff0000, v83
	v_cvt_pk_f32_fp8_e32 v[80:81], v169
	v_cvt_pk_f32_fp8_sdwa v[82:83], v169 src0_sel:WORD_1
	v_sub_f32_e32 v1, v1, v134
	v_sub_f32_e32 v0, v0, v134
	v_sub_f32_e32 v3, v3, v134
	v_sub_f32_e32 v2, v2, v134
	v_pk_mul_f32 v[2:3], v[134:135], v[2:3] op_sel:[1,0]
	v_pk_mul_f32 v[0:1], v[134:135], v[0:1] op_sel:[1,0]
	v_sub_f32_e32 v5, v5, v134
	v_sub_f32_e32 v4, v4, v134
	v_sub_f32_e32 v7, v7, v134
	v_sub_f32_e32 v6, v6, v134
	v_mul_f32_e32 v72, 0x3d000000, v72
	v_pk_fma_f32 v[0:1], v[42:43], v[0:1], v[46:47]
	v_pk_fma_f32 v[2:3], v[40:41], v[2:3], v[44:45]
	v_pk_mul_f32 v[6:7], v[134:135], v[6:7] op_sel:[1,0]
	v_pk_mul_f32 v[4:5], v[134:135], v[4:5] op_sel:[1,0]
	v_pk_mul_f32 v[78:79], v[72:73], v[78:79] op_sel_hi:[0,1]
	v_pk_mul_f32 v[76:77], v[72:73], v[76:77] op_sel_hi:[0,1]
	v_pk_fma_f32 v[4:5], v[34:35], v[4:5], v[38:39]
	v_pk_fma_f32 v[6:7], v[32:33], v[6:7], v[36:37]
	v_pk_fma_f32 v[2:3], v[2:3], s[70:71], v[76:77] op_sel_hi:[1,0,1]
	v_pk_fma_f32 v[0:1], v[0:1], s[70:71], v[78:79] op_sel_hi:[1,0,1]
	v_pk_mul_f32 v[76:77], v[72:73], v[82:83] op_sel_hi:[0,1]
	v_pk_mul_f32 v[78:79], v[72:73], v[80:81] op_sel_hi:[0,1]
	v_pk_fma_f32 v[6:7], v[6:7], s[70:71], v[78:79] op_sel_hi:[1,0,1]
	v_pk_fma_f32 v[4:5], v[4:5], s[70:71], v[76:77] op_sel_hi:[1,0,1]
	v_cvt_pk_f32_fp8_e32 v[76:77], v166
	v_cvt_pk_f32_fp8_sdwa v[78:79], v166 src0_sel:WORD_1
	v_cvt_pk_f32_fp8_e32 v[80:81], v167
	v_cvt_pk_f32_fp8_sdwa v[82:83], v167 src0_sel:WORD_1
	v_sub_f32_e32 v9, v9, v134
	v_sub_f32_e32 v8, v8, v134
	v_sub_f32_e32 v11, v11, v134
	v_sub_f32_e32 v10, v10, v134
	v_pk_mul_f32 v[10:11], v[134:135], v[10:11] op_sel:[1,0]
	v_pk_mul_f32 v[8:9], v[134:135], v[8:9] op_sel:[1,0]
	v_sub_f32_e32 v13, v13, v134
	v_sub_f32_e32 v12, v12, v134
	v_sub_f32_e32 v15, v15, v134
	v_sub_f32_e32 v14, v14, v134
	v_pk_fma_f32 v[8:9], v[26:27], v[8:9], v[30:31]
	v_pk_fma_f32 v[10:11], v[24:25], v[10:11], v[28:29]
	v_pk_mul_f32 v[14:15], v[134:135], v[14:15] op_sel:[1,0]
	v_pk_mul_f32 v[12:13], v[134:135], v[12:13] op_sel:[1,0]
	v_pk_mul_f32 v[78:79], v[72:73], v[78:79] op_sel_hi:[0,1]
	v_pk_mul_f32 v[76:77], v[72:73], v[76:77] op_sel_hi:[0,1]
	v_pk_fma_f32 v[12:13], v[18:19], v[12:13], v[22:23]
	v_pk_fma_f32 v[14:15], v[16:17], v[14:15], v[20:21]
	v_pk_fma_f32 v[10:11], v[10:11], s[70:71], v[76:77] op_sel_hi:[1,0,1]
	v_pk_fma_f32 v[8:9], v[8:9], s[70:71], v[78:79] op_sel_hi:[1,0,1]
	v_pk_mul_f32 v[76:77], v[72:73], v[82:83] op_sel_hi:[0,1]
	v_pk_mul_f32 v[78:79], v[72:73], v[80:81] op_sel_hi:[0,1]
	v_pk_fma_f32 v[14:15], v[14:15], s[70:71], v[78:79] op_sel_hi:[1,0,1]
	v_pk_fma_f32 v[12:13], v[12:13], s[70:71], v[76:77] op_sel_hi:[1,0,1]
	v_cvt_pk_f32_fp8_e32 v[76:77], v164
	v_cvt_pk_f32_fp8_sdwa v[78:79], v164 src0_sel:WORD_1
	v_cvt_pk_f32_fp8_e32 v[80:81], v165
	v_cvt_pk_f32_fp8_sdwa v[82:83], v165 src0_sel:WORD_1
	v_mul_f32_e32 v72, 0x3d000000, v73
	v_pk_fma_f32 v[0:1], v[72:73], v[78:79], v[0:1] op_sel_hi:[0,1,1]
	v_pk_fma_f32 v[2:3], v[72:73], v[76:77], v[2:3] op_sel_hi:[0,1,1]
	v_pk_fma_f32 v[4:5], v[72:73], v[82:83], v[4:5] op_sel_hi:[0,1,1]
	v_pk_fma_f32 v[6:7], v[72:73], v[80:81], v[6:7] op_sel_hi:[0,1,1]
	v_cvt_pk_f32_fp8_e32 v[76:77], v158
	v_cvt_pk_f32_fp8_sdwa v[78:79], v158 src0_sel:WORD_1
	v_cvt_pk_f32_fp8_e32 v[80:81], v159
	v_cvt_pk_f32_fp8_sdwa v[82:83], v159 src0_sel:WORD_1
	v_pk_fma_f32 v[10:11], v[72:73], v[76:77], v[10:11] op_sel_hi:[0,1,1]
	v_pk_fma_f32 v[8:9], v[72:73], v[78:79], v[8:9] op_sel_hi:[0,1,1]
	v_pk_fma_f32 v[14:15], v[72:73], v[80:81], v[14:15] op_sel_hi:[0,1,1]
	v_pk_fma_f32 v[12:13], v[72:73], v[82:83], v[12:13] op_sel_hi:[0,1,1]
	v_cvt_pk_f32_fp8_e32 v[76:77], v162
	v_cvt_pk_f32_fp8_sdwa v[78:79], v162 src0_sel:WORD_1
	v_cvt_pk_f32_fp8_e32 v[80:81], v163
	v_cvt_pk_f32_fp8_sdwa v[82:83], v163 src0_sel:WORD_1
	v_mul_f32_e32 v72, 0x3d000000, v74
	v_pk_fma_f32 v[2:3], v[72:73], v[76:77], v[2:3] op_sel_hi:[0,1,1]
	v_pk_fma_f32 v[0:1], v[72:73], v[78:79], v[0:1] op_sel_hi:[0,1,1]
	v_pk_fma_f32 v[6:7], v[72:73], v[80:81], v[6:7] op_sel_hi:[0,1,1]
	v_pk_fma_f32 v[4:5], v[72:73], v[82:83], v[4:5] op_sel_hi:[0,1,1]
	v_cvt_pk_f32_fp8_e32 v[76:77], v160
	v_cvt_pk_f32_fp8_sdwa v[78:79], v160 src0_sel:WORD_1
	v_cvt_pk_f32_fp8_e32 v[80:81], v161
	v_cvt_pk_f32_fp8_sdwa v[82:83], v161 src0_sel:WORD_1
	v_pk_fma_f32 v[10:11], v[72:73], v[76:77], v[10:11] op_sel_hi:[0,1,1]
	v_pk_fma_f32 v[8:9], v[72:73], v[78:79], v[8:9] op_sel_hi:[0,1,1]
	v_pk_fma_f32 v[14:15], v[72:73], v[80:81], v[14:15] op_sel_hi:[0,1,1]
	v_pk_fma_f32 v[12:13], v[72:73], v[82:83], v[12:13] op_sel_hi:[0,1,1]
	v_mul_f32_e32 v72, 0x3d000000, v75
	v_cvt_pk_f32_fp8_e32 v[74:75], v172
	v_cvt_pk_f32_fp8_e32 v[78:79], v173
	v_cvt_pk_f32_fp8_sdwa v[76:77], v172 src0_sel:WORD_1
	v_cvt_pk_f32_fp8_sdwa v[80:81], v173 src0_sel:WORD_1
	v_pk_fma_f32 v[74:75], v[72:73], v[74:75], v[2:3] op_sel_hi:[0,1,1]
	v_pk_fma_f32 v[2:3], v[72:73], v[78:79], v[6:7] op_sel_hi:[0,1,1]
	v_cvt_pk_f32_fp8_e32 v[6:7], v170
	v_pk_fma_f32 v[76:77], v[72:73], v[76:77], v[0:1] op_sel_hi:[0,1,1]
	v_pk_fma_f32 v[0:1], v[72:73], v[80:81], v[4:5] op_sel_hi:[0,1,1]
	v_cvt_pk_f32_fp8_sdwa v[4:5], v170 src0_sel:WORD_1
	v_cvt_pk_f32_fp8_e32 v[78:79], v171
	v_cvt_pk_f32_fp8_sdwa v[80:81], v171 src0_sel:WORD_1
	v_pk_fma_f32 v[6:7], v[72:73], v[6:7], v[10:11] op_sel_hi:[0,1,1]
	v_pk_fma_f32 v[4:5], v[72:73], v[4:5], v[8:9] op_sel_hi:[0,1,1]
	v_mov_b32_e32 v8, v74
	v_mov_b32_e32 v9, v6
	v_mov_b32_e32 v10, v75
	v_mov_b32_e32 v11, v7
	v_pk_fma_f32 v[12:13], v[72:73], v[80:81], v[12:13] op_sel_hi:[0,1,1]
	v_pk_fma_f32 v[14:15], v[72:73], v[78:79], v[14:15] op_sel_hi:[0,1,1]
	v_pk_add_f32 v[8:9], v[8:9], v[10:11]
	v_mov_b32_e32 v10, v76
	v_mov_b32_e32 v11, v4
	v_mov_b32_e32 v72, v77
	v_mov_b32_e32 v73, v5
	v_pk_add_f32 v[10:11], v[10:11], v[72:73]
	v_mov_b32_e32 v72, v3
	v_pk_add_f32 v[8:9], v[8:9], v[10:11]
	v_mov_b32_e32 v10, v2
	v_mov_b32_e32 v11, v14
	v_mov_b32_e32 v73, v15
	v_pk_add_f32 v[10:11], v[10:11], v[72:73]
	v_mov_b32_e32 v72, v0
	v_mov_b32_e32 v73, v12
	v_mov_b32_e32 v78, v1
	v_mov_b32_e32 v79, v13
	v_pk_add_f32 v[72:73], v[72:73], v[78:79]
	s_mov_b64 s[26:27], -1
	v_pk_add_f32 v[10:11], v[10:11], v[72:73]
	s_nop 0
	v_pk_add_f32 v[8:9], v[8:9], v[10:11]
	s_nop 0
	v_add_f32_e32 v8, 0, v8
	v_add_f32_e32 v8, v8, v9
	s_waitcnt lgkmcnt(0)
; __device__ __forceinline__ float shx(float v, int m, int lane) { return __builtin_bit_cast(float, __builtin_amdgcn_ds_bpermute((lane ^ m) << 2, __builtin_bit_cast(int, v))); }
; __device__ __forceinline__ float wave_sum(float v, int lane) {
; #pragma unroll
;     for (int o = 1; o < 64; o <<= 1) v += shx(v, o, lane);
;     return v;
; __device__ __forceinline__ void phase_combine(CArgs a, LAS unsigned char* lds, int L, int wv, int xw  ) {
;     ...
;             const float mean = wave_sum(s, lane) * (1.f / DM); float s2 = 0.f;
; #pragma unroll
;             for (int j = 0; j < 2; ++j) { v[h][j][0] = v[h][j][0] - mean; v[h][j][1] = v[h][j][1] - mean;
;                 s2 += ((v[h][j][0].x * v[h][j][0].x + v[h][j][0].y * v[h][j][0].y) + (v[h][j][0].z * v[h][j][0].z + v[h][j][0].w * v[h][j][0].w)) + ((v[h][j][1].x * v[h][j][1].x + v[h][j][1].y * v[h][j][1].y) + (v[h][j][1].z * v[h][j][1].z + v[h][j][1].w * v[h][j][1].w)); }
;             const float rstd = 1.0f / sqrtf(wave_sum(s2, lane) * (1.f / DM) + LN_EPS);
;             float am = 0.f;
; #pragma unroll
;             for (int j = 0; j < 2; ++j) { const int c0 = lane * 8 + 512 * j;
;                 v[h][j][0] = v[h][j][0] * rstd * *(const f32x4*)(lng + c0) + *(const f32x4*)(lnb + c0); v[h][j][1] = v[h][j][1] * rstd * *(const f32x4*)(lng + c0 + 4) + *(const f32x4*)(lnb + c0 + 4);
	s_nop 1
	v_add_f32_dpp v8, v8, v8 quad_perm:[1,0,3,2] row_mask:0xf bank_mask:0xf
	s_nop 1
	v_add_f32_dpp v8, v8, v8 quad_perm:[2,3,0,1] row_mask:0xf bank_mask:0xf
	s_nop 1
	v_add_f32_dpp v8, v8, v8 row_half_mirror row_mask:0xf bank_mask:0xf
	s_nop 1
	v_add_f32_dpp v8, v8, v8 row_mirror row_mask:0xf bank_mask:0xf
	v_mov_b32_e32 v9, v8
	s_nop 1
	v_permlane16_swap_b32_e32 v9, v8
	v_add_f32_e32 v8, v8, v9
	v_mov_b32_e32 v9, v8
	s_nop 1
	v_permlane32_swap_b32_e32 v9, v8
	v_add_f32_e32 v8, v8, v9
	v_fmamk_f32 v75, v8, 0xba800000, v75
	v_fmamk_f32 v7, v8, 0xba800000, v7
	v_fmamk_f32 v77, v8, 0xba800000, v77
	v_fmac_f32_e32 v74, 0xba800000, v8
	v_fmamk_f32 v5, v8, 0xba800000, v5
	v_fmac_f32_e32 v6, 0xba800000, v8
	v_mov_b32_e32 v10, v75
	v_mov_b32_e32 v11, v7
	v_fmac_f32_e32 v76, 0xba800000, v8
	v_fmamk_f32 v1, v8, 0xba800000, v1
	v_fmac_f32_e32 v0, 0xba800000, v8
	v_fmamk_f32 v3, v8, 0xba800000, v3
	v_fmac_f32_e32 v2, 0xba800000, v8
	v_fmac_f32_e32 v4, 0xba800000, v8
	v_fmamk_f32 v13, v8, 0xba800000, v13
	v_fmac_f32_e32 v12, 0xba800000, v8
	v_fmamk_f32 v15, v8, 0xba800000, v15
	v_fmac_f32_e32 v14, 0xba800000, v8
	v_mov_b32_e32 v8, v74
	v_mov_b32_e32 v9, v6
	v_pk_mul_f32 v[10:11], v[10:11], v[10:11]
	v_mov_b32_e32 v72, v77
	v_mov_b32_e32 v73, v5
	v_pk_fma_f32 v[8:9], v[8:9], v[8:9], v[10:11]
	v_mov_b32_e32 v10, v76
	v_mov_b32_e32 v11, v4
	v_pk_mul_f32 v[72:73], v[72:73], v[72:73]
	v_mov_b32_e32 v78, v1
	v_pk_fma_f32 v[10:11], v[10:11], v[10:11], v[72:73]
	v_mov_b32_e32 v72, v3
	v_mov_b32_e32 v73, v15
	v_pk_add_f32 v[8:9], v[8:9], v[10:11]
	v_mov_b32_e32 v10, v2
	v_mov_b32_e32 v11, v14
	v_pk_mul_f32 v[72:73], v[72:73], v[72:73]
	v_mov_b32_e32 v79, v13
	v_pk_fma_f32 v[10:11], v[10:11], v[10:11], v[72:73]
	v_mov_b32_e32 v72, v0
	v_mov_b32_e32 v73, v12
	v_pk_mul_f32 v[78:79], v[78:79], v[78:79]
	s_nop 0
	v_pk_fma_f32 v[72:73], v[72:73], v[72:73], v[78:79]
	s_nop 0
	v_pk_add_f32 v[10:11], v[10:11], v[72:73]
	s_nop 0
	v_pk_add_f32 v[8:9], v[8:9], v[10:11]
	s_nop 0
	v_add_f32_e32 v8, v8, v9
	s_waitcnt lgkmcnt(0)
	s_nop 1
	v_add_f32_dpp v8, v8, v8 quad_perm:[1,0,3,2] row_mask:0xf bank_mask:0xf
	s_nop 1
	v_add_f32_dpp v8, v8, v8 quad_perm:[2,3,0,1] row_mask:0xf bank_mask:0xf
	s_nop 1
	v_add_f32_dpp v8, v8, v8 row_half_mirror row_mask:0xf bank_mask:0xf
	s_nop 1
	v_add_f32_dpp v8, v8, v8 row_mirror row_mask:0xf bank_mask:0xf
	v_mov_b32_e32 v9, v8
	s_nop 1
	v_permlane16_swap_b32_e32 v9, v8
	v_add_f32_e32 v8, v8, v9
	v_mov_b32_e32 v9, v8
	s_nop 1
	v_permlane32_swap_b32_e32 v9, v8
	v_add_f32_e32 v8, v8, v9
	v_fmamk_f32 v8, v8, 0x3a800000, v185
	v_cmp_gt_f32_e32 vcc, s55, v8
	v_mul_f32_e32 v9, 0x4f800000, v8
	s_nop 0
	v_cndmask_b32_e32 v8, v8, v9, vcc
	v_sqrt_f32_e32 v9, v8
	s_nop 0
	v_add_u32_e32 v10, -1, v9
	v_fma_f32 v11, -v10, v9, v8
	v_cmp_ge_f32_e64 s[12:13], 0, v11
	v_add_u32_e32 v11, 1, v9
	s_nop 0
	v_cndmask_b32_e64 v10, v9, v10, s[12:13]
	v_fma_f32 v9, -v11, v9, v8
	v_cmp_lt_f32_e64 s[12:13], 0, v9
	s_nop 1
	v_cndmask_b32_e64 v9, v10, v11, s[12:13]
	v_mul_f32_e32 v10, 0x37800000, v9
	v_cndmask_b32_e32 v9, v9, v10, vcc
	v_cmp_class_f32_e32 vcc, v8, v183
	s_nop 1
	v_cndmask_b32_e32 v8, v9, v8, vcc
	v_div_scale_f32 v9, s[12:13], v8, v8, 1.0
	v_rcp_f32_e32 v10, v9
	s_nop 0
	v_fma_f32 v11, -v9, v10, 1.0
	v_fmac_f32_e32 v10, v11, v10
	v_div_scale_f32 v11, vcc, 1.0, v8, 1.0
	v_mul_f32_e32 v72, v11, v10
	v_fma_f32 v73, -v9, v72, v11
	v_fmac_f32_e32 v72, v73, v10
	v_fma_f32 v9, -v9, v72, v11
	v_div_fmas_f32 v9, v9, v10, v72
	v_div_fixup_f32 v84, v9, v8, 1.0
	v_pk_mul_f32 v[86:87], v[74:75], v[84:85] op_sel_hi:[1,0]
	v_pk_mul_f32 v[88:89], v[76:77], v[84:85] op_sel_hi:[1,0]
	global_load_dwordx4 v[8:11], v[108:109], off offset:16
	global_load_dwordx4 v[72:75], v[108:109], off
	global_load_dwordx4 v[76:79], v[110:111], off offset:16
	global_load_dwordx4 v[80:83], v[110:111], off
	v_pk_mul_f32 v[2:3], v[2:3], v[84:85] op_sel_hi:[1,0]
	v_pk_mul_f32 v[0:1], v[0:1], v[84:85] op_sel_hi:[1,0]
	s_andn2_b64 vcc, exec, s[2:3]
	s_waitcnt vmcnt(1)
	v_pk_fma_f32 v[78:79], v[10:11], v[0:1], v[78:79]
	s_waitcnt vmcnt(0)
	v_pk_fma_f32 v[74:75], v[74:75], v[88:89], v[82:83]
	v_pk_fma_f32 v[72:73], v[72:73], v[86:87], v[80:81]
	v_pk_fma_f32 v[76:77], v[8:9], v[2:3], v[76:77]
	v_pk_mul_f32 v[80:81], v[6:7], v[84:85] op_sel_hi:[1,0]
	v_pk_mul_f32 v[82:83], v[4:5], v[84:85] op_sel_hi:[1,0]
	global_load_dwordx4 v[0:3], v[108:109], off offset:2064
	global_load_dwordx4 v[8:11], v[108:109], off offset:2048
	global_load_dwordx4 v[4:7], v[110:111], off offset:2064
	global_load_dwordx4 v[86:89], v[110:111], off offset:2048
	s_waitcnt vmcnt(0)
	v_pk_fma_f32 v[80:81], v[8:9], v[80:81], v[86:87]
	v_pk_mul_f32 v[8:9], v[14:15], v[84:85] op_sel_hi:[1,0]
	v_pk_fma_f32 v[82:83], v[10:11], v[82:83], v[88:89]
	v_pk_mul_f32 v[10:11], v[12:13], v[84:85] op_sel_hi:[1,0]
	v_pk_fma_f32 v[84:85], v[0:1], v[8:9], v[4:5]
	v_cndmask_b32_e64 v0, 0, 1, s[2:3]
	v_pk_fma_f32 v[86:87], v[2:3], v[10:11], v[6:7]
	v_cmp_ne_u32_e64 s[12:13], 1, v0
	s_cbranch_vccnz .LBB0_937

; __device__ __forceinline__ void phase_combine(CArgs a, LAS unsigned char* lds, int L, int wv, int xw  ) {
;     ...
;             for (int j = 0; j < 2; ++j) { const int c0 = lane * 8 + 512 * j; const u32x4 xr = *(const u32x4*)(Z + (size_t)tok * DM + c0); const f32x2 ms = *(const f32x2*)(MS + (size_t)tok * 2);
;                 const f32x4 z0 = (f32x4){bflo(xr.x), bfhi(xr.x), bflo(xr.y), bfhi(xr.y)}, z1 = (f32x4){bflo(xr.z), bfhi(xr.z), bflo(xr.w), bfhi(xr.w)};
;                 v[h][j][0] = DN_ALPHA * ((z0 - ms.x) * ms.y * *(const f32x4*)(lng0 + c0) + *(const f32x4*)(lnb0 + c0)); v[h][j][1] = DN_ALPHA * ((z1 - ms.x) * ms.y * *(const f32x4*)(lng0 + c0 + 4) + *(const f32x4*)(lnb0 + c0 + 4)); } }
; #pragma unroll
;         for (int k = 0; k < 4; ++k)
; #pragma unroll
;             for (int h = 0; h < 4; ++h) { const int ep = k == 0 ? ep4[h].x : k == 1 ? ep4[h].y : k == 2 ? ep4[h].z : ep4[h].w; const float g = g4[h][k];
;                 const size_t row = (size_t)misc[16 + (ep >> 16)] * 256 + (ep & 0xffff);
; #pragma unroll
;                 for (int j = 0; j < 2; ++j) { const u32x2 y = *(const u32x2*)(YS + row * DM + lane * 8 + 512 * j); const float gs = g * (1.f / QS_YS);
;                     const f32x2 y0 = __builtin_amdgcn_cvt_pk_f32_fp8((int)y.x, false), y1 = __builtin_amdgcn_cvt_pk_f32_fp8((int)y.x, true), y2 = __builtin_amdgcn_cvt_pk_f32_fp8((int)y.y, false), y3 = __builtin_amdgcn_cvt_pk_f32_fp8((int)y.y, true);
;                     v[h][j][0] += gs * (f32x4){y0.x, y0.y, y1.x, y1.y}; v[h][j][1] += gs * (f32x4){y2.x, y2.y, y3.x, y3.y}; } }
; #pragma unroll
;         for (int h = 0; h < 4; ++h) { const int tok = tk + h;
;             float s = 0.f;
; #pragma unroll
;             for (int j = 0; j < 2; ++j) s += ((v[h][j][0].x + v[h][j][0].y) + (v[h][j][0].z + v[h][j][0].w)) + ((v[h][j][1].x + v[h][j][1].y) + (v[h][j][1].z + v[h][j][1].w));
;             const float mean = wave_sum(s, lane) * (1.f / DM); float s2 = 0.f;
.LBB0_939:
	v_lshlrev_b32_e32 v10, 16, v64
	v_and_b32_e32 v11, 0xffff0000, v64
	v_lshlrev_b32_e32 v8, 16, v65
	v_and_b32_e32 v9, 0xffff0000, v65
	v_lshlrev_b32_e32 v14, 16, v66
	v_and_b32_e32 v15, 0xffff0000, v66
	v_lshlrev_b32_e32 v12, 16, v67
	v_and_b32_e32 v13, 0xffff0000, v67
	v_cvt_pk_f32_fp8_e32 v[64:65], v146
	v_cvt_pk_f32_fp8_sdwa v[66:67], v146 src0_sel:WORD_1
	v_lshlrev_b32_e32 v2, 16, v68
	v_and_b32_e32 v3, 0xffff0000, v68
	v_lshlrev_b32_e32 v0, 16, v69
	v_and_b32_e32 v1, 0xffff0000, v69
	v_lshlrev_b32_e32 v6, 16, v70
	v_and_b32_e32 v7, 0xffff0000, v70
	v_lshlrev_b32_e32 v4, 16, v71
	v_and_b32_e32 v5, 0xffff0000, v71
	v_cvt_pk_f32_fp8_e32 v[68:69], v147
	v_cvt_pk_f32_fp8_sdwa v[70:71], v147 src0_sel:WORD_1
	v_sub_f32_e32 v1, v1, v120
	v_sub_f32_e32 v0, v0, v120
	v_sub_f32_e32 v3, v3, v120
	v_sub_f32_e32 v2, v2, v120
	v_pk_mul_f32 v[2:3], v[120:121], v[2:3] op_sel:[1,0]
	v_pk_mul_f32 v[0:1], v[120:121], v[0:1] op_sel:[1,0]
	v_sub_f32_e32 v5, v5, v120
	v_sub_f32_e32 v4, v4, v120
	v_sub_f32_e32 v7, v7, v120
	v_sub_f32_e32 v6, v6, v120
	v_mul_f32_e32 v60, 0x3d000000, v60
	v_pk_fma_f32 v[0:1], v[42:43], v[0:1], v[46:47]
	v_pk_fma_f32 v[2:3], v[40:41], v[2:3], v[44:45]
	v_pk_mul_f32 v[6:7], v[120:121], v[6:7] op_sel:[1,0]
	v_pk_mul_f32 v[4:5], v[120:121], v[4:5] op_sel:[1,0]
	v_pk_mul_f32 v[66:67], v[60:61], v[66:67] op_sel_hi:[0,1]
	v_pk_mul_f32 v[64:65], v[60:61], v[64:65] op_sel_hi:[0,1]
	v_pk_fma_f32 v[4:5], v[34:35], v[4:5], v[38:39]
	v_pk_fma_f32 v[6:7], v[32:33], v[6:7], v[36:37]
	v_pk_fma_f32 v[2:3], v[2:3], s[70:71], v[64:65] op_sel_hi:[1,0,1]
	v_pk_fma_f32 v[0:1], v[0:1], s[70:71], v[66:67] op_sel_hi:[1,0,1]
	v_pk_mul_f32 v[64:65], v[60:61], v[70:71] op_sel_hi:[0,1]
	v_pk_mul_f32 v[66:67], v[60:61], v[68:69] op_sel_hi:[0,1]
	v_pk_fma_f32 v[6:7], v[6:7], s[70:71], v[66:67] op_sel_hi:[1,0,1]
	v_pk_fma_f32 v[4:5], v[4:5], s[70:71], v[64:65] op_sel_hi:[1,0,1]
	v_cvt_pk_f32_fp8_e32 v[64:65], v144
	v_cvt_pk_f32_fp8_sdwa v[66:67], v144 src0_sel:WORD_1
	v_cvt_pk_f32_fp8_e32 v[68:69], v145
	v_cvt_pk_f32_fp8_sdwa v[70:71], v145 src0_sel:WORD_1
	v_sub_f32_e32 v9, v9, v120
	v_sub_f32_e32 v8, v8, v120
	v_sub_f32_e32 v11, v11, v120
	v_sub_f32_e32 v10, v10, v120
	v_pk_mul_f32 v[10:11], v[120:121], v[10:11] op_sel:[1,0]
	v_pk_mul_f32 v[8:9], v[120:121], v[8:9] op_sel:[1,0]
	v_sub_f32_e32 v13, v13, v120
	v_sub_f32_e32 v12, v12, v120
	v_sub_f32_e32 v15, v15, v120
	v_sub_f32_e32 v14, v14, v120
	v_pk_fma_f32 v[8:9], v[26:27], v[8:9], v[30:31]
	v_pk_fma_f32 v[10:11], v[24:25], v[10:11], v[28:29]
	v_pk_mul_f32 v[14:15], v[120:121], v[14:15] op_sel:[1,0]
	v_pk_mul_f32 v[12:13], v[120:121], v[12:13] op_sel:[1,0]
	v_pk_mul_f32 v[66:67], v[60:61], v[66:67] op_sel_hi:[0,1]
	v_pk_mul_f32 v[64:65], v[60:61], v[64:65] op_sel_hi:[0,1]
	v_pk_fma_f32 v[12:13], v[18:19], v[12:13], v[22:23]
	v_pk_fma_f32 v[14:15], v[16:17], v[14:15], v[20:21]
	v_pk_fma_f32 v[10:11], v[10:11], s[70:71], v[64:65] op_sel_hi:[1,0,1]
	v_pk_fma_f32 v[8:9], v[8:9], s[70:71], v[66:67] op_sel_hi:[1,0,1]
	v_pk_mul_f32 v[64:65], v[60:61], v[70:71] op_sel_hi:[0,1]
	v_pk_mul_f32 v[66:67], v[60:61], v[68:69] op_sel_hi:[0,1]
	v_pk_fma_f32 v[14:15], v[14:15], s[70:71], v[66:67] op_sel_hi:[1,0,1]
	v_pk_fma_f32 v[12:13], v[12:13], s[70:71], v[64:65] op_sel_hi:[1,0,1]
	v_cvt_pk_f32_fp8_e32 v[64:65], v142
	v_cvt_pk_f32_fp8_sdwa v[66:67], v142 src0_sel:WORD_1
	v_cvt_pk_f32_fp8_e32 v[68:69], v143
	v_cvt_pk_f32_fp8_sdwa v[70:71], v143 src0_sel:WORD_1
	v_mul_f32_e32 v60, 0x3d000000, v61
	v_pk_fma_f32 v[0:1], v[60:61], v[66:67], v[0:1] op_sel_hi:[0,1,1]
	v_pk_fma_f32 v[2:3], v[60:61], v[64:65], v[2:3] op_sel_hi:[0,1,1]
	v_pk_fma_f32 v[4:5], v[60:61], v[70:71], v[4:5] op_sel_hi:[0,1,1]
	v_pk_fma_f32 v[6:7], v[60:61], v[68:69], v[6:7] op_sel_hi:[0,1,1]
	v_cvt_pk_f32_fp8_e32 v[64:65], v136
	v_cvt_pk_f32_fp8_sdwa v[66:67], v136 src0_sel:WORD_1
	v_cvt_pk_f32_fp8_e32 v[68:69], v137
	v_cvt_pk_f32_fp8_sdwa v[70:71], v137 src0_sel:WORD_1
	v_pk_fma_f32 v[10:11], v[60:61], v[64:65], v[10:11] op_sel_hi:[0,1,1]
	v_pk_fma_f32 v[8:9], v[60:61], v[66:67], v[8:9] op_sel_hi:[0,1,1]
	v_pk_fma_f32 v[14:15], v[60:61], v[68:69], v[14:15] op_sel_hi:[0,1,1]
	v_pk_fma_f32 v[12:13], v[60:61], v[70:71], v[12:13] op_sel_hi:[0,1,1]
	v_cvt_pk_f32_fp8_e32 v[64:65], v140
	v_cvt_pk_f32_fp8_sdwa v[66:67], v140 src0_sel:WORD_1
	v_cvt_pk_f32_fp8_e32 v[68:69], v141
	v_cvt_pk_f32_fp8_sdwa v[70:71], v141 src0_sel:WORD_1
	v_mul_f32_e32 v60, 0x3d000000, v62
	v_pk_fma_f32 v[2:3], v[60:61], v[64:65], v[2:3] op_sel_hi:[0,1,1]
	v_pk_fma_f32 v[0:1], v[60:61], v[66:67], v[0:1] op_sel_hi:[0,1,1]
	v_pk_fma_f32 v[6:7], v[60:61], v[68:69], v[6:7] op_sel_hi:[0,1,1]
	v_pk_fma_f32 v[4:5], v[60:61], v[70:71], v[4:5] op_sel_hi:[0,1,1]
	v_cvt_pk_f32_fp8_e32 v[64:65], v138
	v_cvt_pk_f32_fp8_sdwa v[66:67], v138 src0_sel:WORD_1
	v_cvt_pk_f32_fp8_e32 v[68:69], v139
	v_cvt_pk_f32_fp8_sdwa v[70:71], v139 src0_sel:WORD_1
	v_pk_fma_f32 v[10:11], v[60:61], v[64:65], v[10:11] op_sel_hi:[0,1,1]
	v_pk_fma_f32 v[8:9], v[60:61], v[66:67], v[8:9] op_sel_hi:[0,1,1]
	v_pk_fma_f32 v[14:15], v[60:61], v[68:69], v[14:15] op_sel_hi:[0,1,1]
	v_pk_fma_f32 v[12:13], v[60:61], v[70:71], v[12:13] op_sel_hi:[0,1,1]
	v_mul_f32_e32 v60, 0x3d000000, v63
	v_cvt_pk_f32_fp8_e32 v[62:63], v154
	v_cvt_pk_f32_fp8_e32 v[66:67], v155
	v_cvt_pk_f32_fp8_sdwa v[64:65], v154 src0_sel:WORD_1
	v_cvt_pk_f32_fp8_sdwa v[68:69], v155 src0_sel:WORD_1
	v_pk_fma_f32 v[62:63], v[60:61], v[62:63], v[2:3] op_sel_hi:[0,1,1]
	v_pk_fma_f32 v[2:3], v[60:61], v[66:67], v[6:7] op_sel_hi:[0,1,1]
	v_cvt_pk_f32_fp8_e32 v[6:7], v156
	v_pk_fma_f32 v[64:65], v[60:61], v[64:65], v[0:1] op_sel_hi:[0,1,1]
	v_pk_fma_f32 v[0:1], v[60:61], v[68:69], v[4:5] op_sel_hi:[0,1,1]
	v_cvt_pk_f32_fp8_sdwa v[4:5], v156 src0_sel:WORD_1
	v_cvt_pk_f32_fp8_e32 v[66:67], v157
	v_cvt_pk_f32_fp8_sdwa v[68:69], v157 src0_sel:WORD_1
	v_pk_fma_f32 v[6:7], v[60:61], v[6:7], v[10:11] op_sel_hi:[0,1,1]
	v_pk_fma_f32 v[4:5], v[60:61], v[4:5], v[8:9] op_sel_hi:[0,1,1]
	v_mov_b32_e32 v8, v62
	v_mov_b32_e32 v9, v6
	v_mov_b32_e32 v10, v63
	v_mov_b32_e32 v11, v7
	v_pk_fma_f32 v[12:13], v[60:61], v[68:69], v[12:13] op_sel_hi:[0,1,1]
	v_pk_fma_f32 v[14:15], v[60:61], v[66:67], v[14:15] op_sel_hi:[0,1,1]
	v_pk_add_f32 v[8:9], v[8:9], v[10:11]
	v_mov_b32_e32 v10, v64
	v_mov_b32_e32 v11, v4
	v_mov_b32_e32 v60, v65
	v_mov_b32_e32 v61, v5
	v_pk_add_f32 v[10:11], v[10:11], v[60:61]
	v_mov_b32_e32 v60, v3
	v_pk_add_f32 v[8:9], v[8:9], v[10:11]
	v_mov_b32_e32 v10, v2
	v_mov_b32_e32 v11, v14
	v_mov_b32_e32 v61, v15
	v_pk_add_f32 v[10:11], v[10:11], v[60:61]
	v_mov_b32_e32 v60, v0
	v_mov_b32_e32 v61, v12
	v_mov_b32_e32 v66, v1
	v_mov_b32_e32 v67, v13
	v_pk_add_f32 v[60:61], v[60:61], v[66:67]
	s_nop 0
	v_pk_add_f32 v[10:11], v[10:11], v[60:61]
	s_nop 0
	v_pk_add_f32 v[8:9], v[8:9], v[10:11]
	s_nop 0
	v_add_f32_e32 v8, 0, v8
	v_add_f32_e32 v8, v8, v9
	s_waitcnt lgkmcnt(0)
; __device__ __forceinline__ float shx(float v, int m, int lane) { return __builtin_bit_cast(float, __builtin_amdgcn_ds_bpermute((lane ^ m) << 2, __builtin_bit_cast(int, v))); }
; __device__ __forceinline__ float wave_sum(float v, int lane) {
; #pragma unroll
;     for (int o = 1; o < 64; o <<= 1) v += shx(v, o, lane);
;     return v;
; __device__ __forceinline__ void phase_combine(CArgs a, LAS unsigned char* lds, int L, int wv, int xw  ) {
;     ...
;             const float mean = wave_sum(s, lane) * (1.f / DM); float s2 = 0.f;
; #pragma unroll
;             for (int j = 0; j < 2; ++j) { v[h][j][0] = v[h][j][0] - mean; v[h][j][1] = v[h][j][1] - mean;
;                 s2 += ((v[h][j][0].x * v[h][j][0].x + v[h][j][0].y * v[h][j][0].y) + (v[h][j][0].z * v[h][j][0].z + v[h][j][0].w * v[h][j][0].w)) + ((v[h][j][1].x * v[h][j][1].x + v[h][j][1].y * v[h][j][1].y) + (v[h][j][1].z * v[h][j][1].z + v[h][j][1].w * v[h][j][1].w)); }
;             const float rstd = 1.0f / sqrtf(wave_sum(s2, lane) * (1.f / DM) + LN_EPS);
;             float am = 0.f;
; #pragma unroll
;             for (int j = 0; j < 2; ++j) { const int c0 = lane * 8 + 512 * j;
;                 v[h][j][0] = v[h][j][0] * rstd * *(const f32x4*)(lng + c0) + *(const f32x4*)(lnb + c0); v[h][j][1] = v[h][j][1] * rstd * *(const f32x4*)(lng + c0 + 4) + *(const f32x4*)(lnb + c0 + 4);
	s_nop 1
	v_add_f32_dpp v8, v8, v8 quad_perm:[1,0,3,2] row_mask:0xf bank_mask:0xf
	s_nop 1
	v_add_f32_dpp v8, v8, v8 quad_perm:[2,3,0,1] row_mask:0xf bank_mask:0xf
	s_nop 1
	v_add_f32_dpp v8, v8, v8 row_half_mirror row_mask:0xf bank_mask:0xf
	s_nop 1
	v_add_f32_dpp v8, v8, v8 row_mirror row_mask:0xf bank_mask:0xf
	v_mov_b32_e32 v9, v8
	s_nop 1
	v_permlane16_swap_b32_e32 v9, v8
	v_add_f32_e32 v8, v8, v9
	v_mov_b32_e32 v9, v8
	s_nop 1
	v_permlane32_swap_b32_e32 v9, v8
	v_add_f32_e32 v8, v8, v9
	v_fmamk_f32 v63, v8, 0xba800000, v63
	v_fmamk_f32 v7, v8, 0xba800000, v7
	v_fmamk_f32 v65, v8, 0xba800000, v65
	v_fmac_f32_e32 v62, 0xba800000, v8
	v_fmamk_f32 v5, v8, 0xba800000, v5
	v_fmac_f32_e32 v6, 0xba800000, v8
	v_mov_b32_e32 v10, v63
	v_mov_b32_e32 v11, v7
	v_fmac_f32_e32 v64, 0xba800000, v8
	v_fmamk_f32 v1, v8, 0xba800000, v1
	v_fmac_f32_e32 v0, 0xba800000, v8
	v_fmamk_f32 v3, v8, 0xba800000, v3
	v_fmac_f32_e32 v2, 0xba800000, v8
	v_fmac_f32_e32 v4, 0xba800000, v8
	v_fmamk_f32 v13, v8, 0xba800000, v13
	v_fmac_f32_e32 v12, 0xba800000, v8
	v_fmamk_f32 v15, v8, 0xba800000, v15
	v_fmac_f32_e32 v14, 0xba800000, v8
	v_mov_b32_e32 v8, v62
	v_mov_b32_e32 v9, v6
	v_pk_mul_f32 v[10:11], v[10:11], v[10:11]
	v_mov_b32_e32 v60, v65
	v_mov_b32_e32 v61, v5
	v_pk_fma_f32 v[8:9], v[8:9], v[8:9], v[10:11]
	v_mov_b32_e32 v10, v64
	v_mov_b32_e32 v11, v4
	v_pk_mul_f32 v[60:61], v[60:61], v[60:61]
	v_mov_b32_e32 v66, v1
	v_pk_fma_f32 v[10:11], v[10:11], v[10:11], v[60:61]
	v_mov_b32_e32 v60, v3
	v_mov_b32_e32 v61, v15
	v_pk_add_f32 v[8:9], v[8:9], v[10:11]
	v_mov_b32_e32 v10, v2
	v_mov_b32_e32 v11, v14
	v_pk_mul_f32 v[60:61], v[60:61], v[60:61]
	v_mov_b32_e32 v67, v13
	v_pk_fma_f32 v[10:11], v[10:11], v[10:11], v[60:61]
	v_mov_b32_e32 v60, v0
	v_mov_b32_e32 v61, v12
	v_pk_mul_f32 v[66:67], v[66:67], v[66:67]
	s_nop 0
	v_pk_fma_f32 v[60:61], v[60:61], v[60:61], v[66:67]
	s_nop 0
	v_pk_add_f32 v[10:11], v[10:11], v[60:61]
	s_nop 0
	v_pk_add_f32 v[8:9], v[8:9], v[10:11]
	s_nop 0
	v_add_f32_e32 v8, v8, v9
	s_waitcnt lgkmcnt(0)
	s_nop 1
	v_add_f32_dpp v8, v8, v8 quad_perm:[1,0,3,2] row_mask:0xf bank_mask:0xf
	s_nop 1
	v_add_f32_dpp v8, v8, v8 quad_perm:[2,3,0,1] row_mask:0xf bank_mask:0xf
	s_nop 1
	v_add_f32_dpp v8, v8, v8 row_half_mirror row_mask:0xf bank_mask:0xf
	s_nop 1
	v_add_f32_dpp v8, v8, v8 row_mirror row_mask:0xf bank_mask:0xf
	v_mov_b32_e32 v9, v8
	s_nop 1
	v_permlane16_swap_b32_e32 v9, v8
	v_add_f32_e32 v8, v8, v9
	v_mov_b32_e32 v9, v8
	s_nop 1
	v_permlane32_swap_b32_e32 v9, v8
	v_add_f32_e32 v8, v8, v9
	v_fmamk_f32 v8, v8, 0x3a800000, v185
	v_cmp_gt_f32_e32 vcc, s55, v8
	v_mul_f32_e32 v9, 0x4f800000, v8
	s_nop 0
	v_cndmask_b32_e32 v8, v8, v9, vcc
	v_sqrt_f32_e32 v9, v8
	s_nop 0
	v_add_u32_e32 v10, -1, v9
	v_fma_f32 v11, -v10, v9, v8
	v_cmp_ge_f32_e64 s[14:15], 0, v11
	v_add_u32_e32 v11, 1, v9
	s_nop 0
	v_cndmask_b32_e64 v10, v9, v10, s[14:15]
	v_fma_f32 v9, -v11, v9, v8
	v_cmp_lt_f32_e64 s[14:15], 0, v9
	s_nop 1
	v_cndmask_b32_e64 v9, v10, v11, s[14:15]
	v_mul_f32_e32 v10, 0x37800000, v9
	v_cndmask_b32_e32 v9, v9, v10, vcc
	v_cmp_class_f32_e32 vcc, v8, v183
	s_nop 1
	v_cndmask_b32_e32 v8, v9, v8, vcc
	v_div_scale_f32 v9, s[14:15], v8, v8, 1.0
	v_rcp_f32_e32 v10, v9
	s_mov_b64 s[14:15], -1
	v_fma_f32 v11, -v9, v10, 1.0
	v_fmac_f32_e32 v10, v11, v10
	v_div_scale_f32 v11, vcc, 1.0, v8, 1.0
	v_mul_f32_e32 v60, v11, v10
	v_fma_f32 v61, -v9, v60, v11
	v_fmac_f32_e32 v60, v61, v10
	v_fma_f32 v9, -v9, v60, v11
	v_div_fmas_f32 v9, v9, v10, v60
	v_div_fixup_f32 v72, v9, v8, 1.0
	v_pk_mul_f32 v[74:75], v[62:63], v[72:73] op_sel_hi:[1,0]
	v_pk_mul_f32 v[76:77], v[64:65], v[72:73] op_sel_hi:[1,0]
	global_load_dwordx4 v[8:11], v[108:109], off offset:16
	global_load_dwordx4 v[60:63], v[108:109], off
	global_load_dwordx4 v[64:67], v[110:111], off offset:16
	global_load_dwordx4 v[68:71], v[110:111], off
	v_pk_mul_f32 v[2:3], v[2:3], v[72:73] op_sel_hi:[1,0]
	v_pk_mul_f32 v[0:1], v[0:1], v[72:73] op_sel_hi:[1,0]
	s_and_b64 vcc, exec, s[12:13]
	s_waitcnt vmcnt(1)
	v_pk_fma_f32 v[66:67], v[10:11], v[0:1], v[66:67]
	s_waitcnt vmcnt(0)
	v_pk_fma_f32 v[62:63], v[62:63], v[76:77], v[70:71]
	v_pk_fma_f32 v[60:61], v[60:61], v[74:75], v[68:69]
	v_pk_fma_f32 v[64:65], v[8:9], v[2:3], v[64:65]
	v_pk_mul_f32 v[68:69], v[6:7], v[72:73] op_sel_hi:[1,0]
	v_pk_mul_f32 v[70:71], v[4:5], v[72:73] op_sel_hi:[1,0]
	global_load_dwordx4 v[0:3], v[108:109], off offset:2064
	global_load_dwordx4 v[8:11], v[108:109], off offset:2048
	global_load_dwordx4 v[4:7], v[110:111], off offset:2064
	global_load_dwordx4 v[74:77], v[110:111], off offset:2048
	s_waitcnt vmcnt(0)
	v_pk_fma_f32 v[70:71], v[10:11], v[70:71], v[76:77]
	v_pk_fma_f32 v[68:69], v[8:9], v[68:69], v[74:75]
	v_pk_mul_f32 v[8:9], v[14:15], v[72:73] op_sel_hi:[1,0]
	v_pk_mul_f32 v[10:11], v[12:13], v[72:73] op_sel_hi:[1,0]
	v_pk_fma_f32 v[72:73], v[0:1], v[8:9], v[4:5]
	v_pk_fma_f32 v[74:75], v[2:3], v[10:11], v[6:7]
	s_cbranch_vccnz .LBB0_947

; __device__ __forceinline__ void phase_combine(CArgs a, LAS unsigned char* lds, int L, int wv, int xw  ) {
;     ...
;             for (int j = 0; j < 2; ++j) { const int c0 = lane * 8 + 512 * j; const u32x4 xr = *(const u32x4*)(Z + (size_t)tok * DM + c0); const f32x2 ms = *(const f32x2*)(MS + (size_t)tok * 2);
;                 const f32x4 z0 = (f32x4){bflo(xr.x), bfhi(xr.x), bflo(xr.y), bfhi(xr.y)}, z1 = (f32x4){bflo(xr.z), bfhi(xr.z), bflo(xr.w), bfhi(xr.w)};
;                 v[h][j][0] = DN_ALPHA * ((z0 - ms.x) * ms.y * *(const f32x4*)(lng0 + c0) + *(const f32x4*)(lnb0 + c0)); v[h][j][1] = DN_ALPHA * ((z1 - ms.x) * ms.y * *(const f32x4*)(lng0 + c0 + 4) + *(const f32x4*)(lnb0 + c0 + 4)); } }
; #pragma unroll
;         for (int k = 0; k < 4; ++k)
; #pragma unroll
;             for (int h = 0; h < 4; ++h) { const int ep = k == 0 ? ep4[h].x : k == 1 ? ep4[h].y : k == 2 ? ep4[h].z : ep4[h].w; const float g = g4[h][k];
;                 const size_t row = (size_t)misc[16 + (ep >> 16)] * 256 + (ep & 0xffff);
; #pragma unroll
;                 for (int j = 0; j < 2; ++j) { const u32x2 y = *(const u32x2*)(YS + row * DM + lane * 8 + 512 * j); const float gs = g * (1.f / QS_YS);
;                     const f32x2 y0 = __builtin_amdgcn_cvt_pk_f32_fp8((int)y.x, false), y1 = __builtin_amdgcn_cvt_pk_f32_fp8((int)y.x, true), y2 = __builtin_amdgcn_cvt_pk_f32_fp8((int)y.y, false), y3 = __builtin_amdgcn_cvt_pk_f32_fp8((int)y.y, true);
;                     v[h][j][0] += gs * (f32x4){y0.x, y0.y, y1.x, y1.y}; v[h][j][1] += gs * (f32x4){y2.x, y2.y, y3.x, y3.y}; } }
; #pragma unroll
;         for (int h = 0; h < 4; ++h) { const int tok = tk + h;
;             float s = 0.f;
; #pragma unroll
;             for (int j = 0; j < 2; ++j) s += ((v[h][j][0].x + v[h][j][0].y) + (v[h][j][0].z + v[h][j][0].w)) + ((v[h][j][1].x + v[h][j][1].y) + (v[h][j][1].z + v[h][j][1].w));
;             const float mean = wave_sum(s, lane) * (1.f / DM); float s2 = 0.f;
.LBB0_949:
	v_lshlrev_b32_e32 v12, 16, v55
	v_and_b32_e32 v13, 0xffff0000, v55
	v_lshlrev_b32_e32 v10, 16, v52
	v_and_b32_e32 v11, 0xffff0000, v52
	v_sub_f32_e32 v13, v13, v118
	v_sub_f32_e32 v12, v12, v118
	v_lshlrev_b32_e32 v14, 16, v54
	v_and_b32_e32 v15, 0xffff0000, v54
	v_sub_f32_e32 v11, v11, v118
	v_sub_f32_e32 v10, v10, v118
	v_pk_mul_f32 v[12:13], v[118:119], v[12:13] op_sel:[1,0]
	v_pk_mul_f32 v[10:11], v[118:119], v[10:11] op_sel:[1,0]
	v_sub_f32_e32 v15, v15, v118
	v_sub_f32_e32 v14, v14, v118
	v_pk_fma_f32 v[12:13], v[18:19], v[12:13], v[22:23]
	v_cvt_pk_f32_fp8_sdwa v[18:19], v132 src0_sel:WORD_1
	v_lshlrev_b32_e32 v0, 16, v57
	v_and_b32_e32 v1, 0xffff0000, v57
	v_pk_fma_f32 v[10:11], v[24:25], v[10:11], v[28:29]
	v_pk_mul_f32 v[14:15], v[118:119], v[14:15] op_sel:[1,0]
	v_cvt_pk_f32_fp8_sdwa v[24:25], v133 src0_sel:WORD_1
	v_lshlrev_b32_e32 v4, 16, v59
	v_and_b32_e32 v5, 0xffff0000, v59
	v_sub_f32_e32 v1, v1, v118
	v_sub_f32_e32 v0, v0, v118
	v_pk_fma_f32 v[14:15], v[16:17], v[14:15], v[20:21]
	v_cvt_pk_f32_fp8_e32 v[20:21], v132
	v_lshlrev_b32_e32 v2, 16, v56
	v_and_b32_e32 v3, 0xffff0000, v56
	v_pk_mul_f32 v[0:1], v[118:119], v[0:1] op_sel:[1,0]
	v_sub_f32_e32 v5, v5, v118
	v_sub_f32_e32 v4, v4, v118
	v_mul_f32_e32 v16, 0x3d000000, v48
	v_cvt_pk_f32_fp8_e32 v[22:23], v133
	v_lshlrev_b32_e32 v6, 16, v58
	v_and_b32_e32 v7, 0xffff0000, v58
	v_sub_f32_e32 v3, v3, v118
	v_sub_f32_e32 v2, v2, v118
	v_pk_fma_f32 v[0:1], v[42:43], v[0:1], v[46:47]
	v_pk_mul_f32 v[4:5], v[118:119], v[4:5] op_sel:[1,0]
	v_pk_mul_f32 v[18:19], v[16:17], v[18:19] op_sel_hi:[0,1]
	v_pk_mul_f32 v[2:3], v[118:119], v[2:3] op_sel:[1,0]
	v_sub_f32_e32 v7, v7, v118
	v_sub_f32_e32 v6, v6, v118
	v_pk_fma_f32 v[4:5], v[34:35], v[4:5], v[38:39]
	v_pk_fma_f32 v[0:1], v[0:1], s[70:71], v[18:19] op_sel_hi:[1,0,1]
	v_pk_mul_f32 v[18:19], v[16:17], v[24:25] op_sel_hi:[0,1]
	v_pk_fma_f32 v[2:3], v[40:41], v[2:3], v[44:45]
	v_pk_mul_f32 v[6:7], v[118:119], v[6:7] op_sel:[1,0]
	v_pk_mul_f32 v[20:21], v[16:17], v[20:21] op_sel_hi:[0,1]
	v_pk_fma_f32 v[4:5], v[4:5], s[70:71], v[18:19] op_sel_hi:[1,0,1]
	v_cvt_pk_f32_fp8_sdwa v[18:19], v124 src0_sel:WORD_1
	v_pk_fma_f32 v[6:7], v[32:33], v[6:7], v[36:37]
	v_lshlrev_b32_e32 v8, 16, v53
	v_and_b32_e32 v9, 0xffff0000, v53
	v_pk_fma_f32 v[2:3], v[2:3], s[70:71], v[20:21] op_sel_hi:[1,0,1]
	v_pk_mul_f32 v[20:21], v[16:17], v[22:23] op_sel_hi:[0,1]
	v_cvt_pk_f32_fp8_sdwa v[24:25], v125 src0_sel:WORD_1
	v_sub_f32_e32 v9, v9, v118
	v_sub_f32_e32 v8, v8, v118
	v_pk_fma_f32 v[6:7], v[6:7], s[70:71], v[20:21] op_sel_hi:[1,0,1]
	v_cvt_pk_f32_fp8_e32 v[20:21], v124
	v_pk_mul_f32 v[8:9], v[118:119], v[8:9] op_sel:[1,0]
	v_cvt_pk_f32_fp8_e32 v[22:23], v125
	v_pk_fma_f32 v[8:9], v[26:27], v[8:9], v[30:31]
	v_pk_mul_f32 v[18:19], v[16:17], v[18:19] op_sel_hi:[0,1]
	v_pk_fma_f32 v[8:9], v[8:9], s[70:71], v[18:19] op_sel_hi:[1,0,1]
	v_pk_mul_f32 v[18:19], v[16:17], v[24:25] op_sel_hi:[0,1]
	v_pk_mul_f32 v[20:21], v[16:17], v[20:21] op_sel_hi:[0,1]
	v_pk_fma_f32 v[12:13], v[12:13], s[70:71], v[18:19] op_sel_hi:[1,0,1]
	v_cvt_pk_f32_fp8_sdwa v[18:19], v128 src0_sel:WORD_1
	v_pk_fma_f32 v[10:11], v[10:11], s[70:71], v[20:21] op_sel_hi:[1,0,1]
	v_pk_mul_f32 v[16:17], v[16:17], v[22:23] op_sel_hi:[0,1]
	v_cvt_pk_f32_fp8_e32 v[20:21], v128
	v_cvt_pk_f32_fp8_sdwa v[22:23], v129 src0_sel:WORD_1
	v_cvt_pk_f32_fp8_e32 v[24:25], v129
	v_pk_fma_f32 v[14:15], v[14:15], s[70:71], v[16:17] op_sel_hi:[1,0,1]
	v_mul_f32_e32 v16, 0x3d000000, v49
	v_pk_fma_f32 v[0:1], v[16:17], v[18:19], v[0:1] op_sel_hi:[0,1,1]
	v_cvt_pk_f32_fp8_sdwa v[18:19], v122 src0_sel:WORD_1
	v_pk_fma_f32 v[2:3], v[16:17], v[20:21], v[2:3] op_sel_hi:[0,1,1]
	v_pk_fma_f32 v[4:5], v[16:17], v[22:23], v[4:5] op_sel_hi:[0,1,1]
	v_pk_fma_f32 v[6:7], v[16:17], v[24:25], v[6:7] op_sel_hi:[0,1,1]
	v_cvt_pk_f32_fp8_e32 v[20:21], v122
	v_cvt_pk_f32_fp8_sdwa v[22:23], v123 src0_sel:WORD_1
	v_cvt_pk_f32_fp8_e32 v[24:25], v123
	v_pk_fma_f32 v[8:9], v[16:17], v[18:19], v[8:9] op_sel_hi:[0,1,1]
	v_cvt_pk_f32_fp8_e32 v[18:19], v130
	v_pk_fma_f32 v[10:11], v[16:17], v[20:21], v[10:11] op_sel_hi:[0,1,1]
	v_pk_fma_f32 v[12:13], v[16:17], v[22:23], v[12:13] op_sel_hi:[0,1,1]
	v_pk_fma_f32 v[14:15], v[16:17], v[24:25], v[14:15] op_sel_hi:[0,1,1]
	v_cvt_pk_f32_fp8_sdwa v[20:21], v130 src0_sel:WORD_1
	v_cvt_pk_f32_fp8_e32 v[22:23], v131
	v_cvt_pk_f32_fp8_sdwa v[24:25], v131 src0_sel:WORD_1
	v_mul_f32_e32 v16, 0x3d000000, v50
	v_pk_fma_f32 v[2:3], v[16:17], v[18:19], v[2:3] op_sel_hi:[0,1,1]
	v_cvt_pk_f32_fp8_e32 v[18:19], v126
	v_pk_fma_f32 v[0:1], v[16:17], v[20:21], v[0:1] op_sel_hi:[0,1,1]
	v_pk_fma_f32 v[6:7], v[16:17], v[22:23], v[6:7] op_sel_hi:[0,1,1]
	v_pk_fma_f32 v[4:5], v[16:17], v[24:25], v[4:5] op_sel_hi:[0,1,1]
	v_cvt_pk_f32_fp8_sdwa v[20:21], v126 src0_sel:WORD_1
	v_cvt_pk_f32_fp8_e32 v[22:23], v127
	v_cvt_pk_f32_fp8_sdwa v[24:25], v127 src0_sel:WORD_1
	v_pk_fma_f32 v[18:19], v[16:17], v[18:19], v[10:11] op_sel_hi:[0,1,1]
	v_cvt_pk_f32_fp8_e32 v[10:11], v150
	v_pk_fma_f32 v[20:21], v[16:17], v[20:21], v[8:9] op_sel_hi:[0,1,1]
	v_pk_fma_f32 v[14:15], v[16:17], v[22:23], v[14:15] op_sel_hi:[0,1,1]
	v_pk_fma_f32 v[12:13], v[16:17], v[24:25], v[12:13] op_sel_hi:[0,1,1]
	v_cvt_pk_f32_fp8_sdwa v[8:9], v150 src0_sel:WORD_1
	v_cvt_pk_f32_fp8_sdwa v[22:23], v151 src0_sel:WORD_1
	v_cvt_pk_f32_fp8_e32 v[24:25], v151
	v_mul_f32_e32 v16, 0x3d000000, v51
	v_pk_fma_f32 v[10:11], v[16:17], v[10:11], v[2:3] op_sel_hi:[0,1,1]
	v_cvt_pk_f32_fp8_e32 v[2:3], v148
	v_pk_fma_f32 v[8:9], v[16:17], v[8:9], v[0:1] op_sel_hi:[0,1,1]
	v_pk_fma_f32 v[4:5], v[16:17], v[22:23], v[4:5] op_sel_hi:[0,1,1]
	v_pk_fma_f32 v[6:7], v[16:17], v[24:25], v[6:7] op_sel_hi:[0,1,1]
	v_cvt_pk_f32_fp8_sdwa v[0:1], v148 src0_sel:WORD_1
	v_cvt_pk_f32_fp8_sdwa v[22:23], v149 src0_sel:WORD_1
	v_cvt_pk_f32_fp8_e32 v[24:25], v149
	v_pk_fma_f32 v[46:47], v[16:17], v[2:3], v[18:19] op_sel_hi:[0,1,1]
	v_pk_fma_f32 v[44:45], v[16:17], v[0:1], v[20:21] op_sel_hi:[0,1,1]
	v_pk_fma_f32 v[0:1], v[16:17], v[22:23], v[12:13] op_sel_hi:[0,1,1]
	v_pk_fma_f32 v[2:3], v[16:17], v[24:25], v[14:15] op_sel_hi:[0,1,1]
	v_mov_b32_e32 v12, v10
	v_mov_b32_e32 v13, v46
	v_mov_b32_e32 v14, v11
	v_mov_b32_e32 v15, v47
	v_pk_add_f32 v[12:13], v[12:13], v[14:15]
	v_mov_b32_e32 v14, v8
	v_mov_b32_e32 v15, v44
	v_mov_b32_e32 v16, v9
	v_mov_b32_e32 v17, v45
	v_pk_add_f32 v[14:15], v[14:15], v[16:17]
	v_mov_b32_e32 v16, v7
	v_pk_add_f32 v[12:13], v[12:13], v[14:15]
	v_mov_b32_e32 v14, v6
	v_mov_b32_e32 v15, v2
	v_mov_b32_e32 v17, v3
	v_pk_add_f32 v[14:15], v[14:15], v[16:17]
	v_mov_b32_e32 v16, v4
	v_mov_b32_e32 v17, v0
	v_mov_b32_e32 v18, v5
	v_mov_b32_e32 v19, v1
	v_pk_add_f32 v[16:17], v[16:17], v[18:19]
	s_nop 0
	v_pk_add_f32 v[14:15], v[14:15], v[16:17]
	s_nop 0
	v_pk_add_f32 v[12:13], v[12:13], v[14:15]
	s_nop 0
	v_add_f32_e32 v12, 0, v12
	v_add_f32_e32 v12, v12, v13
	s_waitcnt lgkmcnt(0)
; __device__ __forceinline__ float shx(float v, int m, int lane) { return __builtin_bit_cast(float, __builtin_amdgcn_ds_bpermute((lane ^ m) << 2, __builtin_bit_cast(int, v))); }
; __device__ __forceinline__ float wave_sum(float v, int lane) {
; #pragma unroll
;     for (int o = 1; o < 64; o <<= 1) v += shx(v, o, lane);
;     return v;
; __device__ __forceinline__ void phase_combine(CArgs a, LAS unsigned char* lds, int L, int wv, int xw  ) {
;     ...
;             const float mean = wave_sum(s, lane) * (1.f / DM); float s2 = 0.f;
; #pragma unroll
;             for (int j = 0; j < 2; ++j) { v[h][j][0] = v[h][j][0] - mean; v[h][j][1] = v[h][j][1] - mean;
;                 s2 += ((v[h][j][0].x * v[h][j][0].x + v[h][j][0].y * v[h][j][0].y) + (v[h][j][0].z * v[h][j][0].z + v[h][j][0].w * v[h][j][0].w)) + ((v[h][j][1].x * v[h][j][1].x + v[h][j][1].y * v[h][j][1].y) + (v[h][j][1].z * v[h][j][1].z + v[h][j][1].w * v[h][j][1].w)); }
;             const float rstd = 1.0f / sqrtf(wave_sum(s2, lane) * (1.f / DM) + LN_EPS);
;             float am = 0.f;
; #pragma unroll
;             for (int j = 0; j < 2; ++j) { const int c0 = lane * 8 + 512 * j;
;                 v[h][j][0] = v[h][j][0] * rstd * *(const f32x4*)(lng + c0) + *(const f32x4*)(lnb + c0); v[h][j][1] = v[h][j][1] * rstd * *(const f32x4*)(lng + c0 + 4) + *(const f32x4*)(lnb + c0 + 4);
	s_nop 1
	v_add_f32_dpp v12, v12, v12 quad_perm:[1,0,3,2] row_mask:0xf bank_mask:0xf
	s_nop 1
	v_add_f32_dpp v12, v12, v12 quad_perm:[2,3,0,1] row_mask:0xf bank_mask:0xf
	s_nop 1
	v_add_f32_dpp v12, v12, v12 row_half_mirror row_mask:0xf bank_mask:0xf
	s_nop 1
	v_add_f32_dpp v12, v12, v12 row_mirror row_mask:0xf bank_mask:0xf
	v_mov_b32_e32 v13, v12
	s_nop 1
	v_permlane16_swap_b32_e32 v13, v12
	v_add_f32_e32 v12, v12, v13
	v_mov_b32_e32 v13, v12
	s_nop 1
	v_permlane32_swap_b32_e32 v13, v12
	v_add_f32_e32 v12, v12, v13
	v_fmamk_f32 v11, v12, 0xba800000, v11
	v_fmamk_f32 v47, v12, 0xba800000, v47
	v_fmamk_f32 v9, v12, 0xba800000, v9
	v_fmac_f32_e32 v10, 0xba800000, v12
	v_fmamk_f32 v45, v12, 0xba800000, v45
	v_fmac_f32_e32 v46, 0xba800000, v12
	v_mov_b32_e32 v14, v11
	v_mov_b32_e32 v15, v47
	v_fmac_f32_e32 v8, 0xba800000, v12
	v_fmamk_f32 v5, v12, 0xba800000, v5
	v_fmac_f32_e32 v4, 0xba800000, v12
	v_fmamk_f32 v7, v12, 0xba800000, v7
	v_fmac_f32_e32 v6, 0xba800000, v12
	v_fmac_f32_e32 v44, 0xba800000, v12
	v_fmamk_f32 v1, v12, 0xba800000, v1
	v_fmac_f32_e32 v0, 0xba800000, v12
	v_fmamk_f32 v3, v12, 0xba800000, v3
	v_fmac_f32_e32 v2, 0xba800000, v12
	v_mov_b32_e32 v12, v10
	v_mov_b32_e32 v13, v46
	v_pk_mul_f32 v[14:15], v[14:15], v[14:15]
	v_mov_b32_e32 v16, v9
	v_mov_b32_e32 v17, v45
	v_pk_fma_f32 v[12:13], v[12:13], v[12:13], v[14:15]
	v_mov_b32_e32 v14, v8
	v_mov_b32_e32 v15, v44
	v_pk_mul_f32 v[16:17], v[16:17], v[16:17]
	v_mov_b32_e32 v32, v4
	v_pk_fma_f32 v[14:15], v[14:15], v[14:15], v[16:17]
	v_mov_b32_e32 v33, v0
	v_pk_add_f32 v[28:29], v[12:13], v[14:15]
	v_mov_b32_e32 v14, v7
	v_mov_b32_e32 v15, v3
	v_mov_b32_e32 v12, v6
	v_mov_b32_e32 v13, v2
	v_pk_mul_f32 v[14:15], v[14:15], v[14:15]
	s_nop 0
	v_pk_fma_f32 v[30:31], v[12:13], v[12:13], v[14:15]
	v_mov_b32_e32 v12, v5
	v_mov_b32_e32 v13, v1
	v_pk_mul_f32 v[34:35], v[12:13], v[12:13]
	global_load_dwordx4 v[12:15], v[108:109], off offset:16
	global_load_dwordx4 v[16:19], v[108:109], off
	global_load_dwordx4 v[20:23], v[110:111], off offset:16
	global_load_dwordx4 v[24:27], v[110:111], off
	v_pk_fma_f32 v[32:33], v[32:33], v[32:33], v[34:35]
	s_nop 0
	v_pk_add_f32 v[30:31], v[30:31], v[32:33]
	s_nop 0
	v_pk_add_f32 v[28:29], v[28:29], v[30:31]
	s_nop 0
	v_add_f32_e32 v40, v28, v29
	ds_bpermute_b32 v41, v192, v40
	global_load_dwordx4 v[28:31], v[110:111], off offset:2048
	global_load_dwordx4 v[32:35], v[108:109], off offset:2048
	global_load_dwordx4 v[36:39], v[108:109], off offset:2064
	s_waitcnt lgkmcnt(0)
	v_add_f32_e32 v48, v40, v41
	global_load_dwordx4 v[40:43], v[110:111], off offset:2064
	s_waitcnt lgkmcnt(0)
	s_nop 1
	v_add_f32_dpp v48, v48, v48 quad_perm:[2,3,0,1] row_mask:0xf bank_mask:0xf
	s_nop 1
	v_add_f32_dpp v48, v48, v48 row_half_mirror row_mask:0xf bank_mask:0xf
	s_nop 1
	v_add_f32_dpp v48, v48, v48 row_mirror row_mask:0xf bank_mask:0xf
	v_mov_b32_e32 v49, v48
	s_nop 1
	v_permlane16_swap_b32_e32 v49, v48
	v_add_f32_e32 v48, v48, v49
	v_mov_b32_e32 v49, v48
	s_nop 1
	v_permlane32_swap_b32_e32 v49, v48
	v_add_f32_e32 v48, v48, v49
	v_fmamk_f32 v48, v48, 0x3a800000, v185
	v_mul_f32_e32 v49, 0x4f800000, v48
	v_cmp_gt_f32_e32 vcc, s55, v48
	s_nop 1
	v_cndmask_b32_e32 v48, v48, v49, vcc
	v_sqrt_f32_e32 v49, v48
	s_nop 0
	v_add_u32_e32 v50, -1, v49
	v_fma_f32 v51, -v50, v49, v48
	v_cmp_ge_f32_e64 s[14:15], 0, v51
	v_add_u32_e32 v51, 1, v49
	s_nop 0
	v_cndmask_b32_e64 v50, v49, v50, s[14:15]
	v_fma_f32 v49, -v51, v49, v48
	v_cmp_lt_f32_e64 s[14:15], 0, v49
	s_nop 1
	v_cndmask_b32_e64 v49, v50, v51, s[14:15]
	v_mul_f32_e32 v50, 0x37800000, v49
	v_cndmask_b32_e32 v49, v49, v50, vcc
	v_cmp_class_f32_e32 vcc, v48, v183
	s_nop 1
	v_cndmask_b32_e32 v48, v49, v48, vcc
	v_div_scale_f32 v49, s[14:15], v48, v48, 1.0
	v_rcp_f32_e32 v50, v49
	s_nop 0
	v_fma_f32 v51, -v49, v50, 1.0
	v_fmac_f32_e32 v50, v51, v50
	v_div_scale_f32 v51, vcc, 1.0, v48, 1.0
	v_mul_f32_e32 v52, v51, v50
	v_fma_f32 v53, -v49, v52, v51
	v_fmac_f32_e32 v52, v53, v50
	v_fma_f32 v49, -v49, v52, v51
	v_div_fmas_f32 v49, v49, v50, v52
	v_div_fixup_f32 v48, v49, v48, 1.0
	v_pk_mul_f32 v[6:7], v[6:7], v[48:49] op_sel_hi:[1,0]
	v_pk_mul_f32 v[4:5], v[4:5], v[48:49] op_sel_hi:[1,0]
	v_pk_mul_f32 v[10:11], v[10:11], v[48:49] op_sel_hi:[1,0]
	v_pk_mul_f32 v[8:9], v[8:9], v[48:49] op_sel_hi:[1,0]
	s_waitcnt vmcnt(5)
	v_pk_fma_f32 v[22:23], v[14:15], v[4:5], v[22:23]
	v_pk_fma_f32 v[20:21], v[12:13], v[6:7], v[20:21]
	v_pk_mul_f32 v[4:5], v[46:47], v[48:49] op_sel_hi:[1,0]
	v_pk_mul_f32 v[6:7], v[44:45], v[48:49] op_sel_hi:[1,0]
	v_pk_mul_f32 v[2:3], v[2:3], v[48:49] op_sel_hi:[1,0]
	v_pk_mul_f32 v[0:1], v[0:1], v[48:49] op_sel_hi:[1,0]
	s_waitcnt vmcnt(4)
	v_pk_fma_f32 v[18:19], v[18:19], v[8:9], v[26:27]
	v_pk_fma_f32 v[16:17], v[16:17], v[10:11], v[24:25]
	s_waitcnt vmcnt(2)
	v_pk_fma_f32 v[26:27], v[34:35], v[6:7], v[30:31]
	v_pk_fma_f32 v[24:25], v[32:33], v[4:5], v[28:29]
	s_waitcnt vmcnt(0)
	v_pk_fma_f32 v[30:31], v[38:39], v[0:1], v[42:43]
	v_pk_fma_f32 v[28:29], v[36:37], v[2:3], v[40:41]
	s_and_b64 vcc, exec, s[12:13]
	s_mov_b64 s[12:13], -1
	s_cbranch_vccnz .LBB0_957
